# v8 + six-piece load segments of all ten GEMM K-loops: the eight LDS fragment reads interleaved between the LDS-DMA pieces (no m0 write directly behind a DMA, reads fill the m0->DMA wait-state slots)
# baseline (speedup 1.0000x reference)
; #define PG8_LDA(dst, b, h) do { _Pragma("unroll") for (int m = 0; m < 4; ++m) _Pragma("unroll") for (int k = 0; k < 2; ++k) dst[m][k] = *(const PG8_LAS bf16x8*)(lds + PG8_SA(b, h) + aoff + m * 2048 + k * 1024); } while (0)
; #define PG8_LDB(dst, b, h) do { _Pragma("unroll") for (int n = 0; n < 2; ++n) _Pragma("unroll") for (int k = 0; k < 2; ++k) dst[n][k] = *(const PG8_LAS bf16x8*)(lds + PG8_SB(b, h) + boff + n * 2048 + k * 1024); } while (0)
; #define PG8_WAIT_V(n) asm volatile("s_waitcnt vmcnt(" #n ")" ::: "memory")
; #define PG8_WAIT_L(n) asm volatile("s_waitcnt lgkmcnt(" #n ")" ::: "memory")
; #define PG8_BAR __builtin_amdgcn_s_barrier()
; #define PG8_SCHED __builtin_amdgcn_sched_barrier(0)
; template <class Epi, class Sched, bool ALIGN_EPI = false, bool SP2 = false, bool F8 = false, bool I8 = false, bool PF = false>
; __device__ __forceinline__ void gemm_phase(PG8_LAS unsigned char* lds, const Gemm g, const Sched& S, const Epi& E, const int wave_) {
;     ...
;             PG8_LDB(B0, 0, 0); PG8_LDB(B1, 0, 1); PG8_SCHED; PG8_LDA(At, 0, 0); PG8_STAGE(PG8_SA(1, 1), a1 + hstep, voffA);
;             PG8_WAIT_V(8); PG8_WAIT_L(0); PG8_BAR; PG8_MMA(0, 0, At, B0); PG8_MMA(0, 1, At, B1); PG8_BAR; PG8_SCHED;
;             PG8_LDA(At, 0, 1); PG8_STAGE(PG8_SB(0, 0), b2, voffB); PG8_STAGE(PG8_SB(0, 1), b2 + hstep, voffB); PG8_STAGE(PG8_SA(0, 0), a2, voffA);
;             PG8_WAIT_V(8); PG8_WAIT_L(0); PG8_BAR; PG8_MMA(1, 0, At, B0); PG8_MMA(1, 1, At, B1); PG8_BAR; PG8_SCHED;
.LBB0_242:
	ds_read_b128 v[128:131], v180
	ds_read_b128 v[132:135], v180 offset:1024
	ds_read_b128 v[150:153], v180 offset:2048
	ds_read_b128 v[154:157], v180 offset:3072
	ds_read_b128 v[158:161], v181
	ds_read_b128 v[162:165], v181 offset:1024
	ds_read_b128 v[166:169], v181 offset:2048
	ds_read_b128 v[170:173], v181 offset:3072
	s_add_u32 s50, s48, 0xfffe0080
	s_addc_u32 s51, s49, -1
	s_cmp_eq_u32 s79, 4
	s_cselect_b32 s53, s1, s51
	s_cselect_b32 s52, s5, s50
	s_cselect_b32 s51, s39, s78
	s_cselect_b32 s50, s41, s75
	v_lshl_add_u64 v[212:213], s[48:49], 0, v[144:145]
	s_add_i32 m0, s35, 0xc000
	ds_read_b128 v[174:177], v182
	ds_read_b128 v[184:187], v182 offset:1024
	ds_read_b128 v[188:191], v182 offset:2048
	ds_read_b128 v[192:195], v182 offset:3072
	ds_read_b128 v[196:199], v182 offset:4096
	ds_read_b128 v[200:203], v182 offset:5120
	ds_read_b128 v[204:207], v182 offset:6144
	ds_read_b128 v[208:211], v182 offset:7168
	global_load_lds_dwordx4 v[212:213], off
	v_lshl_add_u64 v[212:213], s[48:49], 0, v[146:147]
	s_add_i32 m0, s35, 0xe000
	s_nop 0
	global_load_lds_dwordx4 v[212:213], off
	s_waitcnt vmcnt(8)
	s_waitcnt lgkmcnt(0)
	s_barrier
	s_waitcnt lgkmcnt(0)
	v_mfma_i32_16x16x64_i8 v[124:127], v[128:131], v[174:177], v[124:127]
	v_mfma_i32_16x16x64_i8 v[120:123], v[150:153], v[174:177], v[120:123]
	v_mfma_i32_16x16x64_i8 v[108:111], v[128:131], v[188:191], v[108:111]
	v_mfma_i32_16x16x64_i8 v[104:107], v[150:153], v[188:191], v[104:107]
	v_mfma_i32_16x16x64_i8 v[92:95], v[128:131], v[196:199], v[92:95]
	v_mfma_i32_16x16x64_i8 v[88:91], v[150:153], v[196:199], v[88:91]
	v_mfma_i32_16x16x64_i8 v[76:79], v[128:131], v[204:207], v[76:79]
	v_mfma_i32_16x16x64_i8 v[72:75], v[150:153], v[204:207], v[72:75]
	v_mfma_i32_16x16x64_i8 v[124:127], v[132:135], v[184:187], v[124:127]
	v_mfma_i32_16x16x64_i8 v[120:123], v[154:157], v[184:187], v[120:123]
	v_mfma_i32_16x16x64_i8 v[108:111], v[132:135], v[192:195], v[108:111]
	v_mfma_i32_16x16x64_i8 v[104:107], v[154:157], v[192:195], v[104:107]
	v_mfma_i32_16x16x64_i8 v[92:95], v[132:135], v[200:203], v[92:95]
	v_mfma_i32_16x16x64_i8 v[88:91], v[154:157], v[200:203], v[88:91]
	v_mfma_i32_16x16x64_i8 v[76:79], v[132:135], v[208:211], v[76:79]
	v_mfma_i32_16x16x64_i8 v[72:75], v[154:157], v[208:211], v[72:75]
	v_mfma_i32_16x16x64_i8 v[116:119], v[158:161], v[174:177], v[116:119]
	v_mfma_i32_16x16x64_i8 v[112:115], v[166:169], v[174:177], v[112:115]
	v_mfma_i32_16x16x64_i8 v[100:103], v[158:161], v[188:191], v[100:103]
	v_mfma_i32_16x16x64_i8 v[96:99], v[166:169], v[188:191], v[96:99]
	v_mfma_i32_16x16x64_i8 v[84:87], v[158:161], v[196:199], v[84:87]
	v_mfma_i32_16x16x64_i8 v[80:83], v[166:169], v[196:199], v[80:83]
	v_mfma_i32_16x16x64_i8 v[68:71], v[158:161], v[204:207], v[68:71]
	v_mfma_i32_16x16x64_i8 v[64:67], v[166:169], v[204:207], v[64:67]
	v_mfma_i32_16x16x64_i8 v[116:119], v[162:165], v[184:187], v[116:119]
	v_mfma_i32_16x16x64_i8 v[112:115], v[170:173], v[184:187], v[112:115]
	v_mfma_i32_16x16x64_i8 v[100:103], v[162:165], v[192:195], v[100:103]
	v_mfma_i32_16x16x64_i8 v[96:99], v[170:173], v[192:195], v[96:99]
	v_mfma_i32_16x16x64_i8 v[84:87], v[162:165], v[200:203], v[84:87]
	v_mfma_i32_16x16x64_i8 v[80:83], v[170:173], v[200:203], v[80:83]
	v_mfma_i32_16x16x64_i8 v[68:71], v[162:165], v[208:211], v[68:71]
	v_mfma_i32_16x16x64_i8 v[64:67], v[170:173], v[208:211], v[64:67]
	s_barrier
	s_add_i32 s86, s66, s27
	v_lshl_add_u64 v[212:213], s[50:51], 0, v[138:139]
	s_mov_b32 m0, s86
	ds_read_b128 v[174:177], v182 offset:16384
	global_load_lds_dwordx4 v[212:213], off
	ds_read_b128 v[184:187], v182 offset:17408
	s_add_i32 m0, s86, 0x2000
	s_add_u32 s86, s50, 0x20000
	v_lshl_add_u64 v[214:215], s[50:51], 0, v[142:143]
	s_addc_u32 s87, s51, 0
	s_add_i32 vcc_lo, s67, s27
	global_load_lds_dwordx4 v[214:215], off
	ds_read_b128 v[188:191], v182 offset:18432
	v_lshl_add_u64 v[216:217], s[86:87], 0, v[138:139]
	s_mov_b32 m0, vcc_lo
	v_lshl_add_u64 v[218:219], s[52:53], 0, v[140:141]
	global_load_lds_dwordx4 v[216:217], off
	ds_read_b128 v[192:195], v182 offset:19456
	v_lshl_add_u64 v[216:217], s[86:87], 0, v[142:143]
	s_add_i32 m0, vcc_lo, 0x2000
	ds_read_b128 v[196:199], v182 offset:20480
	global_load_lds_dwordx4 v[216:217], off
	ds_read_b128 v[200:203], v182 offset:21504
	v_lshl_add_u64 v[216:217], s[52:53], 0, v[136:137]
	s_mov_b32 m0, s35
	ds_read_b128 v[204:207], v182 offset:22528
	global_load_lds_dwordx4 v[216:217], off
	ds_read_b128 v[208:211], v182 offset:23552
	s_mov_b32 m0, s37
	s_nop 0
	global_load_lds_dwordx4 v[218:219], off
	s_waitcnt vmcnt(8)
	s_waitcnt lgkmcnt(0)
	s_barrier
; #define PG8_LDA(dst, b, h) do { _Pragma("unroll") for (int m = 0; m < 4; ++m) _Pragma("unroll") for (int k = 0; k < 2; ++k) dst[m][k] = *(const PG8_LAS bf16x8*)(lds + PG8_SA(b, h) + aoff + m * 2048 + k * 1024); } while (0)
; #define PG8_LDB(dst, b, h) do { _Pragma("unroll") for (int n = 0; n < 2; ++n) _Pragma("unroll") for (int k = 0; k < 2; ++k) dst[n][k] = *(const PG8_LAS bf16x8*)(lds + PG8_SB(b, h) + boff + n * 2048 + k * 1024); } while (0)
; #define PG8_WAIT_V(n) asm volatile("s_waitcnt vmcnt(" #n ")" ::: "memory")
; #define PG8_WAIT_L(n) asm volatile("s_waitcnt lgkmcnt(" #n ")" ::: "memory")
; #define PG8_BAR __builtin_amdgcn_s_barrier()
; #define PG8_SCHED __builtin_amdgcn_sched_barrier(0)
; template <class Epi, class Sched, bool ALIGN_EPI = false, bool SP2 = false, bool F8 = false, bool I8 = false, bool PF = false>
; __device__ __forceinline__ void gemm_phase(PG8_LAS unsigned char* lds, const Gemm g, const Sched& S, const Epi& E, const int wave_) {
;     ...
;             PG8_WAIT_V(8); PG8_WAIT_L(0); PG8_BAR; PG8_MMA(1, 0, At, B0); PG8_MMA(1, 1, At, B1); PG8_BAR; PG8_SCHED;
;             PG8_LDB(B0, 1, 0); PG8_LDB(B1, 1, 1); PG8_SCHED; PG8_LDA(At, 1, 0); PG8_STAGE(PG8_SA(0, 1), a2 + hstep, voffA);
;             PG8_WAIT_V(8); PG8_WAIT_L(0); PG8_BAR; PG8_MMA(0, 0, At, B0); PG8_MMA(0, 1, At, B1); PG8_BAR; PG8_SCHED;
;             PG8_LDA(At, 1, 1); PG8_STAGE(PG8_SB(1, 0), b3, voffB); PG8_STAGE(PG8_SB(1, 1), b3 + hstep, voffB); PG8_STAGE(PG8_SA(1, 0), a3, voffA);
	s_waitcnt lgkmcnt(0)
	v_mfma_i32_16x16x64_i8 v[60:63], v[128:131], v[174:177], v[60:63]
	v_mfma_i32_16x16x64_i8 v[56:59], v[150:153], v[174:177], v[56:59]
	v_mfma_i32_16x16x64_i8 v[44:47], v[128:131], v[188:191], v[44:47]
	v_mfma_i32_16x16x64_i8 v[40:43], v[150:153], v[188:191], v[40:43]
	v_mfma_i32_16x16x64_i8 v[28:31], v[128:131], v[196:199], v[28:31]
	v_mfma_i32_16x16x64_i8 v[24:27], v[150:153], v[196:199], v[24:27]
	v_mfma_i32_16x16x64_i8 v[12:15], v[128:131], v[204:207], v[12:15]
	v_mfma_i32_16x16x64_i8 v[8:11], v[150:153], v[204:207], v[8:11]
	v_mfma_i32_16x16x64_i8 v[60:63], v[132:135], v[184:187], v[60:63]
	v_mfma_i32_16x16x64_i8 v[56:59], v[154:157], v[184:187], v[56:59]
	v_mfma_i32_16x16x64_i8 v[44:47], v[132:135], v[192:195], v[44:47]
	v_mfma_i32_16x16x64_i8 v[40:43], v[154:157], v[192:195], v[40:43]
	v_mfma_i32_16x16x64_i8 v[28:31], v[132:135], v[200:203], v[28:31]
	v_mfma_i32_16x16x64_i8 v[24:27], v[154:157], v[200:203], v[24:27]
	v_mfma_i32_16x16x64_i8 v[12:15], v[132:135], v[208:211], v[12:15]
	v_mfma_i32_16x16x64_i8 v[8:11], v[154:157], v[208:211], v[8:11]
	v_mfma_i32_16x16x64_i8 v[52:55], v[158:161], v[174:177], v[52:55]
	v_mfma_i32_16x16x64_i8 v[48:51], v[166:169], v[174:177], v[48:51]
	v_mfma_i32_16x16x64_i8 v[36:39], v[158:161], v[188:191], v[36:39]
	v_mfma_i32_16x16x64_i8 v[32:35], v[166:169], v[188:191], v[32:35]
	v_mfma_i32_16x16x64_i8 v[20:23], v[158:161], v[196:199], v[20:23]
	v_mfma_i32_16x16x64_i8 v[16:19], v[166:169], v[196:199], v[16:19]
	v_mfma_i32_16x16x64_i8 v[4:7], v[158:161], v[204:207], v[4:7]
	v_mfma_i32_16x16x64_i8 v[0:3], v[166:169], v[204:207], v[0:3]
	v_mfma_i32_16x16x64_i8 v[52:55], v[162:165], v[184:187], v[52:55]
	v_mfma_i32_16x16x64_i8 v[48:51], v[170:173], v[184:187], v[48:51]
	v_mfma_i32_16x16x64_i8 v[36:39], v[162:165], v[192:195], v[36:39]
	v_mfma_i32_16x16x64_i8 v[32:35], v[170:173], v[192:195], v[32:35]
	v_mfma_i32_16x16x64_i8 v[20:23], v[162:165], v[200:203], v[20:23]
	v_mfma_i32_16x16x64_i8 v[16:19], v[170:173], v[200:203], v[16:19]
	v_mfma_i32_16x16x64_i8 v[4:7], v[162:165], v[208:211], v[4:7]
	v_mfma_i32_16x16x64_i8 v[0:3], v[170:173], v[208:211], v[0:3]
	s_barrier
	s_add_i32 s86, 0, 0x18000
	s_add_i32 s87, 0, 0x1c000
	v_add_u32_e32 v154, s86, v179
	v_add_u32_e32 v170, s87, v179
	ds_read_b128 v[128:131], v154
	ds_read_b128 v[132:135], v154 offset:1024
	ds_read_b128 v[150:153], v154 offset:2048
	ds_read_b128 v[154:157], v154 offset:3072
	ds_read_b128 v[158:161], v170
	ds_read_b128 v[162:165], v170 offset:1024
	ds_read_b128 v[166:169], v170 offset:2048
	ds_read_b128 v[170:173], v170 offset:3072
	s_add_u32 s52, s52, 0x20000
	s_addc_u32 s53, s53, 0
	s_mov_b32 m0, s54
	v_lshl_add_u64 v[220:221], s[52:53], 0, v[136:137]
	ds_read_b128 v[174:177], v182 offset:32768
	ds_read_b128 v[184:187], v182 offset:33792
	ds_read_b128 v[188:191], v182 offset:34816
	ds_read_b128 v[192:195], v182 offset:35840
	ds_read_b128 v[196:199], v182 offset:36864
	ds_read_b128 v[200:203], v182 offset:37888
	ds_read_b128 v[204:207], v182 offset:38912
	ds_read_b128 v[208:211], v182 offset:39936
	global_load_lds_dwordx4 v[220:221], off
	v_lshl_add_u64 v[220:221], s[52:53], 0, v[140:141]
	s_mov_b32 m0, s55
	s_nop 0
	global_load_lds_dwordx4 v[220:221], off
	s_waitcnt vmcnt(8)
	s_waitcnt lgkmcnt(0)
	s_barrier
	s_waitcnt lgkmcnt(0)
	v_mfma_i32_16x16x64_i8 v[124:127], v[128:131], v[174:177], v[124:127]
	v_mfma_i32_16x16x64_i8 v[120:123], v[150:153], v[174:177], v[120:123]
	v_mfma_i32_16x16x64_i8 v[108:111], v[128:131], v[188:191], v[108:111]
	v_mfma_i32_16x16x64_i8 v[104:107], v[150:153], v[188:191], v[104:107]
	v_mfma_i32_16x16x64_i8 v[92:95], v[128:131], v[196:199], v[92:95]
	v_mfma_i32_16x16x64_i8 v[88:91], v[150:153], v[196:199], v[88:91]
	v_mfma_i32_16x16x64_i8 v[76:79], v[128:131], v[204:207], v[76:79]
	v_mfma_i32_16x16x64_i8 v[72:75], v[150:153], v[204:207], v[72:75]
	v_mfma_i32_16x16x64_i8 v[124:127], v[132:135], v[184:187], v[124:127]
	v_mfma_i32_16x16x64_i8 v[120:123], v[154:157], v[184:187], v[120:123]
	v_mfma_i32_16x16x64_i8 v[108:111], v[132:135], v[192:195], v[108:111]
	v_mfma_i32_16x16x64_i8 v[104:107], v[154:157], v[192:195], v[104:107]
	v_mfma_i32_16x16x64_i8 v[92:95], v[132:135], v[200:203], v[92:95]
	v_mfma_i32_16x16x64_i8 v[88:91], v[154:157], v[200:203], v[88:91]
	v_mfma_i32_16x16x64_i8 v[76:79], v[132:135], v[208:211], v[76:79]
	v_mfma_i32_16x16x64_i8 v[72:75], v[154:157], v[208:211], v[72:75]
	v_mfma_i32_16x16x64_i8 v[116:119], v[158:161], v[174:177], v[116:119]
	v_mfma_i32_16x16x64_i8 v[112:115], v[166:169], v[174:177], v[112:115]
	v_mfma_i32_16x16x64_i8 v[100:103], v[158:161], v[188:191], v[100:103]
	v_mfma_i32_16x16x64_i8 v[96:99], v[166:169], v[188:191], v[96:99]
	v_mfma_i32_16x16x64_i8 v[84:87], v[158:161], v[196:199], v[84:87]
	v_mfma_i32_16x16x64_i8 v[80:83], v[166:169], v[196:199], v[80:83]
	v_mfma_i32_16x16x64_i8 v[68:71], v[158:161], v[204:207], v[68:71]
	v_mfma_i32_16x16x64_i8 v[64:67], v[166:169], v[204:207], v[64:67]
	v_mfma_i32_16x16x64_i8 v[116:119], v[162:165], v[184:187], v[116:119]
	v_mfma_i32_16x16x64_i8 v[112:115], v[170:173], v[184:187], v[112:115]
	v_mfma_i32_16x16x64_i8 v[100:103], v[162:165], v[192:195], v[100:103]
	v_mfma_i32_16x16x64_i8 v[96:99], v[170:173], v[192:195], v[96:99]
	v_mfma_i32_16x16x64_i8 v[84:87], v[162:165], v[200:203], v[84:87]
	v_mfma_i32_16x16x64_i8 v[80:83], v[170:173], v[200:203], v[80:83]
	v_mfma_i32_16x16x64_i8 v[68:71], v[162:165], v[208:211], v[68:71]
	v_mfma_i32_16x16x64_i8 v[64:67], v[170:173], v[208:211], v[64:67]
	s_barrier
; #define PG8_LDA(dst, b, h) do { _Pragma("unroll") for (int m = 0; m < 4; ++m) _Pragma("unroll") for (int k = 0; k < 2; ++k) dst[m][k] = *(const PG8_LAS bf16x8*)(lds + PG8_SA(b, h) + aoff + m * 2048 + k * 1024); } while (0)
; #define PG8_WAIT_V(n) asm volatile("s_waitcnt vmcnt(" #n ")" ::: "memory")
; #define PG8_WAIT_L(n) asm volatile("s_waitcnt lgkmcnt(" #n ")" ::: "memory")
; #define PG8_BAR __builtin_amdgcn_s_barrier()
; #define PG8_SCHED __builtin_amdgcn_sched_barrier(0)
; template <class Epi, class Sched, bool ALIGN_EPI = false, bool SP2 = false, bool F8 = false, bool I8 = false, bool PF = false>
; __device__ __forceinline__ void gemm_phase(PG8_LAS unsigned char* lds, const Gemm g, const Sched& S, const Epi& E, const int wave_) {
;     ...
;             PG8_LDA(At, 1, 1); PG8_STAGE(PG8_SB(1, 0), b3, voffB); PG8_STAGE(PG8_SB(1, 1), b3 + hstep, voffB); PG8_STAGE(PG8_SA(1, 0), a3, voffA);
;             PG8_WAIT_V(8); PG8_WAIT_L(0); PG8_BAR; PG8_MMA(1, 0, At, B0); PG8_MMA(1, 1, At, B1); PG8_BAR; PG8_SCHED;
	s_add_i32 s52, s86, s27
	v_lshl_add_u64 v[212:213], v[212:213], 0, s[14:15]
	s_mov_b32 m0, s52
	ds_read_b128 v[174:177], v182 offset:49152
	global_load_lds_dwordx4 v[212:213], off
	ds_read_b128 v[184:187], v182 offset:50176
	s_add_i32 m0, s52, 0x2000
	s_add_u32 s50, s50, 0x20080
	v_lshl_add_u64 v[212:213], v[214:215], 0, s[14:15]
	s_addc_u32 s51, s51, 0
	s_add_i32 s52, s87, s27
	global_load_lds_dwordx4 v[212:213], off
	ds_read_b128 v[188:191], v182 offset:51200
	v_lshl_add_u64 v[212:213], s[50:51], 0, v[138:139]
	s_mov_b32 m0, s52
	ds_read_b128 v[192:195], v182 offset:52224
	global_load_lds_dwordx4 v[212:213], off
	ds_read_b128 v[196:199], v182 offset:53248
	v_lshl_add_u64 v[212:213], s[50:51], 0, v[142:143]
	s_add_i32 m0, s52, 0x2000
	ds_read_b128 v[200:203], v182 offset:54272
	global_load_lds_dwordx4 v[212:213], off
	ds_read_b128 v[204:207], v182 offset:55296
	v_lshl_add_u64 v[212:213], v[216:217], 0, s[14:15]
	s_mov_b32 m0, s63
	ds_read_b128 v[208:211], v182 offset:56320
	global_load_lds_dwordx4 v[212:213], off
	v_lshl_add_u64 v[212:213], v[218:219], 0, s[14:15]
	s_mov_b32 m0, s64
	s_nop 0
	global_load_lds_dwordx4 v[212:213], off
	s_waitcnt vmcnt(8)
	s_waitcnt lgkmcnt(0)
	s_barrier
	s_waitcnt lgkmcnt(0)
	v_mfma_i32_16x16x64_i8 v[60:63], v[128:131], v[174:177], v[60:63]
	v_mfma_i32_16x16x64_i8 v[56:59], v[150:153], v[174:177], v[56:59]
	v_mfma_i32_16x16x64_i8 v[44:47], v[128:131], v[188:191], v[44:47]
	v_mfma_i32_16x16x64_i8 v[40:43], v[150:153], v[188:191], v[40:43]
	v_mfma_i32_16x16x64_i8 v[28:31], v[128:131], v[196:199], v[28:31]
	v_mfma_i32_16x16x64_i8 v[24:27], v[150:153], v[196:199], v[24:27]
	v_mfma_i32_16x16x64_i8 v[12:15], v[128:131], v[204:207], v[12:15]
	v_mfma_i32_16x16x64_i8 v[8:11], v[150:153], v[204:207], v[8:11]
	v_mfma_i32_16x16x64_i8 v[60:63], v[132:135], v[184:187], v[60:63]
	v_mfma_i32_16x16x64_i8 v[56:59], v[154:157], v[184:187], v[56:59]
	v_mfma_i32_16x16x64_i8 v[44:47], v[132:135], v[192:195], v[44:47]
	v_mfma_i32_16x16x64_i8 v[40:43], v[154:157], v[192:195], v[40:43]
	v_mfma_i32_16x16x64_i8 v[28:31], v[132:135], v[200:203], v[28:31]
	v_mfma_i32_16x16x64_i8 v[24:27], v[154:157], v[200:203], v[24:27]
	v_mfma_i32_16x16x64_i8 v[12:15], v[132:135], v[208:211], v[12:15]
	v_mfma_i32_16x16x64_i8 v[8:11], v[154:157], v[208:211], v[8:11]
	v_mfma_i32_16x16x64_i8 v[52:55], v[158:161], v[174:177], v[52:55]
	v_mfma_i32_16x16x64_i8 v[48:51], v[166:169], v[174:177], v[48:51]
	v_mfma_i32_16x16x64_i8 v[36:39], v[158:161], v[188:191], v[36:39]
	v_mfma_i32_16x16x64_i8 v[32:35], v[166:169], v[188:191], v[32:35]
	v_mfma_i32_16x16x64_i8 v[20:23], v[158:161], v[196:199], v[20:23]
	v_mfma_i32_16x16x64_i8 v[16:19], v[166:169], v[196:199], v[16:19]
	v_mfma_i32_16x16x64_i8 v[4:7], v[158:161], v[204:207], v[4:7]
	v_mfma_i32_16x16x64_i8 v[0:3], v[166:169], v[204:207], v[0:3]
	v_mfma_i32_16x16x64_i8 v[52:55], v[162:165], v[184:187], v[52:55]
	v_mfma_i32_16x16x64_i8 v[48:51], v[170:173], v[184:187], v[48:51]
	v_mfma_i32_16x16x64_i8 v[36:39], v[162:165], v[192:195], v[36:39]
	v_mfma_i32_16x16x64_i8 v[32:35], v[170:173], v[192:195], v[32:35]
	v_mfma_i32_16x16x64_i8 v[20:23], v[162:165], v[200:203], v[20:23]
	v_mfma_i32_16x16x64_i8 v[16:19], v[170:173], v[200:203], v[16:19]
	v_mfma_i32_16x16x64_i8 v[4:7], v[162:165], v[208:211], v[4:7]
	v_mfma_i32_16x16x64_i8 v[0:3], v[170:173], v[208:211], v[0:3]
	s_barrier
	s_add_i32 s79, s79, 2
	s_add_u32 s48, s48, 0x100
	s_addc_u32 s49, s49, 0
	s_add_u32 s75, s75, 0x100
	s_addc_u32 s78, s78, 0
	s_cmp_gt_u32 s79, 5
	s_cbranch_scc0 .LBB0_242
	s_and_b64 vcc, exec, s[16:17]
	s_cbranch_vccz .LBB0_245
	s_barrier

; #define PG8_LDA(dst, b, h) do { _Pragma("unroll") for (int m = 0; m < 4; ++m) _Pragma("unroll") for (int k = 0; k < 2; ++k) dst[m][k] = *(const PG8_LAS bf16x8*)(lds + PG8_SA(b, h) + aoff + m * 2048 + k * 1024); } while (0)
; #define PG8_LDB(dst, b, h) do { _Pragma("unroll") for (int n = 0; n < 2; ++n) _Pragma("unroll") for (int k = 0; k < 2; ++k) dst[n][k] = *(const PG8_LAS bf16x8*)(lds + PG8_SB(b, h) + boff + n * 2048 + k * 1024); } while (0)
; #define PG8_WAIT_V(n) asm volatile("s_waitcnt vmcnt(" #n ")" ::: "memory")
; #define PG8_WAIT_L(n) asm volatile("s_waitcnt lgkmcnt(" #n ")" ::: "memory")
; #define PG8_BAR __builtin_amdgcn_s_barrier()
; #define PG8_SCHED __builtin_amdgcn_sched_barrier(0)
; template <class Epi, class Sched, bool ALIGN_EPI = false, bool SP2 = false, bool F8 = false, bool I8 = false, bool PF = false>
; __device__ __forceinline__ void gemm_phase(PG8_LAS unsigned char* lds, const Gemm g, const Sched& S, const Epi& E, const int wave_) {
;     ...
;             PG8_LDB(B0, 0, 0); PG8_LDB(B1, 0, 1); PG8_SCHED; PG8_LDA(At, 0, 0); PG8_STAGE(PG8_SA(1, 1), a1 + hstep, voffA);
;             PG8_WAIT_V(8); PG8_WAIT_L(0); PG8_BAR; PG8_MMA(0, 0, At, B0); PG8_MMA(0, 1, At, B1); PG8_BAR; PG8_SCHED;
;             PG8_LDA(At, 0, 1); PG8_STAGE(PG8_SB(0, 0), b2, voffB); PG8_STAGE(PG8_SB(0, 1), b2 + hstep, voffB); PG8_STAGE(PG8_SA(0, 0), a2, voffA);
;             PG8_WAIT_V(8); PG8_WAIT_L(0); PG8_BAR; PG8_MMA(1, 0, At, B0); PG8_MMA(1, 1, At, B1); PG8_BAR; PG8_SCHED;
.LBB0_453:
	ds_read_b128 v[128:131], v175
	ds_read_b128 v[132:135], v175 offset:1024
	ds_read_b128 v[136:139], v175 offset:2048
	ds_read_b128 v[140:143], v175 offset:3072
	ds_read_b128 v[144:147], v176
	ds_read_b128 v[148:151], v176 offset:1024
	ds_read_b128 v[166:169], v176 offset:2048
	ds_read_b128 v[170:173], v176 offset:3072
	s_add_u32 s28, s22, 0xfffc0080
	s_addc_u32 s29, s23, -1
	s_cmp_eq_u32 s62, 12
	s_cselect_b32 s31, s13, s29
	s_cselect_b32 s30, s52, s28
	s_cselect_b32 s29, s11, s55
	s_cselect_b32 s28, s53, s54
	v_lshl_add_u64 v[210:211], s[22:23], 0, v[160:161]
	s_add_i32 m0, s21, 0xc000
	ds_read_b128 v[178:181], v177
	ds_read_b128 v[182:185], v177 offset:1024
	ds_read_b128 v[186:189], v177 offset:2048
	ds_read_b128 v[190:193], v177 offset:3072
	ds_read_b128 v[194:197], v177 offset:4096
	ds_read_b128 v[198:201], v177 offset:5120
	ds_read_b128 v[202:205], v177 offset:6144
	ds_read_b128 v[206:209], v177 offset:7168
	global_load_lds_dwordx4 v[210:211], off
	v_lshl_add_u64 v[210:211], s[22:23], 0, v[162:163]
	s_add_i32 m0, s21, 0xe000
	s_nop 0
	global_load_lds_dwordx4 v[210:211], off
	s_waitcnt vmcnt(8)
	s_waitcnt lgkmcnt(0)
	s_barrier
	s_waitcnt lgkmcnt(0)
	v_mfma_f32_16x16x32_bf16 v[124:127], v[128:131], v[178:181], v[124:127]
	v_mfma_f32_16x16x32_bf16 v[120:123], v[136:139], v[178:181], v[120:123]
	v_mfma_f32_16x16x32_bf16 v[116:119], v[128:131], v[186:189], v[116:119]
	v_mfma_f32_16x16x32_bf16 v[112:115], v[136:139], v[186:189], v[112:115]
	v_mfma_f32_16x16x32_bf16 v[96:99], v[128:131], v[194:197], v[96:99]
	v_mfma_f32_16x16x32_bf16 v[88:91], v[136:139], v[194:197], v[88:91]
	v_mfma_f32_16x16x32_bf16 v[80:83], v[128:131], v[202:205], v[80:83]
	v_mfma_f32_16x16x32_bf16 v[72:75], v[136:139], v[202:205], v[72:75]
	v_mfma_f32_16x16x32_bf16 v[124:127], v[132:135], v[182:185], v[124:127]
	v_mfma_f32_16x16x32_bf16 v[120:123], v[140:143], v[182:185], v[120:123]
	v_mfma_f32_16x16x32_bf16 v[116:119], v[132:135], v[190:193], v[116:119]
	v_mfma_f32_16x16x32_bf16 v[112:115], v[140:143], v[190:193], v[112:115]
	v_mfma_f32_16x16x32_bf16 v[96:99], v[132:135], v[198:201], v[96:99]
	v_mfma_f32_16x16x32_bf16 v[88:91], v[140:143], v[198:201], v[88:91]
	v_mfma_f32_16x16x32_bf16 v[80:83], v[132:135], v[206:209], v[80:83]
	v_mfma_f32_16x16x32_bf16 v[72:75], v[140:143], v[206:209], v[72:75]
	v_mfma_f32_16x16x32_bf16 v[108:111], v[144:147], v[178:181], v[108:111]
	v_mfma_f32_16x16x32_bf16 v[104:107], v[166:169], v[178:181], v[104:107]
	v_mfma_f32_16x16x32_bf16 v[100:103], v[144:147], v[186:189], v[100:103]
	v_mfma_f32_16x16x32_bf16 v[92:95], v[166:169], v[186:189], v[92:95]
	v_mfma_f32_16x16x32_bf16 v[84:87], v[144:147], v[194:197], v[84:87]
	v_mfma_f32_16x16x32_bf16 v[76:79], v[166:169], v[194:197], v[76:79]
	v_mfma_f32_16x16x32_bf16 v[68:71], v[144:147], v[202:205], v[68:71]
	v_mfma_f32_16x16x32_bf16 v[64:67], v[166:169], v[202:205], v[64:67]
	v_mfma_f32_16x16x32_bf16 v[108:111], v[148:151], v[182:185], v[108:111]
	v_mfma_f32_16x16x32_bf16 v[104:107], v[170:173], v[182:185], v[104:107]
	v_mfma_f32_16x16x32_bf16 v[100:103], v[148:151], v[190:193], v[100:103]
	v_mfma_f32_16x16x32_bf16 v[92:95], v[170:173], v[190:193], v[92:95]
	v_mfma_f32_16x16x32_bf16 v[84:87], v[148:151], v[198:201], v[84:87]
	v_mfma_f32_16x16x32_bf16 v[76:79], v[170:173], v[198:201], v[76:79]
	v_mfma_f32_16x16x32_bf16 v[68:71], v[148:151], v[206:209], v[68:71]
	v_mfma_f32_16x16x32_bf16 v[64:67], v[170:173], v[206:209], v[64:67]
	s_barrier
	s_add_i32 s63, s49, s36
	v_lshl_add_u64 v[210:211], s[28:29], 0, v[156:157]
	s_mov_b32 m0, s63
	ds_read_b128 v[178:181], v177 offset:16384
	global_load_lds_dwordx4 v[210:211], off
	ds_read_b128 v[182:185], v177 offset:17408
	s_add_i32 m0, s63, 0x2000
	s_add_u32 s64, s28, 0x40000
	v_lshl_add_u64 v[212:213], s[28:29], 0, v[152:153]
	s_addc_u32 s65, s29, 0
	s_add_i32 s63, s50, s36
	global_load_lds_dwordx4 v[212:213], off
	ds_read_b128 v[186:189], v177 offset:18432
	v_lshl_add_u64 v[214:215], s[64:65], 0, v[156:157]
	s_mov_b32 m0, s63
	v_lshl_add_u64 v[216:217], s[30:31], 0, v[154:155]
	global_load_lds_dwordx4 v[214:215], off
	ds_read_b128 v[190:193], v177 offset:19456
	v_lshl_add_u64 v[214:215], s[64:65], 0, v[152:153]
	s_add_i32 m0, s63, 0x2000
	ds_read_b128 v[194:197], v177 offset:20480
	global_load_lds_dwordx4 v[214:215], off
	ds_read_b128 v[198:201], v177 offset:21504
	v_lshl_add_u64 v[214:215], s[30:31], 0, v[158:159]
	s_mov_b32 m0, s21
	ds_read_b128 v[202:205], v177 offset:22528
	global_load_lds_dwordx4 v[214:215], off
	ds_read_b128 v[206:209], v177 offset:23552
	s_mov_b32 m0, s37
	s_nop 0
	global_load_lds_dwordx4 v[216:217], off
	s_waitcnt vmcnt(8)
	s_waitcnt lgkmcnt(0)
	s_barrier
; #define PG8_LDA(dst, b, h) do { _Pragma("unroll") for (int m = 0; m < 4; ++m) _Pragma("unroll") for (int k = 0; k < 2; ++k) dst[m][k] = *(const PG8_LAS bf16x8*)(lds + PG8_SA(b, h) + aoff + m * 2048 + k * 1024); } while (0)
; #define PG8_LDB(dst, b, h) do { _Pragma("unroll") for (int n = 0; n < 2; ++n) _Pragma("unroll") for (int k = 0; k < 2; ++k) dst[n][k] = *(const PG8_LAS bf16x8*)(lds + PG8_SB(b, h) + boff + n * 2048 + k * 1024); } while (0)
; #define PG8_WAIT_V(n) asm volatile("s_waitcnt vmcnt(" #n ")" ::: "memory")
; #define PG8_WAIT_L(n) asm volatile("s_waitcnt lgkmcnt(" #n ")" ::: "memory")
; #define PG8_BAR __builtin_amdgcn_s_barrier()
; #define PG8_SCHED __builtin_amdgcn_sched_barrier(0)
; template <class Epi, class Sched, bool ALIGN_EPI = false, bool SP2 = false, bool F8 = false, bool I8 = false, bool PF = false>
; __device__ __forceinline__ void gemm_phase(PG8_LAS unsigned char* lds, const Gemm g, const Sched& S, const Epi& E, const int wave_) {
;     ...
;             PG8_WAIT_V(8); PG8_WAIT_L(0); PG8_BAR; PG8_MMA(1, 0, At, B0); PG8_MMA(1, 1, At, B1); PG8_BAR; PG8_SCHED;
;             PG8_LDB(B0, 1, 0); PG8_LDB(B1, 1, 1); PG8_SCHED; PG8_LDA(At, 1, 0); PG8_STAGE(PG8_SA(0, 1), a2 + hstep, voffA);
;             PG8_WAIT_V(8); PG8_WAIT_L(0); PG8_BAR; PG8_MMA(0, 0, At, B0); PG8_MMA(0, 1, At, B1); PG8_BAR; PG8_SCHED;
;             PG8_LDA(At, 1, 1); PG8_STAGE(PG8_SB(1, 0), b3, voffB); PG8_STAGE(PG8_SB(1, 1), b3 + hstep, voffB); PG8_STAGE(PG8_SA(1, 0), a3, voffA);
	s_waitcnt lgkmcnt(0)
	v_mfma_f32_16x16x32_bf16 v[60:63], v[128:131], v[178:181], v[60:63]
	v_mfma_f32_16x16x32_bf16 v[56:59], v[136:139], v[178:181], v[56:59]
	v_mfma_f32_16x16x32_bf16 v[48:51], v[128:131], v[186:189], v[48:51]
	v_mfma_f32_16x16x32_bf16 v[40:43], v[136:139], v[186:189], v[40:43]
	v_mfma_f32_16x16x32_bf16 v[32:35], v[128:131], v[194:197], v[32:35]
	v_mfma_f32_16x16x32_bf16 v[24:27], v[136:139], v[194:197], v[24:27]
	v_mfma_f32_16x16x32_bf16 v[16:19], v[128:131], v[202:205], v[16:19]
	v_mfma_f32_16x16x32_bf16 v[8:11], v[136:139], v[202:205], v[8:11]
	v_mfma_f32_16x16x32_bf16 v[60:63], v[132:135], v[182:185], v[60:63]
	v_mfma_f32_16x16x32_bf16 v[56:59], v[140:143], v[182:185], v[56:59]
	v_mfma_f32_16x16x32_bf16 v[48:51], v[132:135], v[190:193], v[48:51]
	v_mfma_f32_16x16x32_bf16 v[40:43], v[140:143], v[190:193], v[40:43]
	v_mfma_f32_16x16x32_bf16 v[32:35], v[132:135], v[198:201], v[32:35]
	v_mfma_f32_16x16x32_bf16 v[24:27], v[140:143], v[198:201], v[24:27]
	v_mfma_f32_16x16x32_bf16 v[16:19], v[132:135], v[206:209], v[16:19]
	v_mfma_f32_16x16x32_bf16 v[8:11], v[140:143], v[206:209], v[8:11]
	v_mfma_f32_16x16x32_bf16 v[52:55], v[144:147], v[178:181], v[52:55]
	v_mfma_f32_16x16x32_bf16 v[44:47], v[166:169], v[178:181], v[44:47]
	v_mfma_f32_16x16x32_bf16 v[36:39], v[144:147], v[186:189], v[36:39]
	v_mfma_f32_16x16x32_bf16 v[28:31], v[166:169], v[186:189], v[28:31]
	v_mfma_f32_16x16x32_bf16 v[20:23], v[144:147], v[194:197], v[20:23]
	v_mfma_f32_16x16x32_bf16 v[12:15], v[166:169], v[194:197], v[12:15]
	v_mfma_f32_16x16x32_bf16 v[4:7], v[144:147], v[202:205], v[4:7]
	v_mfma_f32_16x16x32_bf16 v[0:3], v[166:169], v[202:205], v[0:3]
	v_mfma_f32_16x16x32_bf16 v[52:55], v[148:151], v[182:185], v[52:55]
	v_mfma_f32_16x16x32_bf16 v[44:47], v[170:173], v[182:185], v[44:47]
	v_mfma_f32_16x16x32_bf16 v[36:39], v[148:151], v[190:193], v[36:39]
	v_mfma_f32_16x16x32_bf16 v[28:31], v[170:173], v[190:193], v[28:31]
	v_mfma_f32_16x16x32_bf16 v[20:23], v[148:151], v[198:201], v[20:23]
	v_mfma_f32_16x16x32_bf16 v[12:15], v[170:173], v[198:201], v[12:15]
	v_mfma_f32_16x16x32_bf16 v[4:7], v[148:151], v[206:209], v[4:7]
	v_mfma_f32_16x16x32_bf16 v[0:3], v[170:173], v[206:209], v[0:3]
	s_barrier
	s_add_i32 s63, 0, 0x18000
	s_add_i32 s64, 0, 0x1c000
	v_add_u32_e32 v140, s63, v174
	v_add_u32_e32 v170, s64, v174
	ds_read_b128 v[128:131], v140
	ds_read_b128 v[132:135], v140 offset:1024
	ds_read_b128 v[136:139], v140 offset:2048
	ds_read_b128 v[140:143], v140 offset:3072
	ds_read_b128 v[144:147], v170
	ds_read_b128 v[148:151], v170 offset:1024
	ds_read_b128 v[166:169], v170 offset:2048
	ds_read_b128 v[170:173], v170 offset:3072
	s_add_u32 s30, s30, 0x40000
	s_addc_u32 s31, s31, 0
	s_mov_b32 m0, s38
	v_lshl_add_u64 v[218:219], s[30:31], 0, v[158:159]
	ds_read_b128 v[178:181], v177 offset:32768
	ds_read_b128 v[182:185], v177 offset:33792
	ds_read_b128 v[186:189], v177 offset:34816
	ds_read_b128 v[190:193], v177 offset:35840
	ds_read_b128 v[194:197], v177 offset:36864
	ds_read_b128 v[198:201], v177 offset:37888
	ds_read_b128 v[202:205], v177 offset:38912
	ds_read_b128 v[206:209], v177 offset:39936
	global_load_lds_dwordx4 v[218:219], off
	v_lshl_add_u64 v[218:219], s[30:31], 0, v[154:155]
	s_mov_b32 m0, s39
	s_nop 0
	global_load_lds_dwordx4 v[218:219], off
	s_waitcnt vmcnt(8)
	s_waitcnt lgkmcnt(0)
	s_barrier
	s_waitcnt lgkmcnt(0)
	v_mfma_f32_16x16x32_bf16 v[124:127], v[128:131], v[178:181], v[124:127]
	v_mfma_f32_16x16x32_bf16 v[120:123], v[136:139], v[178:181], v[120:123]
	v_mfma_f32_16x16x32_bf16 v[116:119], v[128:131], v[186:189], v[116:119]
	v_mfma_f32_16x16x32_bf16 v[112:115], v[136:139], v[186:189], v[112:115]
	v_mfma_f32_16x16x32_bf16 v[96:99], v[128:131], v[194:197], v[96:99]
	v_mfma_f32_16x16x32_bf16 v[88:91], v[136:139], v[194:197], v[88:91]
	v_mfma_f32_16x16x32_bf16 v[80:83], v[128:131], v[202:205], v[80:83]
	v_mfma_f32_16x16x32_bf16 v[72:75], v[136:139], v[202:205], v[72:75]
	v_mfma_f32_16x16x32_bf16 v[124:127], v[132:135], v[182:185], v[124:127]
	v_mfma_f32_16x16x32_bf16 v[120:123], v[140:143], v[182:185], v[120:123]
	v_mfma_f32_16x16x32_bf16 v[116:119], v[132:135], v[190:193], v[116:119]
	v_mfma_f32_16x16x32_bf16 v[112:115], v[140:143], v[190:193], v[112:115]
	v_mfma_f32_16x16x32_bf16 v[96:99], v[132:135], v[198:201], v[96:99]
	v_mfma_f32_16x16x32_bf16 v[88:91], v[140:143], v[198:201], v[88:91]
	v_mfma_f32_16x16x32_bf16 v[80:83], v[132:135], v[206:209], v[80:83]
	v_mfma_f32_16x16x32_bf16 v[72:75], v[140:143], v[206:209], v[72:75]
	v_mfma_f32_16x16x32_bf16 v[108:111], v[144:147], v[178:181], v[108:111]
	v_mfma_f32_16x16x32_bf16 v[104:107], v[166:169], v[178:181], v[104:107]
	v_mfma_f32_16x16x32_bf16 v[100:103], v[144:147], v[186:189], v[100:103]
	v_mfma_f32_16x16x32_bf16 v[92:95], v[166:169], v[186:189], v[92:95]
	v_mfma_f32_16x16x32_bf16 v[84:87], v[144:147], v[194:197], v[84:87]
	v_mfma_f32_16x16x32_bf16 v[76:79], v[166:169], v[194:197], v[76:79]
	v_mfma_f32_16x16x32_bf16 v[68:71], v[144:147], v[202:205], v[68:71]
	v_mfma_f32_16x16x32_bf16 v[64:67], v[166:169], v[202:205], v[64:67]
	v_mfma_f32_16x16x32_bf16 v[108:111], v[148:151], v[182:185], v[108:111]
	v_mfma_f32_16x16x32_bf16 v[104:107], v[170:173], v[182:185], v[104:107]
	v_mfma_f32_16x16x32_bf16 v[100:103], v[148:151], v[190:193], v[100:103]
	v_mfma_f32_16x16x32_bf16 v[92:95], v[170:173], v[190:193], v[92:95]
	v_mfma_f32_16x16x32_bf16 v[84:87], v[148:151], v[198:201], v[84:87]
	v_mfma_f32_16x16x32_bf16 v[76:79], v[170:173], v[198:201], v[76:79]
	v_mfma_f32_16x16x32_bf16 v[68:71], v[148:151], v[206:209], v[68:71]
	v_mfma_f32_16x16x32_bf16 v[64:67], v[170:173], v[206:209], v[64:67]
	s_barrier
; #define PG8_LDA(dst, b, h) do { _Pragma("unroll") for (int m = 0; m < 4; ++m) _Pragma("unroll") for (int k = 0; k < 2; ++k) dst[m][k] = *(const PG8_LAS bf16x8*)(lds + PG8_SA(b, h) + aoff + m * 2048 + k * 1024); } while (0)
; #define PG8_WAIT_V(n) asm volatile("s_waitcnt vmcnt(" #n ")" ::: "memory")
; #define PG8_WAIT_L(n) asm volatile("s_waitcnt lgkmcnt(" #n ")" ::: "memory")
; #define PG8_BAR __builtin_amdgcn_s_barrier()
; #define PG8_SCHED __builtin_amdgcn_sched_barrier(0)
; template <class Epi, class Sched, bool ALIGN_EPI = false, bool SP2 = false, bool F8 = false, bool I8 = false, bool PF = false>
; __device__ __forceinline__ void gemm_phase(PG8_LAS unsigned char* lds, const Gemm g, const Sched& S, const Epi& E, const int wave_) {
;     ...
;             PG8_LDA(At, 1, 1); PG8_STAGE(PG8_SB(1, 0), b3, voffB); PG8_STAGE(PG8_SB(1, 1), b3 + hstep, voffB); PG8_STAGE(PG8_SA(1, 0), a3, voffA);
;             PG8_WAIT_V(8); PG8_WAIT_L(0); PG8_BAR; PG8_MMA(1, 0, At, B0); PG8_MMA(1, 1, At, B1); PG8_BAR; PG8_SCHED;
	s_add_i32 s30, s63, s36
	v_lshl_add_u64 v[210:211], v[210:211], 0, s[6:7]
	s_mov_b32 m0, s30
	ds_read_b128 v[178:181], v177 offset:49152
	global_load_lds_dwordx4 v[210:211], off
	ds_read_b128 v[182:185], v177 offset:50176
	s_add_i32 m0, s30, 0x2000
	s_add_u32 s28, s28, 0x40080
	v_lshl_add_u64 v[210:211], v[212:213], 0, s[6:7]
	s_addc_u32 s29, s29, 0
	s_add_i32 s30, s64, s36
	global_load_lds_dwordx4 v[210:211], off
	ds_read_b128 v[186:189], v177 offset:51200
	v_lshl_add_u64 v[210:211], s[28:29], 0, v[156:157]
	s_mov_b32 m0, s30
	ds_read_b128 v[190:193], v177 offset:52224
	global_load_lds_dwordx4 v[210:211], off
	ds_read_b128 v[194:197], v177 offset:53248
	v_lshl_add_u64 v[210:211], s[28:29], 0, v[152:153]
	s_add_i32 m0, s30, 0x2000
	ds_read_b128 v[198:201], v177 offset:54272
	global_load_lds_dwordx4 v[210:211], off
	ds_read_b128 v[202:205], v177 offset:55296
	v_lshl_add_u64 v[210:211], v[214:215], 0, s[6:7]
	s_mov_b32 m0, s46
	ds_read_b128 v[206:209], v177 offset:56320
	global_load_lds_dwordx4 v[210:211], off
	v_lshl_add_u64 v[210:211], v[216:217], 0, s[6:7]
	s_mov_b32 m0, s47
	s_nop 0
	global_load_lds_dwordx4 v[210:211], off
	s_waitcnt vmcnt(8)
	s_waitcnt lgkmcnt(0)
	s_barrier
	s_waitcnt lgkmcnt(0)
	v_mfma_f32_16x16x32_bf16 v[60:63], v[128:131], v[178:181], v[60:63]
	v_mfma_f32_16x16x32_bf16 v[56:59], v[136:139], v[178:181], v[56:59]
	v_mfma_f32_16x16x32_bf16 v[48:51], v[128:131], v[186:189], v[48:51]
	v_mfma_f32_16x16x32_bf16 v[40:43], v[136:139], v[186:189], v[40:43]
	v_mfma_f32_16x16x32_bf16 v[32:35], v[128:131], v[194:197], v[32:35]
	v_mfma_f32_16x16x32_bf16 v[24:27], v[136:139], v[194:197], v[24:27]
	v_mfma_f32_16x16x32_bf16 v[16:19], v[128:131], v[202:205], v[16:19]
	v_mfma_f32_16x16x32_bf16 v[8:11], v[136:139], v[202:205], v[8:11]
	v_mfma_f32_16x16x32_bf16 v[60:63], v[132:135], v[182:185], v[60:63]
	v_mfma_f32_16x16x32_bf16 v[56:59], v[140:143], v[182:185], v[56:59]
	v_mfma_f32_16x16x32_bf16 v[48:51], v[132:135], v[190:193], v[48:51]
	v_mfma_f32_16x16x32_bf16 v[40:43], v[140:143], v[190:193], v[40:43]
	v_mfma_f32_16x16x32_bf16 v[32:35], v[132:135], v[198:201], v[32:35]
	v_mfma_f32_16x16x32_bf16 v[24:27], v[140:143], v[198:201], v[24:27]
	v_mfma_f32_16x16x32_bf16 v[16:19], v[132:135], v[206:209], v[16:19]
	v_mfma_f32_16x16x32_bf16 v[8:11], v[140:143], v[206:209], v[8:11]
	v_mfma_f32_16x16x32_bf16 v[52:55], v[144:147], v[178:181], v[52:55]
	v_mfma_f32_16x16x32_bf16 v[44:47], v[166:169], v[178:181], v[44:47]
	v_mfma_f32_16x16x32_bf16 v[36:39], v[144:147], v[186:189], v[36:39]
	v_mfma_f32_16x16x32_bf16 v[28:31], v[166:169], v[186:189], v[28:31]
	v_mfma_f32_16x16x32_bf16 v[20:23], v[144:147], v[194:197], v[20:23]
	v_mfma_f32_16x16x32_bf16 v[12:15], v[166:169], v[194:197], v[12:15]
	v_mfma_f32_16x16x32_bf16 v[4:7], v[144:147], v[202:205], v[4:7]
	v_mfma_f32_16x16x32_bf16 v[0:3], v[166:169], v[202:205], v[0:3]
	v_mfma_f32_16x16x32_bf16 v[52:55], v[148:151], v[182:185], v[52:55]
	v_mfma_f32_16x16x32_bf16 v[44:47], v[170:173], v[182:185], v[44:47]
	v_mfma_f32_16x16x32_bf16 v[36:39], v[148:151], v[190:193], v[36:39]
	v_mfma_f32_16x16x32_bf16 v[28:31], v[170:173], v[190:193], v[28:31]
	v_mfma_f32_16x16x32_bf16 v[20:23], v[148:151], v[198:201], v[20:23]
	v_mfma_f32_16x16x32_bf16 v[12:15], v[170:173], v[198:201], v[12:15]
	v_mfma_f32_16x16x32_bf16 v[4:7], v[148:151], v[206:209], v[4:7]
	v_mfma_f32_16x16x32_bf16 v[0:3], v[170:173], v[206:209], v[0:3]
	s_barrier
	s_add_i32 s62, s62, 2
	s_add_u32 s22, s22, 0x100
	s_addc_u32 s23, s23, 0
	s_add_u32 s54, s54, 0x100
	s_addc_u32 s55, s55, 0
	s_cmp_gt_u32 s62, 13
	s_cbranch_scc0 .LBB0_453
	s_and_b64 vcc, exec, s[8:9]
	s_cbranch_vccz .LBB0_456
	s_barrier

; #define PG8_LDA(dst, b, h) do { _Pragma("unroll") for (int m = 0; m < 4; ++m) _Pragma("unroll") for (int k = 0; k < 2; ++k) dst[m][k] = *(const PG8_LAS bf16x8*)(lds + PG8_SA(b, h) + aoff + m * 2048 + k * 1024); } while (0)
; #define PG8_LDB(dst, b, h) do { _Pragma("unroll") for (int n = 0; n < 2; ++n) _Pragma("unroll") for (int k = 0; k < 2; ++k) dst[n][k] = *(const PG8_LAS bf16x8*)(lds + PG8_SB(b, h) + boff + n * 2048 + k * 1024); } while (0)
; #define PG8_WAIT_V(n) asm volatile("s_waitcnt vmcnt(" #n ")" ::: "memory")
; #define PG8_WAIT_L(n) asm volatile("s_waitcnt lgkmcnt(" #n ")" ::: "memory")
; #define PG8_BAR __builtin_amdgcn_s_barrier()
; #define PG8_SCHED __builtin_amdgcn_sched_barrier(0)
; template <class Epi, class Sched, bool ALIGN_EPI = false, bool SP2 = false, bool F8 = false, bool I8 = false, bool PF = false>
; __device__ __forceinline__ void gemm_phase(PG8_LAS unsigned char* lds, const Gemm g, const Sched& S, const Epi& E, const int wave_) {
;     ...
;             PG8_LDB(B0, 0, 0); PG8_LDB(B1, 0, 1); PG8_SCHED; PG8_LDA(At, 0, 0); PG8_STAGE(PG8_SA(1, 1), a1 + hstep, voffA);
;             PG8_WAIT_V(8); PG8_WAIT_L(0); PG8_BAR; PG8_MMA(0, 0, At, B0); PG8_MMA(0, 1, At, B1); PG8_BAR; PG8_SCHED;
;             PG8_LDA(At, 0, 1); PG8_STAGE(PG8_SB(0, 0), b2, voffB); PG8_STAGE(PG8_SB(0, 1), b2 + hstep, voffB); PG8_STAGE(PG8_SA(0, 0), a2, voffA);
;             PG8_WAIT_V(8); PG8_WAIT_L(0); PG8_BAR; PG8_MMA(1, 0, At, B0); PG8_MMA(1, 1, At, B1); PG8_BAR; PG8_SCHED;
.LBB0_591:
	ds_read_b128 v[142:145], v153
	ds_read_b128 v[146:149], v153 offset:1024
	ds_read_b128 v[158:161], v153 offset:2048
	ds_read_b128 v[162:165], v153 offset:3072
	ds_read_b128 v[166:169], v154
	ds_read_b128 v[170:173], v154 offset:1024
	ds_read_b128 v[174:177], v154 offset:2048
	ds_read_b128 v[178:181], v154 offset:3072
	s_add_u32 s34, s30, 0xfffe0080
	s_addc_u32 s35, s31, -1
	s_cmp_eq_u32 s64, 4
	s_cselect_b32 s37, s19, s35
	s_cselect_b32 s36, s56, s34
	s_cselect_b32 s35, s17, s63
	s_cselect_b32 s34, s57, s62
	v_lshl_add_u64 v[150:151], s[30:31], 0, v[136:137]
	s_add_i32 m0, s29, 0xc000
	ds_read_b128 v[182:185], v155
	ds_read_b128 v[186:189], v155 offset:1024
	ds_read_b128 v[190:193], v155 offset:2048
	ds_read_b128 v[194:197], v155 offset:3072
	ds_read_b128 v[198:201], v155 offset:4096
	ds_read_b128 v[202:205], v155 offset:5120
	ds_read_b128 v[206:209], v155 offset:6144
	ds_read_b128 v[210:213], v155 offset:7168
	global_load_lds_dwordx4 v[150:151], off
	v_lshl_add_u64 v[150:151], s[30:31], 0, v[138:139]
	s_add_i32 m0, s29, 0xe000
	s_nop 0
	global_load_lds_dwordx4 v[150:151], off
	s_waitcnt vmcnt(8)
	s_waitcnt lgkmcnt(0)
	s_barrier
	s_waitcnt lgkmcnt(0)
	v_mfma_i32_16x16x64_i8 v[124:127], v[142:145], v[182:185], v[124:127]
	v_mfma_i32_16x16x64_i8 v[120:123], v[158:161], v[182:185], v[120:123]
	v_mfma_i32_16x16x64_i8 v[108:111], v[142:145], v[190:193], v[108:111]
	v_mfma_i32_16x16x64_i8 v[104:107], v[158:161], v[190:193], v[104:107]
	v_mfma_i32_16x16x64_i8 v[92:95], v[142:145], v[198:201], v[92:95]
	v_mfma_i32_16x16x64_i8 v[88:91], v[158:161], v[198:201], v[88:91]
	v_mfma_i32_16x16x64_i8 v[76:79], v[142:145], v[206:209], v[76:79]
	v_mfma_i32_16x16x64_i8 v[72:75], v[158:161], v[206:209], v[72:75]
	v_mfma_i32_16x16x64_i8 v[124:127], v[146:149], v[186:189], v[124:127]
	v_mfma_i32_16x16x64_i8 v[120:123], v[162:165], v[186:189], v[120:123]
	v_mfma_i32_16x16x64_i8 v[108:111], v[146:149], v[194:197], v[108:111]
	v_mfma_i32_16x16x64_i8 v[104:107], v[162:165], v[194:197], v[104:107]
	v_mfma_i32_16x16x64_i8 v[92:95], v[146:149], v[202:205], v[92:95]
	v_mfma_i32_16x16x64_i8 v[88:91], v[162:165], v[202:205], v[88:91]
	v_mfma_i32_16x16x64_i8 v[76:79], v[146:149], v[210:213], v[76:79]
	v_mfma_i32_16x16x64_i8 v[72:75], v[162:165], v[210:213], v[72:75]
	v_mfma_i32_16x16x64_i8 v[116:119], v[166:169], v[182:185], v[116:119]
	v_mfma_i32_16x16x64_i8 v[112:115], v[174:177], v[182:185], v[112:115]
	v_mfma_i32_16x16x64_i8 v[100:103], v[166:169], v[190:193], v[100:103]
	v_mfma_i32_16x16x64_i8 v[96:99], v[174:177], v[190:193], v[96:99]
	v_mfma_i32_16x16x64_i8 v[84:87], v[166:169], v[198:201], v[84:87]
	v_mfma_i32_16x16x64_i8 v[80:83], v[174:177], v[198:201], v[80:83]
	v_mfma_i32_16x16x64_i8 v[68:71], v[166:169], v[206:209], v[68:71]
	v_mfma_i32_16x16x64_i8 v[64:67], v[174:177], v[206:209], v[64:67]
	v_mfma_i32_16x16x64_i8 v[116:119], v[170:173], v[186:189], v[116:119]
	v_mfma_i32_16x16x64_i8 v[112:115], v[178:181], v[186:189], v[112:115]
	v_mfma_i32_16x16x64_i8 v[100:103], v[170:173], v[194:197], v[100:103]
	v_mfma_i32_16x16x64_i8 v[96:99], v[178:181], v[194:197], v[96:99]
	v_mfma_i32_16x16x64_i8 v[84:87], v[170:173], v[202:205], v[84:87]
	v_mfma_i32_16x16x64_i8 v[80:83], v[178:181], v[202:205], v[80:83]
	v_mfma_i32_16x16x64_i8 v[68:71], v[170:173], v[210:213], v[68:71]
	v_mfma_i32_16x16x64_i8 v[64:67], v[178:181], v[210:213], v[64:67]
	s_barrier
	s_add_i32 s65, s51, s39
	v_lshl_add_u64 v[150:151], s[34:35], 0, v[132:133]
	s_mov_b32 m0, s65
	ds_read_b128 v[182:185], v155 offset:16384
	global_load_lds_dwordx4 v[150:151], off
	ds_read_b128 v[186:189], v155 offset:17408
	s_add_i32 m0, s65, 0x2000
	s_add_u32 s66, s34, 0x20000
	v_lshl_add_u64 v[214:215], s[34:35], 0, v[128:129]
	s_addc_u32 s67, s35, 0
	s_add_i32 s65, s52, s39
	global_load_lds_dwordx4 v[214:215], off
	ds_read_b128 v[190:193], v155 offset:18432
	v_lshl_add_u64 v[216:217], s[66:67], 0, v[132:133]
	s_mov_b32 m0, s65
	v_lshl_add_u64 v[218:219], s[36:37], 0, v[130:131]
	global_load_lds_dwordx4 v[216:217], off
	ds_read_b128 v[194:197], v155 offset:19456
	v_lshl_add_u64 v[216:217], s[66:67], 0, v[128:129]
	s_add_i32 m0, s65, 0x2000
	ds_read_b128 v[198:201], v155 offset:20480
	global_load_lds_dwordx4 v[216:217], off
	ds_read_b128 v[202:205], v155 offset:21504
	v_lshl_add_u64 v[216:217], s[36:37], 0, v[134:135]
	s_mov_b32 m0, s29
	ds_read_b128 v[206:209], v155 offset:22528
	global_load_lds_dwordx4 v[216:217], off
	ds_read_b128 v[210:213], v155 offset:23552
	s_mov_b32 m0, s41
	s_nop 0
	global_load_lds_dwordx4 v[218:219], off
	s_waitcnt vmcnt(8)
	s_waitcnt lgkmcnt(0)
	s_barrier
; #define PG8_LDA(dst, b, h) do { _Pragma("unroll") for (int m = 0; m < 4; ++m) _Pragma("unroll") for (int k = 0; k < 2; ++k) dst[m][k] = *(const PG8_LAS bf16x8*)(lds + PG8_SA(b, h) + aoff + m * 2048 + k * 1024); } while (0)
; #define PG8_LDB(dst, b, h) do { _Pragma("unroll") for (int n = 0; n < 2; ++n) _Pragma("unroll") for (int k = 0; k < 2; ++k) dst[n][k] = *(const PG8_LAS bf16x8*)(lds + PG8_SB(b, h) + boff + n * 2048 + k * 1024); } while (0)
; #define PG8_WAIT_V(n) asm volatile("s_waitcnt vmcnt(" #n ")" ::: "memory")
; #define PG8_WAIT_L(n) asm volatile("s_waitcnt lgkmcnt(" #n ")" ::: "memory")
; #define PG8_BAR __builtin_amdgcn_s_barrier()
; #define PG8_SCHED __builtin_amdgcn_sched_barrier(0)
; template <class Epi, class Sched, bool ALIGN_EPI = false, bool SP2 = false, bool F8 = false, bool I8 = false, bool PF = false>
; __device__ __forceinline__ void gemm_phase(PG8_LAS unsigned char* lds, const Gemm g, const Sched& S, const Epi& E, const int wave_) {
;     ...
;             PG8_WAIT_V(8); PG8_WAIT_L(0); PG8_BAR; PG8_MMA(1, 0, At, B0); PG8_MMA(1, 1, At, B1); PG8_BAR; PG8_SCHED;
;             PG8_LDB(B0, 1, 0); PG8_LDB(B1, 1, 1); PG8_SCHED; PG8_LDA(At, 1, 0); PG8_STAGE(PG8_SA(0, 1), a2 + hstep, voffA);
;             PG8_WAIT_V(8); PG8_WAIT_L(0); PG8_BAR; PG8_MMA(0, 0, At, B0); PG8_MMA(0, 1, At, B1); PG8_BAR; PG8_SCHED;
;             PG8_LDA(At, 1, 1); PG8_STAGE(PG8_SB(1, 0), b3, voffB); PG8_STAGE(PG8_SB(1, 1), b3 + hstep, voffB); PG8_STAGE(PG8_SA(1, 0), a3, voffA);
	s_waitcnt lgkmcnt(0)
	v_mfma_i32_16x16x64_i8 v[60:63], v[142:145], v[182:185], v[60:63]
	v_mfma_i32_16x16x64_i8 v[56:59], v[158:161], v[182:185], v[56:59]
	v_mfma_i32_16x16x64_i8 v[44:47], v[142:145], v[190:193], v[44:47]
	v_mfma_i32_16x16x64_i8 v[40:43], v[158:161], v[190:193], v[40:43]
	v_mfma_i32_16x16x64_i8 v[28:31], v[142:145], v[198:201], v[28:31]
	v_mfma_i32_16x16x64_i8 v[24:27], v[158:161], v[198:201], v[24:27]
	v_mfma_i32_16x16x64_i8 v[12:15], v[142:145], v[206:209], v[12:15]
	v_mfma_i32_16x16x64_i8 v[8:11], v[158:161], v[206:209], v[8:11]
	v_mfma_i32_16x16x64_i8 v[60:63], v[146:149], v[186:189], v[60:63]
	v_mfma_i32_16x16x64_i8 v[56:59], v[162:165], v[186:189], v[56:59]
	v_mfma_i32_16x16x64_i8 v[44:47], v[146:149], v[194:197], v[44:47]
	v_mfma_i32_16x16x64_i8 v[40:43], v[162:165], v[194:197], v[40:43]
	v_mfma_i32_16x16x64_i8 v[28:31], v[146:149], v[202:205], v[28:31]
	v_mfma_i32_16x16x64_i8 v[24:27], v[162:165], v[202:205], v[24:27]
	v_mfma_i32_16x16x64_i8 v[12:15], v[146:149], v[210:213], v[12:15]
	v_mfma_i32_16x16x64_i8 v[8:11], v[162:165], v[210:213], v[8:11]
	v_mfma_i32_16x16x64_i8 v[52:55], v[166:169], v[182:185], v[52:55]
	v_mfma_i32_16x16x64_i8 v[48:51], v[174:177], v[182:185], v[48:51]
	v_mfma_i32_16x16x64_i8 v[36:39], v[166:169], v[190:193], v[36:39]
	v_mfma_i32_16x16x64_i8 v[32:35], v[174:177], v[190:193], v[32:35]
	v_mfma_i32_16x16x64_i8 v[20:23], v[166:169], v[198:201], v[20:23]
	v_mfma_i32_16x16x64_i8 v[16:19], v[174:177], v[198:201], v[16:19]
	v_mfma_i32_16x16x64_i8 v[4:7], v[166:169], v[206:209], v[4:7]
	v_mfma_i32_16x16x64_i8 v[0:3], v[174:177], v[206:209], v[0:3]
	v_mfma_i32_16x16x64_i8 v[52:55], v[170:173], v[186:189], v[52:55]
	v_mfma_i32_16x16x64_i8 v[48:51], v[178:181], v[186:189], v[48:51]
	v_mfma_i32_16x16x64_i8 v[36:39], v[170:173], v[194:197], v[36:39]
	v_mfma_i32_16x16x64_i8 v[32:35], v[178:181], v[194:197], v[32:35]
	v_mfma_i32_16x16x64_i8 v[20:23], v[170:173], v[202:205], v[20:23]
	v_mfma_i32_16x16x64_i8 v[16:19], v[178:181], v[202:205], v[16:19]
	v_mfma_i32_16x16x64_i8 v[4:7], v[170:173], v[210:213], v[4:7]
	v_mfma_i32_16x16x64_i8 v[0:3], v[178:181], v[210:213], v[0:3]
	s_barrier
	s_add_i32 s65, 0, 0x18000
	v_add_u32_e32 v157, s65, v152
	s_add_i32 s66, 0, 0x1c000
	ds_read_b128 v[142:145], v157
	ds_read_b128 v[146:149], v157 offset:1024
	ds_read_b128 v[158:161], v157 offset:2048
	ds_read_b128 v[162:165], v157 offset:3072
	v_add_u32_e32 v157, s66, v152
	ds_read_b128 v[166:169], v157
	ds_read_b128 v[170:173], v157 offset:1024
	ds_read_b128 v[174:177], v157 offset:2048
	ds_read_b128 v[178:181], v157 offset:3072
	s_add_u32 s36, s36, 0x20000
	s_addc_u32 s37, s37, 0
	s_mov_b32 m0, s42
	v_lshl_add_u64 v[220:221], s[36:37], 0, v[134:135]
	ds_read_b128 v[182:185], v155 offset:32768
	ds_read_b128 v[186:189], v155 offset:33792
	ds_read_b128 v[190:193], v155 offset:34816
	ds_read_b128 v[194:197], v155 offset:35840
	ds_read_b128 v[198:201], v155 offset:36864
	ds_read_b128 v[202:205], v155 offset:37888
	ds_read_b128 v[206:209], v155 offset:38912
	ds_read_b128 v[210:213], v155 offset:39936
	global_load_lds_dwordx4 v[220:221], off
	v_lshl_add_u64 v[220:221], s[36:37], 0, v[130:131]
	s_mov_b32 m0, s43
	s_nop 0
	global_load_lds_dwordx4 v[220:221], off
	s_waitcnt vmcnt(8)
	s_waitcnt lgkmcnt(0)
	s_barrier
	s_waitcnt lgkmcnt(0)
	v_mfma_i32_16x16x64_i8 v[124:127], v[142:145], v[182:185], v[124:127]
	v_mfma_i32_16x16x64_i8 v[120:123], v[158:161], v[182:185], v[120:123]
	v_mfma_i32_16x16x64_i8 v[108:111], v[142:145], v[190:193], v[108:111]
	v_mfma_i32_16x16x64_i8 v[104:107], v[158:161], v[190:193], v[104:107]
	v_mfma_i32_16x16x64_i8 v[92:95], v[142:145], v[198:201], v[92:95]
	v_mfma_i32_16x16x64_i8 v[88:91], v[158:161], v[198:201], v[88:91]
	v_mfma_i32_16x16x64_i8 v[76:79], v[142:145], v[206:209], v[76:79]
	v_mfma_i32_16x16x64_i8 v[72:75], v[158:161], v[206:209], v[72:75]
	v_mfma_i32_16x16x64_i8 v[124:127], v[146:149], v[186:189], v[124:127]
	v_mfma_i32_16x16x64_i8 v[120:123], v[162:165], v[186:189], v[120:123]
	v_mfma_i32_16x16x64_i8 v[108:111], v[146:149], v[194:197], v[108:111]
	v_mfma_i32_16x16x64_i8 v[104:107], v[162:165], v[194:197], v[104:107]
	v_mfma_i32_16x16x64_i8 v[92:95], v[146:149], v[202:205], v[92:95]
	v_mfma_i32_16x16x64_i8 v[88:91], v[162:165], v[202:205], v[88:91]
	v_mfma_i32_16x16x64_i8 v[76:79], v[146:149], v[210:213], v[76:79]
	v_mfma_i32_16x16x64_i8 v[72:75], v[162:165], v[210:213], v[72:75]
	v_mfma_i32_16x16x64_i8 v[116:119], v[166:169], v[182:185], v[116:119]
	v_mfma_i32_16x16x64_i8 v[112:115], v[174:177], v[182:185], v[112:115]
	v_mfma_i32_16x16x64_i8 v[100:103], v[166:169], v[190:193], v[100:103]
	v_mfma_i32_16x16x64_i8 v[96:99], v[174:177], v[190:193], v[96:99]
	v_mfma_i32_16x16x64_i8 v[84:87], v[166:169], v[198:201], v[84:87]
	v_mfma_i32_16x16x64_i8 v[80:83], v[174:177], v[198:201], v[80:83]
	v_mfma_i32_16x16x64_i8 v[68:71], v[166:169], v[206:209], v[68:71]
	v_mfma_i32_16x16x64_i8 v[64:67], v[174:177], v[206:209], v[64:67]
	v_mfma_i32_16x16x64_i8 v[116:119], v[170:173], v[186:189], v[116:119]
	v_mfma_i32_16x16x64_i8 v[112:115], v[178:181], v[186:189], v[112:115]
	v_mfma_i32_16x16x64_i8 v[100:103], v[170:173], v[194:197], v[100:103]
	v_mfma_i32_16x16x64_i8 v[96:99], v[178:181], v[194:197], v[96:99]
	v_mfma_i32_16x16x64_i8 v[84:87], v[170:173], v[202:205], v[84:87]
	v_mfma_i32_16x16x64_i8 v[80:83], v[178:181], v[202:205], v[80:83]
	v_mfma_i32_16x16x64_i8 v[68:71], v[170:173], v[210:213], v[68:71]
	v_mfma_i32_16x16x64_i8 v[64:67], v[178:181], v[210:213], v[64:67]
	s_barrier
; #define PG8_LDA(dst, b, h) do { _Pragma("unroll") for (int m = 0; m < 4; ++m) _Pragma("unroll") for (int k = 0; k < 2; ++k) dst[m][k] = *(const PG8_LAS bf16x8*)(lds + PG8_SA(b, h) + aoff + m * 2048 + k * 1024); } while (0)
; #define PG8_WAIT_V(n) asm volatile("s_waitcnt vmcnt(" #n ")" ::: "memory")
; #define PG8_WAIT_L(n) asm volatile("s_waitcnt lgkmcnt(" #n ")" ::: "memory")
; #define PG8_BAR __builtin_amdgcn_s_barrier()
; #define PG8_SCHED __builtin_amdgcn_sched_barrier(0)
; template <class Epi, class Sched, bool ALIGN_EPI = false, bool SP2 = false, bool F8 = false, bool I8 = false, bool PF = false>
; __device__ __forceinline__ void gemm_phase(PG8_LAS unsigned char* lds, const Gemm g, const Sched& S, const Epi& E, const int wave_) {
;     ...
;             PG8_LDA(At, 1, 1); PG8_STAGE(PG8_SB(1, 0), b3, voffB); PG8_STAGE(PG8_SB(1, 1), b3 + hstep, voffB); PG8_STAGE(PG8_SA(1, 0), a3, voffA);
;             PG8_WAIT_V(8); PG8_WAIT_L(0); PG8_BAR; PG8_MMA(1, 0, At, B0); PG8_MMA(1, 1, At, B1); PG8_BAR; PG8_SCHED;
	s_add_i32 s36, s65, s39
	v_lshl_add_u64 v[150:151], v[150:151], 0, s[10:11]
	s_mov_b32 m0, s36
	ds_read_b128 v[182:185], v155 offset:49152
	global_load_lds_dwordx4 v[150:151], off
	ds_read_b128 v[186:189], v155 offset:50176
	s_add_i32 m0, s36, 0x2000
	s_add_u32 s34, s34, 0x20080
	v_lshl_add_u64 v[150:151], v[214:215], 0, s[10:11]
	s_addc_u32 s35, s35, 0
	s_add_i32 s36, s66, s39
	global_load_lds_dwordx4 v[150:151], off
	ds_read_b128 v[190:193], v155 offset:51200
	v_lshl_add_u64 v[150:151], s[34:35], 0, v[132:133]
	s_mov_b32 m0, s36
	ds_read_b128 v[194:197], v155 offset:52224
	global_load_lds_dwordx4 v[150:151], off
	ds_read_b128 v[198:201], v155 offset:53248
	v_lshl_add_u64 v[150:151], s[34:35], 0, v[128:129]
	s_add_i32 m0, s36, 0x2000
	ds_read_b128 v[202:205], v155 offset:54272
	global_load_lds_dwordx4 v[150:151], off
	ds_read_b128 v[206:209], v155 offset:55296
	v_lshl_add_u64 v[150:151], v[216:217], 0, s[10:11]
	s_mov_b32 m0, s48
	ds_read_b128 v[210:213], v155 offset:56320
	global_load_lds_dwordx4 v[150:151], off
	v_lshl_add_u64 v[150:151], v[218:219], 0, s[10:11]
	s_mov_b32 m0, s49
	s_nop 0
	global_load_lds_dwordx4 v[150:151], off
	s_waitcnt vmcnt(8)
	s_waitcnt lgkmcnt(0)
	s_barrier
	s_waitcnt lgkmcnt(0)
	v_mfma_i32_16x16x64_i8 v[60:63], v[142:145], v[182:185], v[60:63]
	v_mfma_i32_16x16x64_i8 v[56:59], v[158:161], v[182:185], v[56:59]
	v_mfma_i32_16x16x64_i8 v[44:47], v[142:145], v[190:193], v[44:47]
	v_mfma_i32_16x16x64_i8 v[40:43], v[158:161], v[190:193], v[40:43]
	v_mfma_i32_16x16x64_i8 v[28:31], v[142:145], v[198:201], v[28:31]
	v_mfma_i32_16x16x64_i8 v[24:27], v[158:161], v[198:201], v[24:27]
	v_mfma_i32_16x16x64_i8 v[12:15], v[142:145], v[206:209], v[12:15]
	v_mfma_i32_16x16x64_i8 v[8:11], v[158:161], v[206:209], v[8:11]
	v_mfma_i32_16x16x64_i8 v[60:63], v[146:149], v[186:189], v[60:63]
	v_mfma_i32_16x16x64_i8 v[56:59], v[162:165], v[186:189], v[56:59]
	v_mfma_i32_16x16x64_i8 v[44:47], v[146:149], v[194:197], v[44:47]
	v_mfma_i32_16x16x64_i8 v[40:43], v[162:165], v[194:197], v[40:43]
	v_mfma_i32_16x16x64_i8 v[28:31], v[146:149], v[202:205], v[28:31]
	v_mfma_i32_16x16x64_i8 v[24:27], v[162:165], v[202:205], v[24:27]
	v_mfma_i32_16x16x64_i8 v[12:15], v[146:149], v[210:213], v[12:15]
	v_mfma_i32_16x16x64_i8 v[8:11], v[162:165], v[210:213], v[8:11]
	v_mfma_i32_16x16x64_i8 v[52:55], v[166:169], v[182:185], v[52:55]
	v_mfma_i32_16x16x64_i8 v[48:51], v[174:177], v[182:185], v[48:51]
	v_mfma_i32_16x16x64_i8 v[36:39], v[166:169], v[190:193], v[36:39]
	v_mfma_i32_16x16x64_i8 v[32:35], v[174:177], v[190:193], v[32:35]
	v_mfma_i32_16x16x64_i8 v[20:23], v[166:169], v[198:201], v[20:23]
	v_mfma_i32_16x16x64_i8 v[16:19], v[174:177], v[198:201], v[16:19]
	v_mfma_i32_16x16x64_i8 v[4:7], v[166:169], v[206:209], v[4:7]
	v_mfma_i32_16x16x64_i8 v[0:3], v[174:177], v[206:209], v[0:3]
	v_mfma_i32_16x16x64_i8 v[52:55], v[170:173], v[186:189], v[52:55]
	v_mfma_i32_16x16x64_i8 v[48:51], v[178:181], v[186:189], v[48:51]
	v_mfma_i32_16x16x64_i8 v[36:39], v[170:173], v[194:197], v[36:39]
	v_mfma_i32_16x16x64_i8 v[32:35], v[178:181], v[194:197], v[32:35]
	v_mfma_i32_16x16x64_i8 v[20:23], v[170:173], v[202:205], v[20:23]
	v_mfma_i32_16x16x64_i8 v[16:19], v[178:181], v[202:205], v[16:19]
	v_mfma_i32_16x16x64_i8 v[4:7], v[170:173], v[210:213], v[4:7]
	v_mfma_i32_16x16x64_i8 v[0:3], v[178:181], v[210:213], v[0:3]
	s_barrier
	s_add_i32 s64, s64, 2
	s_add_u32 s30, s30, 0x100
	s_addc_u32 s31, s31, 0
	s_add_u32 s62, s62, 0x100
	s_addc_u32 s63, s63, 0
	s_cmp_gt_u32 s64, 5
	s_cbranch_scc0 .LBB0_591
	s_and_b64 vcc, exec, s[12:13]
	s_cbranch_vccz .LBB0_594
	s_barrier

; #define PG8_LDA(dst, b, h) do { _Pragma("unroll") for (int m = 0; m < 4; ++m) _Pragma("unroll") for (int k = 0; k < 2; ++k) dst[m][k] = *(const PG8_LAS bf16x8*)(lds + PG8_SA(b, h) + aoff + m * 2048 + k * 1024); } while (0)
; #define PG8_LDB(dst, b, h) do { _Pragma("unroll") for (int n = 0; n < 2; ++n) _Pragma("unroll") for (int k = 0; k < 2; ++k) dst[n][k] = *(const PG8_LAS bf16x8*)(lds + PG8_SB(b, h) + boff + n * 2048 + k * 1024); } while (0)
; #define PG8_WAIT_V(n) asm volatile("s_waitcnt vmcnt(" #n ")" ::: "memory")
; #define PG8_WAIT_L(n) asm volatile("s_waitcnt lgkmcnt(" #n ")" ::: "memory")
; #define PG8_BAR __builtin_amdgcn_s_barrier()
; #define PG8_SCHED __builtin_amdgcn_sched_barrier(0)
; template <class Epi, class Sched, bool ALIGN_EPI = false, bool SP2 = false, bool F8 = false, bool I8 = false, bool PF = false>
; __device__ __forceinline__ void gemm_phase(PG8_LAS unsigned char* lds, const Gemm g, const Sched& S, const Epi& E, const int wave_) {
;     ...
;             PG8_LDB(B0, 0, 0); PG8_LDB(B1, 0, 1); PG8_SCHED; PG8_LDA(At, 0, 0); PG8_STAGE(PG8_SA(1, 1), a1 + hstep, voffA);
;             PG8_WAIT_V(8); PG8_WAIT_L(0); PG8_BAR; PG8_MMA(0, 0, At, B0); PG8_MMA(0, 1, At, B1); PG8_BAR; PG8_SCHED;
;             PG8_LDA(At, 0, 1); PG8_STAGE(PG8_SB(0, 0), b2, voffB); PG8_STAGE(PG8_SB(0, 1), b2 + hstep, voffB); PG8_STAGE(PG8_SA(0, 0), a2, voffA);
;             PG8_WAIT_V(8); PG8_WAIT_L(0); PG8_BAR; PG8_MMA(1, 0, At, B0); PG8_MMA(1, 1, At, B1); PG8_BAR; PG8_SCHED;
.LBB0_671:
	ds_read_b128 v[24:27], v209
	ds_read_b128 v[28:31], v209 offset:1024
	ds_read_b128 v[16:19], v209 offset:2048
	ds_read_b128 v[20:23], v209 offset:3072
	ds_read_b128 v[8:11], v210
	ds_read_b128 v[12:15], v210 offset:1024
	ds_read_b128 v[0:3], v210 offset:2048
	ds_read_b128 v[4:7], v210 offset:3072
	s_add_u32 s28, s30, 0x100
	s_addc_u32 s29, s31, 0
	s_cmp_eq_u32 s65, 18
	s_cselect_b32 s37, s23, s29
	s_cselect_b32 s36, s22, s28
	s_cselect_b32 s35, s27, s64
	s_cselect_b32 s34, s26, s63
	v_lshl_add_u64 v[160:161], s[30:31], 0, v[172:173]
	s_add_i32 m0, s40, 0xc000
	ds_read_b128 v[178:181], v211
	ds_read_b128 v[182:185], v211 offset:1024
	ds_read_b128 v[186:189], v211 offset:2048
	ds_read_b128 v[190:193], v211 offset:3072
	ds_read_b128 v[194:197], v211 offset:4096
	ds_read_b128 v[198:201], v211 offset:5120
	ds_read_b128 v[212:215], v211 offset:6144
	ds_read_b128 v[216:219], v211 offset:7168
	global_load_lds_dwordx4 v[160:161], off
	v_lshl_add_u64 v[160:161], s[30:31], 0, v[174:175]
	s_add_i32 m0, s40, 0xe000
	s_nop 0
	global_load_lds_dwordx4 v[160:161], off
	s_waitcnt vmcnt(8)
	s_waitcnt lgkmcnt(0)
	s_barrier
	s_waitcnt lgkmcnt(0)
	v_mfma_f32_16x16x128_f8f6f4 v[156:159], v[24:31], v[178:185], v[156:159]
	v_mfma_f32_16x16x128_f8f6f4 v[152:155], v[16:23], v[178:185], v[152:155]
	v_mfma_f32_16x16x128_f8f6f4 v[140:143], v[24:31], v[186:193], v[140:143]
	v_mfma_f32_16x16x128_f8f6f4 v[136:139], v[16:23], v[186:193], v[136:139]
	v_mfma_f32_16x16x128_f8f6f4 v[124:127], v[24:31], v[194:201], v[124:127]
	v_mfma_f32_16x16x128_f8f6f4 v[120:123], v[16:23], v[194:201], v[120:123]
	v_mfma_f32_16x16x128_f8f6f4 v[108:111], v[24:31], v[212:219], v[108:111]
	v_mfma_f32_16x16x128_f8f6f4 v[104:107], v[16:23], v[212:219], v[104:107]
	v_mfma_f32_16x16x128_f8f6f4 v[148:151], v[8:15], v[178:185], v[148:151]
	v_mfma_f32_16x16x128_f8f6f4 v[144:147], v[0:7], v[178:185], v[144:147]
	v_mfma_f32_16x16x128_f8f6f4 v[132:135], v[8:15], v[186:193], v[132:135]
	v_mfma_f32_16x16x128_f8f6f4 v[128:131], v[0:7], v[186:193], v[128:131]
	v_mfma_f32_16x16x128_f8f6f4 v[116:119], v[8:15], v[194:201], v[116:119]
	v_mfma_f32_16x16x128_f8f6f4 v[112:115], v[0:7], v[194:201], v[112:115]
	v_mfma_f32_16x16x128_f8f6f4 v[100:103], v[8:15], v[212:219], v[100:103]
	v_mfma_f32_16x16x128_f8f6f4 v[96:99], v[0:7], v[212:219], v[96:99]
	s_barrier
	s_add_i32 s30, s53, s39
	v_lshl_add_u64 v[160:161], s[34:35], 0, v[168:169]
	s_mov_b32 m0, s30
	ds_read_b128 v[182:185], v211 offset:16384
	global_load_lds_dwordx4 v[160:161], off
	ds_read_b128 v[186:189], v211 offset:17408
	s_add_i32 m0, s30, 0x2000
	s_add_u32 s30, s34, 0x58000
	v_lshl_add_u64 v[162:163], s[34:35], 0, v[164:165]
	s_addc_u32 s31, s35, 0
	s_add_i32 s66, s54, s39
	global_load_lds_dwordx4 v[162:163], off
	ds_read_b128 v[190:193], v211 offset:18432
	v_lshl_add_u64 v[178:179], s[30:31], 0, v[168:169]
	s_mov_b32 m0, s66
	v_lshl_add_u64 v[180:181], s[36:37], 0, v[166:167]
	global_load_lds_dwordx4 v[178:179], off
	ds_read_b128 v[194:197], v211 offset:19456
	v_lshl_add_u64 v[178:179], s[30:31], 0, v[164:165]
	s_add_i32 m0, s66, 0x2000
	ds_read_b128 v[198:201], v211 offset:20480
	global_load_lds_dwordx4 v[178:179], off
	ds_read_b128 v[202:205], v211 offset:21504
	v_lshl_add_u64 v[178:179], s[36:37], 0, v[170:171]
	s_mov_b32 m0, s40
	ds_read_b128 v[212:215], v211 offset:22528
	global_load_lds_dwordx4 v[178:179], off
	ds_read_b128 v[216:219], v211 offset:23552
	s_mov_b32 m0, s41
	s_nop 0
	global_load_lds_dwordx4 v[180:181], off
	s_waitcnt vmcnt(8)
	s_waitcnt lgkmcnt(0)
	s_barrier
	s_waitcnt lgkmcnt(0)
	v_mfma_f32_16x16x128_f8f6f4 v[92:95], v[24:31], v[182:189], v[92:95]
	v_mfma_f32_16x16x128_f8f6f4 v[88:91], v[16:23], v[182:189], v[88:91]
	v_mfma_f32_16x16x128_f8f6f4 v[76:79], v[24:31], v[190:197], v[76:79]
	v_mfma_f32_16x16x128_f8f6f4 v[72:75], v[16:23], v[190:197], v[72:75]
	v_mfma_f32_16x16x128_f8f6f4 v[60:63], v[24:31], v[198:205], v[60:63]
	v_mfma_f32_16x16x128_f8f6f4 v[56:59], v[16:23], v[198:205], v[56:59]
	v_mfma_f32_16x16x128_f8f6f4 v[44:47], v[24:31], v[212:219], v[44:47]
	v_mfma_f32_16x16x128_f8f6f4 v[40:43], v[16:23], v[212:219], v[40:43]
	v_mfma_f32_16x16x128_f8f6f4 v[84:87], v[8:15], v[182:189], v[84:87]
	v_mfma_f32_16x16x128_f8f6f4 v[80:83], v[0:7], v[182:189], v[80:83]
	v_mfma_f32_16x16x128_f8f6f4 v[68:71], v[8:15], v[190:197], v[68:71]
	v_mfma_f32_16x16x128_f8f6f4 v[64:67], v[0:7], v[190:197], v[64:67]
	v_mfma_f32_16x16x128_f8f6f4 v[52:55], v[8:15], v[198:205], v[52:55]
	v_mfma_f32_16x16x128_f8f6f4 v[48:51], v[0:7], v[198:205], v[48:51]
	v_mfma_f32_16x16x128_f8f6f4 v[36:39], v[8:15], v[212:219], v[36:39]
	v_mfma_f32_16x16x128_f8f6f4 v[32:35], v[0:7], v[212:219], v[32:35]
	s_barrier
; #define PG8_LDA(dst, b, h) do { _Pragma("unroll") for (int m = 0; m < 4; ++m) _Pragma("unroll") for (int k = 0; k < 2; ++k) dst[m][k] = *(const PG8_LAS bf16x8*)(lds + PG8_SA(b, h) + aoff + m * 2048 + k * 1024); } while (0)
; #define PG8_LDB(dst, b, h) do { _Pragma("unroll") for (int n = 0; n < 2; ++n) _Pragma("unroll") for (int k = 0; k < 2; ++k) dst[n][k] = *(const PG8_LAS bf16x8*)(lds + PG8_SB(b, h) + boff + n * 2048 + k * 1024); } while (0)
; #define PG8_WAIT_V(n) asm volatile("s_waitcnt vmcnt(" #n ")" ::: "memory")
; #define PG8_WAIT_L(n) asm volatile("s_waitcnt lgkmcnt(" #n ")" ::: "memory")
; #define PG8_BAR __builtin_amdgcn_s_barrier()
; #define PG8_SCHED __builtin_amdgcn_sched_barrier(0)
; template <class Epi, class Sched, bool ALIGN_EPI = false, bool SP2 = false, bool F8 = false, bool I8 = false, bool PF = false>
; __device__ __forceinline__ void gemm_phase(PG8_LAS unsigned char* lds, const Gemm g, const Sched& S, const Epi& E, const int wave_) {
;     ...
;             PG8_LDB(B0, 1, 0); PG8_LDB(B1, 1, 1); PG8_SCHED; PG8_LDA(At, 1, 0); PG8_STAGE(PG8_SA(0, 1), a2 + hstep, voffA);
;             PG8_WAIT_V(8); PG8_WAIT_L(0); PG8_BAR; PG8_MMA(0, 0, At, B0); PG8_MMA(0, 1, At, B1); PG8_BAR; PG8_SCHED;
;             PG8_LDA(At, 1, 1); PG8_STAGE(PG8_SB(1, 0), b3, voffB); PG8_STAGE(PG8_SB(1, 1), b3 + hstep, voffB); PG8_STAGE(PG8_SA(1, 0), a3, voffA);
;             PG8_WAIT_V(8); PG8_WAIT_L(0); PG8_BAR; PG8_MMA(1, 0, At, B0); PG8_MMA(1, 1, At, B1); PG8_BAR; PG8_SCHED;
	s_add_i32 s66, 0, 0x18000
	s_add_i32 s67, 0, 0x1c000
	v_add_u32_e32 v12, s66, v208
	v_add_u32_e32 v28, s67, v208
	ds_read_b128 v[0:3], v12
	ds_read_b128 v[4:7], v12 offset:1024
	ds_read_b128 v[8:11], v12 offset:2048
	ds_read_b128 v[12:15], v12 offset:3072
	ds_read_b128 v[16:19], v28
	ds_read_b128 v[20:23], v28 offset:1024
	ds_read_b128 v[24:27], v28 offset:2048
	ds_read_b128 v[28:31], v28 offset:3072
	s_add_u32 s30, s36, 0x58000
	s_addc_u32 s31, s37, 0
	s_mov_b32 m0, s42
	v_lshl_add_u64 v[206:207], s[30:31], 0, v[170:171]
	ds_read_b128 v[182:185], v211 offset:32768
	ds_read_b128 v[186:189], v211 offset:33792
	ds_read_b128 v[190:193], v211 offset:34816
	ds_read_b128 v[194:197], v211 offset:35840
	ds_read_b128 v[198:201], v211 offset:36864
	ds_read_b128 v[202:205], v211 offset:37888
	ds_read_b128 v[212:215], v211 offset:38912
	ds_read_b128 v[216:219], v211 offset:39936
	global_load_lds_dwordx4 v[206:207], off
	v_lshl_add_u64 v[206:207], s[30:31], 0, v[166:167]
	s_mov_b32 m0, s43
	s_nop 0
	global_load_lds_dwordx4 v[206:207], off
	s_waitcnt vmcnt(8)
	s_waitcnt lgkmcnt(0)
	s_barrier
	s_waitcnt lgkmcnt(0)
	v_mfma_f32_16x16x128_f8f6f4 v[156:159], v[0:7], v[182:189], v[156:159]
	v_mfma_f32_16x16x128_f8f6f4 v[152:155], v[8:15], v[182:189], v[152:155]
	v_mfma_f32_16x16x128_f8f6f4 v[140:143], v[0:7], v[190:197], v[140:143]
	v_mfma_f32_16x16x128_f8f6f4 v[136:139], v[8:15], v[190:197], v[136:139]
	v_mfma_f32_16x16x128_f8f6f4 v[124:127], v[0:7], v[198:205], v[124:127]
	v_mfma_f32_16x16x128_f8f6f4 v[120:123], v[8:15], v[198:205], v[120:123]
	v_mfma_f32_16x16x128_f8f6f4 v[108:111], v[0:7], v[212:219], v[108:111]
	v_mfma_f32_16x16x128_f8f6f4 v[104:107], v[8:15], v[212:219], v[104:107]
	v_mfma_f32_16x16x128_f8f6f4 v[148:151], v[16:23], v[182:189], v[148:151]
	v_mfma_f32_16x16x128_f8f6f4 v[144:147], v[24:31], v[182:189], v[144:147]
	v_mfma_f32_16x16x128_f8f6f4 v[132:135], v[16:23], v[190:197], v[132:135]
	v_mfma_f32_16x16x128_f8f6f4 v[128:131], v[24:31], v[190:197], v[128:131]
	v_mfma_f32_16x16x128_f8f6f4 v[116:119], v[16:23], v[198:205], v[116:119]
	v_mfma_f32_16x16x128_f8f6f4 v[112:115], v[24:31], v[198:205], v[112:115]
	v_mfma_f32_16x16x128_f8f6f4 v[100:103], v[16:23], v[212:219], v[100:103]
	v_mfma_f32_16x16x128_f8f6f4 v[96:99], v[24:31], v[212:219], v[96:99]
	s_barrier
	s_add_i32 s30, s66, s39
	v_lshl_add_u64 v[160:161], v[160:161], 0, s[10:11]
	s_mov_b32 m0, s30
	ds_read_b128 v[182:185], v211 offset:49152
	global_load_lds_dwordx4 v[160:161], off
	ds_read_b128 v[186:189], v211 offset:50176
	s_add_i32 m0, s30, 0x2000
	s_add_u32 s30, s34, 0x58080
	v_lshl_add_u64 v[160:161], v[162:163], 0, s[10:11]
	s_addc_u32 s31, s35, 0
	s_add_i32 s34, s67, s39
	global_load_lds_dwordx4 v[160:161], off
	ds_read_b128 v[190:193], v211 offset:51200
	v_lshl_add_u64 v[160:161], s[30:31], 0, v[168:169]
	s_mov_b32 m0, s34
	ds_read_b128 v[194:197], v211 offset:52224
	global_load_lds_dwordx4 v[160:161], off
	ds_read_b128 v[198:201], v211 offset:53248
	v_lshl_add_u64 v[160:161], s[30:31], 0, v[164:165]
	s_add_i32 m0, s34, 0x2000
	ds_read_b128 v[202:205], v211 offset:54272
	global_load_lds_dwordx4 v[160:161], off
	ds_read_b128 v[212:215], v211 offset:55296
	v_lshl_add_u64 v[160:161], v[178:179], 0, s[10:11]
	s_mov_b32 m0, s50
	ds_read_b128 v[216:219], v211 offset:56320
	global_load_lds_dwordx4 v[160:161], off
	v_lshl_add_u64 v[160:161], v[180:181], 0, s[10:11]
	s_mov_b32 m0, s51
	s_nop 0
	global_load_lds_dwordx4 v[160:161], off
	s_waitcnt vmcnt(8)
	s_waitcnt lgkmcnt(0)
	s_barrier
	s_waitcnt lgkmcnt(0)
	v_mfma_f32_16x16x128_f8f6f4 v[92:95], v[0:7], v[182:189], v[92:95]
	v_mfma_f32_16x16x128_f8f6f4 v[88:91], v[8:15], v[182:189], v[88:91]
	v_mfma_f32_16x16x128_f8f6f4 v[76:79], v[0:7], v[190:197], v[76:79]
	v_mfma_f32_16x16x128_f8f6f4 v[72:75], v[8:15], v[190:197], v[72:75]
	v_mfma_f32_16x16x128_f8f6f4 v[60:63], v[0:7], v[198:205], v[60:63]
	v_mfma_f32_16x16x128_f8f6f4 v[56:59], v[8:15], v[198:205], v[56:59]
	v_mfma_f32_16x16x128_f8f6f4 v[44:47], v[0:7], v[212:219], v[44:47]
	v_mfma_f32_16x16x128_f8f6f4 v[40:43], v[8:15], v[212:219], v[40:43]
	v_mfma_f32_16x16x128_f8f6f4 v[84:87], v[16:23], v[182:189], v[84:87]
	v_mfma_f32_16x16x128_f8f6f4 v[80:83], v[24:31], v[182:189], v[80:83]
	v_mfma_f32_16x16x128_f8f6f4 v[68:71], v[16:23], v[190:197], v[68:71]
	v_mfma_f32_16x16x128_f8f6f4 v[64:67], v[24:31], v[190:197], v[64:67]
	v_mfma_f32_16x16x128_f8f6f4 v[52:55], v[16:23], v[198:205], v[52:55]
	v_mfma_f32_16x16x128_f8f6f4 v[48:51], v[24:31], v[198:205], v[48:51]
	v_mfma_f32_16x16x128_f8f6f4 v[36:39], v[16:23], v[212:219], v[36:39]
	v_mfma_f32_16x16x128_f8f6f4 v[32:35], v[24:31], v[212:219], v[32:35]
	s_barrier
	s_add_i32 s65, s65, 2
	s_add_u32 s63, s63, 0x100
	s_addc_u32 s64, s64, 0
	s_cmp_gt_u32 s65, 19
	s_mov_b64 s[30:31], s[28:29]
	s_cbranch_scc0 .LBB0_671
	s_and_b64 vcc, exec, s[12:13]
	s_cbranch_vccz .LBB0_674
	s_barrier

; #define PG8_LDA(dst, b, h) do { _Pragma("unroll") for (int m = 0; m < 4; ++m) _Pragma("unroll") for (int k = 0; k < 2; ++k) dst[m][k] = *(const PG8_LAS bf16x8*)(lds + PG8_SA(b, h) + aoff + m * 2048 + k * 1024); } while (0)
; #define PG8_LDB(dst, b, h) do { _Pragma("unroll") for (int n = 0; n < 2; ++n) _Pragma("unroll") for (int k = 0; k < 2; ++k) dst[n][k] = *(const PG8_LAS bf16x8*)(lds + PG8_SB(b, h) + boff + n * 2048 + k * 1024); } while (0)
; #define PG8_WAIT_V(n) asm volatile("s_waitcnt vmcnt(" #n ")" ::: "memory")
; #define PG8_WAIT_L(n) asm volatile("s_waitcnt lgkmcnt(" #n ")" ::: "memory")
; #define PG8_BAR __builtin_amdgcn_s_barrier()
; #define PG8_SCHED __builtin_amdgcn_sched_barrier(0)
; template <class Epi, class Sched, bool ALIGN_EPI = false, bool SP2 = false, bool F8 = false, bool I8 = false, bool PF = false>
; __device__ __forceinline__ void gemm_phase(PG8_LAS unsigned char* lds, const Gemm g, const Sched& S, const Epi& E, const int wave_) {
;     ...
;             PG8_LDB(B0, 0, 0); PG8_LDB(B1, 0, 1); PG8_SCHED; PG8_LDA(At, 0, 0); PG8_STAGE(PG8_SA(1, 1), a1 + hstep, voffA);
;             PG8_WAIT_V(8); PG8_WAIT_L(0); PG8_BAR; PG8_MMA(0, 0, At, B0); PG8_MMA(0, 1, At, B1); PG8_BAR; PG8_SCHED;
;             PG8_LDA(At, 0, 1); PG8_STAGE(PG8_SB(0, 0), b2, voffB); PG8_STAGE(PG8_SB(0, 1), b2 + hstep, voffB); PG8_STAGE(PG8_SA(0, 0), a2, voffA);
;             PG8_WAIT_V(8); PG8_WAIT_L(0); PG8_BAR; PG8_MMA(1, 0, At, B0); PG8_MMA(1, 1, At, B1); PG8_BAR; PG8_SCHED;
.LBB0_809:
	ds_read_b128 v[142:145], v151
	ds_read_b128 v[156:159], v151 offset:1024
	ds_read_b128 v[160:163], v151 offset:2048
	ds_read_b128 v[164:167], v151 offset:3072
	ds_read_b128 v[168:171], v153
	ds_read_b128 v[172:175], v153 offset:1024
	ds_read_b128 v[176:179], v153 offset:2048
	ds_read_b128 v[180:183], v153 offset:3072
	s_add_u32 s34, s30, 0xfffe0080
	s_addc_u32 s35, s31, -1
	s_cmp_eq_u32 s63, 4
	s_cselect_b32 s37, s19, s35
	s_cselect_b32 s36, s55, s34
	s_cselect_b32 s35, s17, s62
	s_cselect_b32 s34, s56, s57
	v_lshl_add_u64 v[146:147], s[30:31], 0, v[136:137]
	s_add_i32 m0, s29, 0xc000
	ds_read_b128 v[184:187], v155
	ds_read_b128 v[188:191], v155 offset:1024
	ds_read_b128 v[192:195], v155 offset:2048
	ds_read_b128 v[196:199], v155 offset:3072
	ds_read_b128 v[200:203], v155 offset:4096
	ds_read_b128 v[204:207], v155 offset:5120
	ds_read_b128 v[208:211], v155 offset:6144
	ds_read_b128 v[212:215], v155 offset:7168
	global_load_lds_dwordx4 v[146:147], off
	v_lshl_add_u64 v[146:147], s[30:31], 0, v[138:139]
	s_add_i32 m0, s29, 0xe000
	s_nop 0
	global_load_lds_dwordx4 v[146:147], off
	s_waitcnt vmcnt(8)
	s_waitcnt lgkmcnt(0)
	s_barrier
	s_waitcnt lgkmcnt(0)
	v_mfma_i32_16x16x64_i8 v[124:127], v[142:145], v[184:187], v[124:127]
	v_mfma_i32_16x16x64_i8 v[120:123], v[160:163], v[184:187], v[120:123]
	v_mfma_i32_16x16x64_i8 v[108:111], v[142:145], v[192:195], v[108:111]
	v_mfma_i32_16x16x64_i8 v[104:107], v[160:163], v[192:195], v[104:107]
	v_mfma_i32_16x16x64_i8 v[92:95], v[142:145], v[200:203], v[92:95]
	v_mfma_i32_16x16x64_i8 v[88:91], v[160:163], v[200:203], v[88:91]
	v_mfma_i32_16x16x64_i8 v[76:79], v[142:145], v[208:211], v[76:79]
	v_mfma_i32_16x16x64_i8 v[72:75], v[160:163], v[208:211], v[72:75]
	v_mfma_i32_16x16x64_i8 v[124:127], v[156:159], v[188:191], v[124:127]
	v_mfma_i32_16x16x64_i8 v[120:123], v[164:167], v[188:191], v[120:123]
	v_mfma_i32_16x16x64_i8 v[108:111], v[156:159], v[196:199], v[108:111]
	v_mfma_i32_16x16x64_i8 v[104:107], v[164:167], v[196:199], v[104:107]
	v_mfma_i32_16x16x64_i8 v[92:95], v[156:159], v[204:207], v[92:95]
	v_mfma_i32_16x16x64_i8 v[88:91], v[164:167], v[204:207], v[88:91]
	v_mfma_i32_16x16x64_i8 v[76:79], v[156:159], v[212:215], v[76:79]
	v_mfma_i32_16x16x64_i8 v[72:75], v[164:167], v[212:215], v[72:75]
	v_mfma_i32_16x16x64_i8 v[116:119], v[168:171], v[184:187], v[116:119]
	v_mfma_i32_16x16x64_i8 v[112:115], v[176:179], v[184:187], v[112:115]
	v_mfma_i32_16x16x64_i8 v[100:103], v[168:171], v[192:195], v[100:103]
	v_mfma_i32_16x16x64_i8 v[96:99], v[176:179], v[192:195], v[96:99]
	v_mfma_i32_16x16x64_i8 v[84:87], v[168:171], v[200:203], v[84:87]
	v_mfma_i32_16x16x64_i8 v[80:83], v[176:179], v[200:203], v[80:83]
	v_mfma_i32_16x16x64_i8 v[68:71], v[168:171], v[208:211], v[68:71]
	v_mfma_i32_16x16x64_i8 v[64:67], v[176:179], v[208:211], v[64:67]
	v_mfma_i32_16x16x64_i8 v[116:119], v[172:175], v[188:191], v[116:119]
	v_mfma_i32_16x16x64_i8 v[112:115], v[180:183], v[188:191], v[112:115]
	v_mfma_i32_16x16x64_i8 v[100:103], v[172:175], v[196:199], v[100:103]
	v_mfma_i32_16x16x64_i8 v[96:99], v[180:183], v[196:199], v[96:99]
	v_mfma_i32_16x16x64_i8 v[84:87], v[172:175], v[204:207], v[84:87]
	v_mfma_i32_16x16x64_i8 v[80:83], v[180:183], v[204:207], v[80:83]
	v_mfma_i32_16x16x64_i8 v[68:71], v[172:175], v[212:215], v[68:71]
	v_mfma_i32_16x16x64_i8 v[64:67], v[180:183], v[212:215], v[64:67]
	s_barrier
	s_add_i32 s64, s51, s39
	v_lshl_add_u64 v[146:147], s[34:35], 0, v[132:133]
	s_mov_b32 m0, s64
	ds_read_b128 v[184:187], v155 offset:16384
	global_load_lds_dwordx4 v[146:147], off
	ds_read_b128 v[188:191], v155 offset:17408
	s_add_i32 m0, s64, 0x2000
	s_add_u32 s64, s34, 0x20000
	v_lshl_add_u64 v[216:217], s[34:35], 0, v[128:129]
	s_addc_u32 s65, s35, 0
	s_add_i32 s66, s52, s39
	global_load_lds_dwordx4 v[216:217], off
	ds_read_b128 v[192:195], v155 offset:18432
	v_lshl_add_u64 v[218:219], s[64:65], 0, v[132:133]
	s_mov_b32 m0, s66
	v_lshl_add_u64 v[220:221], s[36:37], 0, v[130:131]
	global_load_lds_dwordx4 v[218:219], off
	ds_read_b128 v[196:199], v155 offset:19456
	v_lshl_add_u64 v[218:219], s[64:65], 0, v[128:129]
	s_add_i32 m0, s66, 0x2000
	ds_read_b128 v[200:203], v155 offset:20480
	global_load_lds_dwordx4 v[218:219], off
	ds_read_b128 v[204:207], v155 offset:21504
	v_lshl_add_u64 v[218:219], s[36:37], 0, v[134:135]
	s_mov_b32 m0, s29
	ds_read_b128 v[208:211], v155 offset:22528
	global_load_lds_dwordx4 v[218:219], off
	ds_read_b128 v[212:215], v155 offset:23552
	s_mov_b32 m0, s41
	s_nop 0
	global_load_lds_dwordx4 v[220:221], off
	s_waitcnt vmcnt(8)
	s_waitcnt lgkmcnt(0)
	s_barrier
; #define PG8_LDA(dst, b, h) do { _Pragma("unroll") for (int m = 0; m < 4; ++m) _Pragma("unroll") for (int k = 0; k < 2; ++k) dst[m][k] = *(const PG8_LAS bf16x8*)(lds + PG8_SA(b, h) + aoff + m * 2048 + k * 1024); } while (0)
; #define PG8_LDB(dst, b, h) do { _Pragma("unroll") for (int n = 0; n < 2; ++n) _Pragma("unroll") for (int k = 0; k < 2; ++k) dst[n][k] = *(const PG8_LAS bf16x8*)(lds + PG8_SB(b, h) + boff + n * 2048 + k * 1024); } while (0)
; #define PG8_WAIT_V(n) asm volatile("s_waitcnt vmcnt(" #n ")" ::: "memory")
; #define PG8_WAIT_L(n) asm volatile("s_waitcnt lgkmcnt(" #n ")" ::: "memory")
; #define PG8_BAR __builtin_amdgcn_s_barrier()
; #define PG8_SCHED __builtin_amdgcn_sched_barrier(0)
; template <class Epi, class Sched, bool ALIGN_EPI = false, bool SP2 = false, bool F8 = false, bool I8 = false, bool PF = false>
; __device__ __forceinline__ void gemm_phase(PG8_LAS unsigned char* lds, const Gemm g, const Sched& S, const Epi& E, const int wave_) {
;     ...
;             PG8_WAIT_V(8); PG8_WAIT_L(0); PG8_BAR; PG8_MMA(1, 0, At, B0); PG8_MMA(1, 1, At, B1); PG8_BAR; PG8_SCHED;
;             PG8_LDB(B0, 1, 0); PG8_LDB(B1, 1, 1); PG8_SCHED; PG8_LDA(At, 1, 0); PG8_STAGE(PG8_SA(0, 1), a2 + hstep, voffA);
;             PG8_WAIT_V(8); PG8_WAIT_L(0); PG8_BAR; PG8_MMA(0, 0, At, B0); PG8_MMA(0, 1, At, B1); PG8_BAR; PG8_SCHED;
	s_waitcnt lgkmcnt(0)
	v_mfma_i32_16x16x64_i8 v[60:63], v[142:145], v[184:187], v[60:63]
	v_mfma_i32_16x16x64_i8 v[56:59], v[160:163], v[184:187], v[56:59]
	v_mfma_i32_16x16x64_i8 v[44:47], v[142:145], v[192:195], v[44:47]
	v_mfma_i32_16x16x64_i8 v[40:43], v[160:163], v[192:195], v[40:43]
	v_mfma_i32_16x16x64_i8 v[28:31], v[142:145], v[200:203], v[28:31]
	v_mfma_i32_16x16x64_i8 v[24:27], v[160:163], v[200:203], v[24:27]
	v_mfma_i32_16x16x64_i8 v[12:15], v[142:145], v[208:211], v[12:15]
	v_mfma_i32_16x16x64_i8 v[8:11], v[160:163], v[208:211], v[8:11]
	v_mfma_i32_16x16x64_i8 v[60:63], v[156:159], v[188:191], v[60:63]
	v_mfma_i32_16x16x64_i8 v[56:59], v[164:167], v[188:191], v[56:59]
	v_mfma_i32_16x16x64_i8 v[44:47], v[156:159], v[196:199], v[44:47]
	v_mfma_i32_16x16x64_i8 v[40:43], v[164:167], v[196:199], v[40:43]
	v_mfma_i32_16x16x64_i8 v[28:31], v[156:159], v[204:207], v[28:31]
	v_mfma_i32_16x16x64_i8 v[24:27], v[164:167], v[204:207], v[24:27]
	v_mfma_i32_16x16x64_i8 v[12:15], v[156:159], v[212:215], v[12:15]
	v_mfma_i32_16x16x64_i8 v[8:11], v[164:167], v[212:215], v[8:11]
	v_mfma_i32_16x16x64_i8 v[52:55], v[168:171], v[184:187], v[52:55]
	v_mfma_i32_16x16x64_i8 v[48:51], v[176:179], v[184:187], v[48:51]
	v_mfma_i32_16x16x64_i8 v[36:39], v[168:171], v[192:195], v[36:39]
	v_mfma_i32_16x16x64_i8 v[32:35], v[176:179], v[192:195], v[32:35]
	v_mfma_i32_16x16x64_i8 v[20:23], v[168:171], v[200:203], v[20:23]
	v_mfma_i32_16x16x64_i8 v[16:19], v[176:179], v[200:203], v[16:19]
	v_mfma_i32_16x16x64_i8 v[4:7], v[168:171], v[208:211], v[4:7]
	v_mfma_i32_16x16x64_i8 v[0:3], v[176:179], v[208:211], v[0:3]
	v_mfma_i32_16x16x64_i8 v[52:55], v[172:175], v[188:191], v[52:55]
	v_mfma_i32_16x16x64_i8 v[48:51], v[180:183], v[188:191], v[48:51]
	v_mfma_i32_16x16x64_i8 v[36:39], v[172:175], v[196:199], v[36:39]
	v_mfma_i32_16x16x64_i8 v[32:35], v[180:183], v[196:199], v[32:35]
	v_mfma_i32_16x16x64_i8 v[20:23], v[172:175], v[204:207], v[20:23]
	v_mfma_i32_16x16x64_i8 v[16:19], v[180:183], v[204:207], v[16:19]
	v_mfma_i32_16x16x64_i8 v[4:7], v[172:175], v[212:215], v[4:7]
	v_mfma_i32_16x16x64_i8 v[0:3], v[180:183], v[212:215], v[0:3]
	s_barrier
	s_add_i32 s64, 0, 0x18000
	v_add_u32_e32 v148, s64, v149
	s_add_i32 s65, 0, 0x1c000
	ds_read_b128 v[142:145], v148
	ds_read_b128 v[156:159], v148 offset:1024
	ds_read_b128 v[160:163], v148 offset:2048
	ds_read_b128 v[164:167], v148 offset:3072
	v_add_u32_e32 v148, s65, v149
	ds_read_b128 v[168:171], v148
	ds_read_b128 v[172:175], v148 offset:1024
	ds_read_b128 v[176:179], v148 offset:2048
	ds_read_b128 v[180:183], v148 offset:3072
	s_add_u32 s36, s36, 0x20000
	s_addc_u32 s37, s37, 0
	s_mov_b32 m0, s42
	v_lshl_add_u64 v[222:223], s[36:37], 0, v[134:135]
	ds_read_b128 v[184:187], v155 offset:32768
	ds_read_b128 v[188:191], v155 offset:33792
	ds_read_b128 v[192:195], v155 offset:34816
	ds_read_b128 v[196:199], v155 offset:35840
	ds_read_b128 v[200:203], v155 offset:36864
	ds_read_b128 v[204:207], v155 offset:37888
	ds_read_b128 v[208:211], v155 offset:38912
	ds_read_b128 v[212:215], v155 offset:39936
	global_load_lds_dwordx4 v[222:223], off
	v_lshl_add_u64 v[222:223], s[36:37], 0, v[130:131]
	s_mov_b32 m0, s43
	s_nop 0
	global_load_lds_dwordx4 v[222:223], off
	s_waitcnt vmcnt(8)
	s_waitcnt lgkmcnt(0)
	s_barrier
	s_waitcnt lgkmcnt(0)
	v_mfma_i32_16x16x64_i8 v[124:127], v[142:145], v[184:187], v[124:127]
	v_mfma_i32_16x16x64_i8 v[120:123], v[160:163], v[184:187], v[120:123]
	v_mfma_i32_16x16x64_i8 v[108:111], v[142:145], v[192:195], v[108:111]
	v_mfma_i32_16x16x64_i8 v[104:107], v[160:163], v[192:195], v[104:107]
	v_mfma_i32_16x16x64_i8 v[92:95], v[142:145], v[200:203], v[92:95]
	v_mfma_i32_16x16x64_i8 v[88:91], v[160:163], v[200:203], v[88:91]
	v_mfma_i32_16x16x64_i8 v[76:79], v[142:145], v[208:211], v[76:79]
	v_mfma_i32_16x16x64_i8 v[72:75], v[160:163], v[208:211], v[72:75]
	v_mfma_i32_16x16x64_i8 v[124:127], v[156:159], v[188:191], v[124:127]
	v_mfma_i32_16x16x64_i8 v[120:123], v[164:167], v[188:191], v[120:123]
	v_mfma_i32_16x16x64_i8 v[108:111], v[156:159], v[196:199], v[108:111]
	v_mfma_i32_16x16x64_i8 v[104:107], v[164:167], v[196:199], v[104:107]
	v_mfma_i32_16x16x64_i8 v[92:95], v[156:159], v[204:207], v[92:95]
	v_mfma_i32_16x16x64_i8 v[88:91], v[164:167], v[204:207], v[88:91]
	v_mfma_i32_16x16x64_i8 v[76:79], v[156:159], v[212:215], v[76:79]
	v_mfma_i32_16x16x64_i8 v[72:75], v[164:167], v[212:215], v[72:75]
	v_mfma_i32_16x16x64_i8 v[116:119], v[168:171], v[184:187], v[116:119]
	v_mfma_i32_16x16x64_i8 v[112:115], v[176:179], v[184:187], v[112:115]
	v_mfma_i32_16x16x64_i8 v[100:103], v[168:171], v[192:195], v[100:103]
	v_mfma_i32_16x16x64_i8 v[96:99], v[176:179], v[192:195], v[96:99]
	v_mfma_i32_16x16x64_i8 v[84:87], v[168:171], v[200:203], v[84:87]
	v_mfma_i32_16x16x64_i8 v[80:83], v[176:179], v[200:203], v[80:83]
	v_mfma_i32_16x16x64_i8 v[68:71], v[168:171], v[208:211], v[68:71]
	v_mfma_i32_16x16x64_i8 v[64:67], v[176:179], v[208:211], v[64:67]
	v_mfma_i32_16x16x64_i8 v[116:119], v[172:175], v[188:191], v[116:119]
	v_mfma_i32_16x16x64_i8 v[112:115], v[180:183], v[188:191], v[112:115]
	v_mfma_i32_16x16x64_i8 v[100:103], v[172:175], v[196:199], v[100:103]
	v_mfma_i32_16x16x64_i8 v[96:99], v[180:183], v[196:199], v[96:99]
	v_mfma_i32_16x16x64_i8 v[84:87], v[172:175], v[204:207], v[84:87]
	v_mfma_i32_16x16x64_i8 v[80:83], v[180:183], v[204:207], v[80:83]
	v_mfma_i32_16x16x64_i8 v[68:71], v[172:175], v[212:215], v[68:71]
	v_mfma_i32_16x16x64_i8 v[64:67], v[180:183], v[212:215], v[64:67]
	s_barrier
; #define PG8_LDA(dst, b, h) do { _Pragma("unroll") for (int m = 0; m < 4; ++m) _Pragma("unroll") for (int k = 0; k < 2; ++k) dst[m][k] = *(const PG8_LAS bf16x8*)(lds + PG8_SA(b, h) + aoff + m * 2048 + k * 1024); } while (0)
; #define PG8_WAIT_V(n) asm volatile("s_waitcnt vmcnt(" #n ")" ::: "memory")
; #define PG8_WAIT_L(n) asm volatile("s_waitcnt lgkmcnt(" #n ")" ::: "memory")
; #define PG8_BAR __builtin_amdgcn_s_barrier()
; #define PG8_SCHED __builtin_amdgcn_sched_barrier(0)
; template <class Epi, class Sched, bool ALIGN_EPI = false, bool SP2 = false, bool F8 = false, bool I8 = false, bool PF = false>
; __device__ __forceinline__ void gemm_phase(PG8_LAS unsigned char* lds, const Gemm g, const Sched& S, const Epi& E, const int wave_) {
;     ...
;             PG8_LDA(At, 1, 1); PG8_STAGE(PG8_SB(1, 0), b3, voffB); PG8_STAGE(PG8_SB(1, 1), b3 + hstep, voffB); PG8_STAGE(PG8_SA(1, 0), a3, voffA);
;             PG8_WAIT_V(8); PG8_WAIT_L(0); PG8_BAR; PG8_MMA(1, 0, At, B0); PG8_MMA(1, 1, At, B1); PG8_BAR; PG8_SCHED;
	s_add_i32 s36, s64, s39
	v_lshl_add_u64 v[146:147], v[146:147], 0, s[10:11]
	s_mov_b32 m0, s36
	ds_read_b128 v[184:187], v155 offset:49152
	global_load_lds_dwordx4 v[146:147], off
	ds_read_b128 v[188:191], v155 offset:50176
	s_add_i32 m0, s36, 0x2000
	s_add_u32 s34, s34, 0x20080
	v_lshl_add_u64 v[146:147], v[216:217], 0, s[10:11]
	s_addc_u32 s35, s35, 0
	s_add_i32 s36, s65, s39
	global_load_lds_dwordx4 v[146:147], off
	ds_read_b128 v[192:195], v155 offset:51200
	v_lshl_add_u64 v[146:147], s[34:35], 0, v[132:133]
	s_mov_b32 m0, s36
	ds_read_b128 v[196:199], v155 offset:52224
	global_load_lds_dwordx4 v[146:147], off
	ds_read_b128 v[200:203], v155 offset:53248
	v_lshl_add_u64 v[146:147], s[34:35], 0, v[128:129]
	s_add_i32 m0, s36, 0x2000
	ds_read_b128 v[204:207], v155 offset:54272
	global_load_lds_dwordx4 v[146:147], off
	ds_read_b128 v[208:211], v155 offset:55296
	v_lshl_add_u64 v[146:147], v[218:219], 0, s[10:11]
	s_mov_b32 m0, s48
	ds_read_b128 v[212:215], v155 offset:56320
	global_load_lds_dwordx4 v[146:147], off
	v_lshl_add_u64 v[146:147], v[220:221], 0, s[10:11]
	s_mov_b32 m0, s49
	s_nop 0
	global_load_lds_dwordx4 v[146:147], off
	s_waitcnt vmcnt(8)
	s_waitcnt lgkmcnt(0)
	s_barrier
	s_waitcnt lgkmcnt(0)
	v_mfma_i32_16x16x64_i8 v[60:63], v[142:145], v[184:187], v[60:63]
	v_mfma_i32_16x16x64_i8 v[56:59], v[160:163], v[184:187], v[56:59]
	v_mfma_i32_16x16x64_i8 v[44:47], v[142:145], v[192:195], v[44:47]
	v_mfma_i32_16x16x64_i8 v[40:43], v[160:163], v[192:195], v[40:43]
	v_mfma_i32_16x16x64_i8 v[28:31], v[142:145], v[200:203], v[28:31]
	v_mfma_i32_16x16x64_i8 v[24:27], v[160:163], v[200:203], v[24:27]
	v_mfma_i32_16x16x64_i8 v[12:15], v[142:145], v[208:211], v[12:15]
	v_mfma_i32_16x16x64_i8 v[8:11], v[160:163], v[208:211], v[8:11]
	v_mfma_i32_16x16x64_i8 v[60:63], v[156:159], v[188:191], v[60:63]
	v_mfma_i32_16x16x64_i8 v[56:59], v[164:167], v[188:191], v[56:59]
	v_mfma_i32_16x16x64_i8 v[44:47], v[156:159], v[196:199], v[44:47]
	v_mfma_i32_16x16x64_i8 v[40:43], v[164:167], v[196:199], v[40:43]
	v_mfma_i32_16x16x64_i8 v[28:31], v[156:159], v[204:207], v[28:31]
	v_mfma_i32_16x16x64_i8 v[24:27], v[164:167], v[204:207], v[24:27]
	v_mfma_i32_16x16x64_i8 v[12:15], v[156:159], v[212:215], v[12:15]
	v_mfma_i32_16x16x64_i8 v[8:11], v[164:167], v[212:215], v[8:11]
	v_mfma_i32_16x16x64_i8 v[52:55], v[168:171], v[184:187], v[52:55]
	v_mfma_i32_16x16x64_i8 v[48:51], v[176:179], v[184:187], v[48:51]
	v_mfma_i32_16x16x64_i8 v[36:39], v[168:171], v[192:195], v[36:39]
	v_mfma_i32_16x16x64_i8 v[32:35], v[176:179], v[192:195], v[32:35]
	v_mfma_i32_16x16x64_i8 v[20:23], v[168:171], v[200:203], v[20:23]
	v_mfma_i32_16x16x64_i8 v[16:19], v[176:179], v[200:203], v[16:19]
	v_mfma_i32_16x16x64_i8 v[4:7], v[168:171], v[208:211], v[4:7]
	v_mfma_i32_16x16x64_i8 v[0:3], v[176:179], v[208:211], v[0:3]
	v_mfma_i32_16x16x64_i8 v[52:55], v[172:175], v[188:191], v[52:55]
	v_mfma_i32_16x16x64_i8 v[48:51], v[180:183], v[188:191], v[48:51]
	v_mfma_i32_16x16x64_i8 v[36:39], v[172:175], v[196:199], v[36:39]
	v_mfma_i32_16x16x64_i8 v[32:35], v[180:183], v[196:199], v[32:35]
	v_mfma_i32_16x16x64_i8 v[20:23], v[172:175], v[204:207], v[20:23]
	v_mfma_i32_16x16x64_i8 v[16:19], v[180:183], v[204:207], v[16:19]
	v_mfma_i32_16x16x64_i8 v[4:7], v[172:175], v[212:215], v[4:7]
	v_mfma_i32_16x16x64_i8 v[0:3], v[180:183], v[212:215], v[0:3]
	s_barrier
	s_add_i32 s63, s63, 2
	s_add_u32 s30, s30, 0x100
	s_addc_u32 s31, s31, 0
	s_add_u32 s57, s57, 0x100
	s_addc_u32 s62, s62, 0
	s_cmp_gt_u32 s63, 5
	s_cbranch_scc0 .LBB0_809
	s_and_b64 vcc, exec, s[12:13]
	s_cbranch_vccz .LBB0_812
	s_barrier

; #define PG8_LDA(dst, b, h) do { _Pragma("unroll") for (int m = 0; m < 4; ++m) _Pragma("unroll") for (int k = 0; k < 2; ++k) dst[m][k] = *(const PG8_LAS bf16x8*)(lds + PG8_SA(b, h) + aoff + m * 2048 + k * 1024); } while (0)
; #define PG8_LDB(dst, b, h) do { _Pragma("unroll") for (int n = 0; n < 2; ++n) _Pragma("unroll") for (int k = 0; k < 2; ++k) dst[n][k] = *(const PG8_LAS bf16x8*)(lds + PG8_SB(b, h) + boff + n * 2048 + k * 1024); } while (0)
; #define PG8_WAIT_V(n) asm volatile("s_waitcnt vmcnt(" #n ")" ::: "memory")
; #define PG8_WAIT_L(n) asm volatile("s_waitcnt lgkmcnt(" #n ")" ::: "memory")
; #define PG8_BAR __builtin_amdgcn_s_barrier()
; #define PG8_SCHED __builtin_amdgcn_sched_barrier(0)
; template <class Epi, class Sched, bool ALIGN_EPI = false, bool SP2 = false, bool F8 = false, bool I8 = false, bool PF = false>
; __device__ __forceinline__ void gemm_phase(PG8_LAS unsigned char* lds, const Gemm g, const Sched& S, const Epi& E, const int wave_) {
;     ...
;             PG8_LDB(B0, 0, 0); PG8_LDB(B1, 0, 1); PG8_SCHED; PG8_LDA(At, 0, 0); PG8_STAGE(PG8_SA(1, 1), a1 + hstep, voffA);
;             PG8_WAIT_V(8); PG8_WAIT_L(0); PG8_BAR; PG8_MMA(0, 0, At, B0); PG8_MMA(0, 1, At, B1); PG8_BAR; PG8_SCHED;
;             PG8_LDA(At, 0, 1); PG8_STAGE(PG8_SB(0, 0), b2, voffB); PG8_STAGE(PG8_SB(0, 1), b2 + hstep, voffB); PG8_STAGE(PG8_SA(0, 0), a2, voffA);
;             PG8_WAIT_V(8); PG8_WAIT_L(0); PG8_BAR; PG8_MMA(1, 0, At, B0); PG8_MMA(1, 1, At, B1); PG8_BAR; PG8_SCHED;
.LBB0_967:
	ds_read_b128 v[144:147], v151
	ds_read_b128 v[154:157], v151 offset:1024
	ds_read_b128 v[158:161], v151 offset:2048
	ds_read_b128 v[162:165], v151 offset:3072
	ds_read_b128 v[166:169], v152
	ds_read_b128 v[170:173], v152 offset:1024
	ds_read_b128 v[174:177], v152 offset:2048
	ds_read_b128 v[178:181], v152 offset:3072
	s_add_u32 s40, s38, 0xfffe0080
	s_addc_u32 s41, s39, -1
	s_cmp_eq_u32 s72, 4
	s_cselect_b32 s43, s5, s41
	s_cselect_b32 s42, s27, s40
	s_cselect_b32 s41, s23, s71
	s_cselect_b32 s40, s37, s70
	v_lshl_add_u64 v[148:149], s[38:39], 0, v[138:139]
	s_add_i32 m0, s51, 0xc000
	ds_read_b128 v[182:185], v153
	ds_read_b128 v[186:189], v153 offset:1024
	ds_read_b128 v[190:193], v153 offset:2048
	ds_read_b128 v[194:197], v153 offset:3072
	ds_read_b128 v[198:201], v153 offset:4096
	ds_read_b128 v[202:205], v153 offset:5120
	ds_read_b128 v[206:209], v153 offset:6144
	ds_read_b128 v[210:213], v153 offset:7168
	global_load_lds_dwordx4 v[148:149], off
	v_lshl_add_u64 v[148:149], s[38:39], 0, v[140:141]
	s_add_i32 m0, s51, 0xe000
	s_nop 0
	global_load_lds_dwordx4 v[148:149], off
	s_waitcnt vmcnt(8)
	s_waitcnt lgkmcnt(0)
	s_barrier
	s_waitcnt lgkmcnt(0)
	v_mfma_f32_16x16x32_bf16 v[124:127], v[144:147], v[182:185], v[124:127]
	v_mfma_f32_16x16x32_bf16 v[120:123], v[158:161], v[182:185], v[120:123]
	v_mfma_f32_16x16x32_bf16 v[108:111], v[144:147], v[190:193], v[108:111]
	v_mfma_f32_16x16x32_bf16 v[104:107], v[158:161], v[190:193], v[104:107]
	v_mfma_f32_16x16x32_bf16 v[92:95], v[144:147], v[198:201], v[92:95]
	v_mfma_f32_16x16x32_bf16 v[88:91], v[158:161], v[198:201], v[88:91]
	v_mfma_f32_16x16x32_bf16 v[76:79], v[144:147], v[206:209], v[76:79]
	v_mfma_f32_16x16x32_bf16 v[72:75], v[158:161], v[206:209], v[72:75]
	v_mfma_f32_16x16x32_bf16 v[124:127], v[154:157], v[186:189], v[124:127]
	v_mfma_f32_16x16x32_bf16 v[120:123], v[162:165], v[186:189], v[120:123]
	v_mfma_f32_16x16x32_bf16 v[108:111], v[154:157], v[194:197], v[108:111]
	v_mfma_f32_16x16x32_bf16 v[104:107], v[162:165], v[194:197], v[104:107]
	v_mfma_f32_16x16x32_bf16 v[92:95], v[154:157], v[202:205], v[92:95]
	v_mfma_f32_16x16x32_bf16 v[88:91], v[162:165], v[202:205], v[88:91]
	v_mfma_f32_16x16x32_bf16 v[76:79], v[154:157], v[210:213], v[76:79]
	v_mfma_f32_16x16x32_bf16 v[72:75], v[162:165], v[210:213], v[72:75]
	v_mfma_f32_16x16x32_bf16 v[116:119], v[166:169], v[182:185], v[116:119]
	v_mfma_f32_16x16x32_bf16 v[112:115], v[174:177], v[182:185], v[112:115]
	v_mfma_f32_16x16x32_bf16 v[100:103], v[166:169], v[190:193], v[100:103]
	v_mfma_f32_16x16x32_bf16 v[96:99], v[174:177], v[190:193], v[96:99]
	v_mfma_f32_16x16x32_bf16 v[84:87], v[166:169], v[198:201], v[84:87]
	v_mfma_f32_16x16x32_bf16 v[80:83], v[174:177], v[198:201], v[80:83]
	v_mfma_f32_16x16x32_bf16 v[68:71], v[166:169], v[206:209], v[68:71]
	v_mfma_f32_16x16x32_bf16 v[64:67], v[174:177], v[206:209], v[64:67]
	v_mfma_f32_16x16x32_bf16 v[116:119], v[170:173], v[186:189], v[116:119]
	v_mfma_f32_16x16x32_bf16 v[112:115], v[178:181], v[186:189], v[112:115]
	v_mfma_f32_16x16x32_bf16 v[100:103], v[170:173], v[194:197], v[100:103]
	v_mfma_f32_16x16x32_bf16 v[96:99], v[178:181], v[194:197], v[96:99]
	v_mfma_f32_16x16x32_bf16 v[84:87], v[170:173], v[202:205], v[84:87]
	v_mfma_f32_16x16x32_bf16 v[80:83], v[178:181], v[202:205], v[80:83]
	v_mfma_f32_16x16x32_bf16 v[68:71], v[170:173], v[210:213], v[68:71]
	v_mfma_f32_16x16x32_bf16 v[64:67], v[178:181], v[210:213], v[64:67]
	s_barrier
	s_add_i32 s73, s67, s48
	v_lshl_add_u64 v[148:149], s[40:41], 0, v[130:131]
	s_mov_b32 m0, s73
	ds_read_b128 v[182:185], v153 offset:16384
	global_load_lds_dwordx4 v[148:149], off
	ds_read_b128 v[186:189], v153 offset:17408
	s_add_i32 m0, s73, 0x2000
	s_add_u32 s74, s40, 0x20000
	v_lshl_add_u64 v[214:215], s[40:41], 0, v[134:135]
	s_addc_u32 s75, s41, 0
	s_add_i32 s73, s68, s48
	global_load_lds_dwordx4 v[214:215], off
	ds_read_b128 v[190:193], v153 offset:18432
	v_lshl_add_u64 v[216:217], s[74:75], 0, v[130:131]
	s_mov_b32 m0, s73
	v_lshl_add_u64 v[218:219], s[42:43], 0, v[132:133]
	global_load_lds_dwordx4 v[216:217], off
	ds_read_b128 v[194:197], v153 offset:19456
	v_lshl_add_u64 v[216:217], s[74:75], 0, v[134:135]
	s_add_i32 m0, s73, 0x2000
	ds_read_b128 v[198:201], v153 offset:20480
	global_load_lds_dwordx4 v[216:217], off
	ds_read_b128 v[202:205], v153 offset:21504
	v_lshl_add_u64 v[216:217], s[42:43], 0, v[128:129]
	s_mov_b32 m0, s51
	ds_read_b128 v[206:209], v153 offset:22528
	global_load_lds_dwordx4 v[216:217], off
	ds_read_b128 v[210:213], v153 offset:23552
	s_mov_b32 m0, s52
	s_nop 0
	global_load_lds_dwordx4 v[218:219], off
	s_waitcnt vmcnt(8)
	s_waitcnt lgkmcnt(0)
	s_barrier
; #define PG8_LDA(dst, b, h) do { _Pragma("unroll") for (int m = 0; m < 4; ++m) _Pragma("unroll") for (int k = 0; k < 2; ++k) dst[m][k] = *(const PG8_LAS bf16x8*)(lds + PG8_SA(b, h) + aoff + m * 2048 + k * 1024); } while (0)
; #define PG8_LDB(dst, b, h) do { _Pragma("unroll") for (int n = 0; n < 2; ++n) _Pragma("unroll") for (int k = 0; k < 2; ++k) dst[n][k] = *(const PG8_LAS bf16x8*)(lds + PG8_SB(b, h) + boff + n * 2048 + k * 1024); } while (0)
; #define PG8_WAIT_V(n) asm volatile("s_waitcnt vmcnt(" #n ")" ::: "memory")
; #define PG8_WAIT_L(n) asm volatile("s_waitcnt lgkmcnt(" #n ")" ::: "memory")
; #define PG8_BAR __builtin_amdgcn_s_barrier()
; #define PG8_SCHED __builtin_amdgcn_sched_barrier(0)
; template <class Epi, class Sched, bool ALIGN_EPI = false, bool SP2 = false, bool F8 = false, bool I8 = false, bool PF = false>
; __device__ __forceinline__ void gemm_phase(PG8_LAS unsigned char* lds, const Gemm g, const Sched& S, const Epi& E, const int wave_) {
;     ...
;             PG8_WAIT_V(8); PG8_WAIT_L(0); PG8_BAR; PG8_MMA(1, 0, At, B0); PG8_MMA(1, 1, At, B1); PG8_BAR; PG8_SCHED;
;             PG8_LDB(B0, 1, 0); PG8_LDB(B1, 1, 1); PG8_SCHED; PG8_LDA(At, 1, 0); PG8_STAGE(PG8_SA(0, 1), a2 + hstep, voffA);
;             PG8_WAIT_V(8); PG8_WAIT_L(0); PG8_BAR; PG8_MMA(0, 0, At, B0); PG8_MMA(0, 1, At, B1); PG8_BAR; PG8_SCHED;
	s_waitcnt lgkmcnt(0)
	v_mfma_f32_16x16x32_bf16 v[60:63], v[144:147], v[182:185], v[60:63]
	v_mfma_f32_16x16x32_bf16 v[56:59], v[158:161], v[182:185], v[56:59]
	v_mfma_f32_16x16x32_bf16 v[44:47], v[144:147], v[190:193], v[44:47]
	v_mfma_f32_16x16x32_bf16 v[40:43], v[158:161], v[190:193], v[40:43]
	v_mfma_f32_16x16x32_bf16 v[28:31], v[144:147], v[198:201], v[28:31]
	v_mfma_f32_16x16x32_bf16 v[24:27], v[158:161], v[198:201], v[24:27]
	v_mfma_f32_16x16x32_bf16 v[12:15], v[144:147], v[206:209], v[12:15]
	v_mfma_f32_16x16x32_bf16 v[8:11], v[158:161], v[206:209], v[8:11]
	v_mfma_f32_16x16x32_bf16 v[60:63], v[154:157], v[186:189], v[60:63]
	v_mfma_f32_16x16x32_bf16 v[56:59], v[162:165], v[186:189], v[56:59]
	v_mfma_f32_16x16x32_bf16 v[44:47], v[154:157], v[194:197], v[44:47]
	v_mfma_f32_16x16x32_bf16 v[40:43], v[162:165], v[194:197], v[40:43]
	v_mfma_f32_16x16x32_bf16 v[28:31], v[154:157], v[202:205], v[28:31]
	v_mfma_f32_16x16x32_bf16 v[24:27], v[162:165], v[202:205], v[24:27]
	v_mfma_f32_16x16x32_bf16 v[12:15], v[154:157], v[210:213], v[12:15]
	v_mfma_f32_16x16x32_bf16 v[8:11], v[162:165], v[210:213], v[8:11]
	v_mfma_f32_16x16x32_bf16 v[52:55], v[166:169], v[182:185], v[52:55]
	v_mfma_f32_16x16x32_bf16 v[48:51], v[174:177], v[182:185], v[48:51]
	v_mfma_f32_16x16x32_bf16 v[36:39], v[166:169], v[190:193], v[36:39]
	v_mfma_f32_16x16x32_bf16 v[32:35], v[174:177], v[190:193], v[32:35]
	v_mfma_f32_16x16x32_bf16 v[20:23], v[166:169], v[198:201], v[20:23]
	v_mfma_f32_16x16x32_bf16 v[16:19], v[174:177], v[198:201], v[16:19]
	v_mfma_f32_16x16x32_bf16 v[4:7], v[166:169], v[206:209], v[4:7]
	v_mfma_f32_16x16x32_bf16 v[0:3], v[174:177], v[206:209], v[0:3]
	v_mfma_f32_16x16x32_bf16 v[52:55], v[170:173], v[186:189], v[52:55]
	v_mfma_f32_16x16x32_bf16 v[48:51], v[178:181], v[186:189], v[48:51]
	v_mfma_f32_16x16x32_bf16 v[36:39], v[170:173], v[194:197], v[36:39]
	v_mfma_f32_16x16x32_bf16 v[32:35], v[178:181], v[194:197], v[32:35]
	v_mfma_f32_16x16x32_bf16 v[20:23], v[170:173], v[202:205], v[20:23]
	v_mfma_f32_16x16x32_bf16 v[16:19], v[178:181], v[202:205], v[16:19]
	v_mfma_f32_16x16x32_bf16 v[4:7], v[170:173], v[210:213], v[4:7]
	v_mfma_f32_16x16x32_bf16 v[0:3], v[178:181], v[210:213], v[0:3]
	s_barrier
	s_add_i32 s73, 0, 0x18000
	v_add_u32_e32 v136, s73, v150
	s_add_i32 s74, 0, 0x1c000
	ds_read_b128 v[144:147], v136
	ds_read_b128 v[154:157], v136 offset:1024
	ds_read_b128 v[158:161], v136 offset:2048
	ds_read_b128 v[162:165], v136 offset:3072
	v_add_u32_e32 v136, s74, v150
	ds_read_b128 v[166:169], v136
	ds_read_b128 v[170:173], v136 offset:1024
	ds_read_b128 v[174:177], v136 offset:2048
	ds_read_b128 v[178:181], v136 offset:3072
	s_add_u32 s42, s42, 0x20000
	s_addc_u32 s43, s43, 0
	s_mov_b32 m0, s53
	v_lshl_add_u64 v[220:221], s[42:43], 0, v[128:129]
	ds_read_b128 v[182:185], v153 offset:32768
	ds_read_b128 v[186:189], v153 offset:33792
	ds_read_b128 v[190:193], v153 offset:34816
	ds_read_b128 v[194:197], v153 offset:35840
	ds_read_b128 v[198:201], v153 offset:36864
	ds_read_b128 v[202:205], v153 offset:37888
	ds_read_b128 v[206:209], v153 offset:38912
	ds_read_b128 v[210:213], v153 offset:39936
	global_load_lds_dwordx4 v[220:221], off
	v_lshl_add_u64 v[220:221], s[42:43], 0, v[132:133]
	s_mov_b32 m0, s54
	s_nop 0
	global_load_lds_dwordx4 v[220:221], off
	s_waitcnt vmcnt(8)
	s_waitcnt lgkmcnt(0)
	s_barrier
	s_waitcnt lgkmcnt(0)
	v_mfma_f32_16x16x32_bf16 v[124:127], v[144:147], v[182:185], v[124:127]
	v_mfma_f32_16x16x32_bf16 v[120:123], v[158:161], v[182:185], v[120:123]
	v_mfma_f32_16x16x32_bf16 v[108:111], v[144:147], v[190:193], v[108:111]
	v_mfma_f32_16x16x32_bf16 v[104:107], v[158:161], v[190:193], v[104:107]
	v_mfma_f32_16x16x32_bf16 v[92:95], v[144:147], v[198:201], v[92:95]
	v_mfma_f32_16x16x32_bf16 v[88:91], v[158:161], v[198:201], v[88:91]
	v_mfma_f32_16x16x32_bf16 v[76:79], v[144:147], v[206:209], v[76:79]
	v_mfma_f32_16x16x32_bf16 v[72:75], v[158:161], v[206:209], v[72:75]
	v_mfma_f32_16x16x32_bf16 v[124:127], v[154:157], v[186:189], v[124:127]
	v_mfma_f32_16x16x32_bf16 v[120:123], v[162:165], v[186:189], v[120:123]
	v_mfma_f32_16x16x32_bf16 v[108:111], v[154:157], v[194:197], v[108:111]
	v_mfma_f32_16x16x32_bf16 v[104:107], v[162:165], v[194:197], v[104:107]
	v_mfma_f32_16x16x32_bf16 v[92:95], v[154:157], v[202:205], v[92:95]
	v_mfma_f32_16x16x32_bf16 v[88:91], v[162:165], v[202:205], v[88:91]
	v_mfma_f32_16x16x32_bf16 v[76:79], v[154:157], v[210:213], v[76:79]
	v_mfma_f32_16x16x32_bf16 v[72:75], v[162:165], v[210:213], v[72:75]
	v_mfma_f32_16x16x32_bf16 v[116:119], v[166:169], v[182:185], v[116:119]
	v_mfma_f32_16x16x32_bf16 v[112:115], v[174:177], v[182:185], v[112:115]
	v_mfma_f32_16x16x32_bf16 v[100:103], v[166:169], v[190:193], v[100:103]
	v_mfma_f32_16x16x32_bf16 v[96:99], v[174:177], v[190:193], v[96:99]
	v_mfma_f32_16x16x32_bf16 v[84:87], v[166:169], v[198:201], v[84:87]
	v_mfma_f32_16x16x32_bf16 v[80:83], v[174:177], v[198:201], v[80:83]
	v_mfma_f32_16x16x32_bf16 v[68:71], v[166:169], v[206:209], v[68:71]
	v_mfma_f32_16x16x32_bf16 v[64:67], v[174:177], v[206:209], v[64:67]
	v_mfma_f32_16x16x32_bf16 v[116:119], v[170:173], v[186:189], v[116:119]
	v_mfma_f32_16x16x32_bf16 v[112:115], v[178:181], v[186:189], v[112:115]
	v_mfma_f32_16x16x32_bf16 v[100:103], v[170:173], v[194:197], v[100:103]
	v_mfma_f32_16x16x32_bf16 v[96:99], v[178:181], v[194:197], v[96:99]
	v_mfma_f32_16x16x32_bf16 v[84:87], v[170:173], v[202:205], v[84:87]
	v_mfma_f32_16x16x32_bf16 v[80:83], v[178:181], v[202:205], v[80:83]
	v_mfma_f32_16x16x32_bf16 v[68:71], v[170:173], v[210:213], v[68:71]
	v_mfma_f32_16x16x32_bf16 v[64:67], v[178:181], v[210:213], v[64:67]
	s_barrier
; #define PG8_LDA(dst, b, h) do { _Pragma("unroll") for (int m = 0; m < 4; ++m) _Pragma("unroll") for (int k = 0; k < 2; ++k) dst[m][k] = *(const PG8_LAS bf16x8*)(lds + PG8_SA(b, h) + aoff + m * 2048 + k * 1024); } while (0)
; #define PG8_WAIT_V(n) asm volatile("s_waitcnt vmcnt(" #n ")" ::: "memory")
; #define PG8_WAIT_L(n) asm volatile("s_waitcnt lgkmcnt(" #n ")" ::: "memory")
; #define PG8_BAR __builtin_amdgcn_s_barrier()
; #define PG8_SCHED __builtin_amdgcn_sched_barrier(0)
; template <class Epi, class Sched, bool ALIGN_EPI = false, bool SP2 = false, bool F8 = false, bool I8 = false, bool PF = false>
; __device__ __forceinline__ void gemm_phase(PG8_LAS unsigned char* lds, const Gemm g, const Sched& S, const Epi& E, const int wave_) {
;     ...
;             PG8_LDA(At, 1, 1); PG8_STAGE(PG8_SB(1, 0), b3, voffB); PG8_STAGE(PG8_SB(1, 1), b3 + hstep, voffB); PG8_STAGE(PG8_SA(1, 0), a3, voffA);
;             PG8_WAIT_V(8); PG8_WAIT_L(0); PG8_BAR; PG8_MMA(1, 0, At, B0); PG8_MMA(1, 1, At, B1); PG8_BAR; PG8_SCHED;
	s_add_i32 s42, s73, s48
	v_lshl_add_u64 v[148:149], v[148:149], 0, s[16:17]
	s_mov_b32 m0, s42
	ds_read_b128 v[182:185], v153 offset:49152
	global_load_lds_dwordx4 v[148:149], off
	ds_read_b128 v[186:189], v153 offset:50176
	s_add_i32 m0, s42, 0x2000
	s_add_u32 s40, s40, 0x20080
	v_lshl_add_u64 v[148:149], v[214:215], 0, s[16:17]
	s_addc_u32 s41, s41, 0
	s_add_i32 s42, s74, s48
	global_load_lds_dwordx4 v[148:149], off
	ds_read_b128 v[190:193], v153 offset:51200
	v_lshl_add_u64 v[148:149], s[40:41], 0, v[130:131]
	s_mov_b32 m0, s42
	ds_read_b128 v[194:197], v153 offset:52224
	global_load_lds_dwordx4 v[148:149], off
	ds_read_b128 v[198:201], v153 offset:53248
	v_lshl_add_u64 v[148:149], s[40:41], 0, v[134:135]
	s_add_i32 m0, s42, 0x2000
	ds_read_b128 v[202:205], v153 offset:54272
	global_load_lds_dwordx4 v[148:149], off
	ds_read_b128 v[206:209], v153 offset:55296
	v_lshl_add_u64 v[148:149], v[216:217], 0, s[16:17]
	s_mov_b32 m0, s62
	ds_read_b128 v[210:213], v153 offset:56320
	global_load_lds_dwordx4 v[148:149], off
	v_lshl_add_u64 v[148:149], v[218:219], 0, s[16:17]
	s_mov_b32 m0, s63
	s_nop 0
	global_load_lds_dwordx4 v[148:149], off
	s_waitcnt vmcnt(8)
	s_waitcnt lgkmcnt(0)
	s_barrier
	s_waitcnt lgkmcnt(0)
	v_mfma_f32_16x16x32_bf16 v[60:63], v[144:147], v[182:185], v[60:63]
	v_mfma_f32_16x16x32_bf16 v[56:59], v[158:161], v[182:185], v[56:59]
	v_mfma_f32_16x16x32_bf16 v[44:47], v[144:147], v[190:193], v[44:47]
	v_mfma_f32_16x16x32_bf16 v[40:43], v[158:161], v[190:193], v[40:43]
	v_mfma_f32_16x16x32_bf16 v[28:31], v[144:147], v[198:201], v[28:31]
	v_mfma_f32_16x16x32_bf16 v[24:27], v[158:161], v[198:201], v[24:27]
	v_mfma_f32_16x16x32_bf16 v[12:15], v[144:147], v[206:209], v[12:15]
	v_mfma_f32_16x16x32_bf16 v[8:11], v[158:161], v[206:209], v[8:11]
	v_mfma_f32_16x16x32_bf16 v[60:63], v[154:157], v[186:189], v[60:63]
	v_mfma_f32_16x16x32_bf16 v[56:59], v[162:165], v[186:189], v[56:59]
	v_mfma_f32_16x16x32_bf16 v[44:47], v[154:157], v[194:197], v[44:47]
	v_mfma_f32_16x16x32_bf16 v[40:43], v[162:165], v[194:197], v[40:43]
	v_mfma_f32_16x16x32_bf16 v[28:31], v[154:157], v[202:205], v[28:31]
	v_mfma_f32_16x16x32_bf16 v[24:27], v[162:165], v[202:205], v[24:27]
	v_mfma_f32_16x16x32_bf16 v[12:15], v[154:157], v[210:213], v[12:15]
	v_mfma_f32_16x16x32_bf16 v[8:11], v[162:165], v[210:213], v[8:11]
	v_mfma_f32_16x16x32_bf16 v[52:55], v[166:169], v[182:185], v[52:55]
	v_mfma_f32_16x16x32_bf16 v[48:51], v[174:177], v[182:185], v[48:51]
	v_mfma_f32_16x16x32_bf16 v[36:39], v[166:169], v[190:193], v[36:39]
	v_mfma_f32_16x16x32_bf16 v[32:35], v[174:177], v[190:193], v[32:35]
	v_mfma_f32_16x16x32_bf16 v[20:23], v[166:169], v[198:201], v[20:23]
	v_mfma_f32_16x16x32_bf16 v[16:19], v[174:177], v[198:201], v[16:19]
	v_mfma_f32_16x16x32_bf16 v[4:7], v[166:169], v[206:209], v[4:7]
	v_mfma_f32_16x16x32_bf16 v[0:3], v[174:177], v[206:209], v[0:3]
	v_mfma_f32_16x16x32_bf16 v[52:55], v[170:173], v[186:189], v[52:55]
	v_mfma_f32_16x16x32_bf16 v[48:51], v[178:181], v[186:189], v[48:51]
	v_mfma_f32_16x16x32_bf16 v[36:39], v[170:173], v[194:197], v[36:39]
	v_mfma_f32_16x16x32_bf16 v[32:35], v[178:181], v[194:197], v[32:35]
	v_mfma_f32_16x16x32_bf16 v[20:23], v[170:173], v[202:205], v[20:23]
	v_mfma_f32_16x16x32_bf16 v[16:19], v[178:181], v[202:205], v[16:19]
	v_mfma_f32_16x16x32_bf16 v[4:7], v[170:173], v[210:213], v[4:7]
	v_mfma_f32_16x16x32_bf16 v[0:3], v[178:181], v[210:213], v[0:3]
	s_barrier
	s_add_i32 s72, s72, 2
	s_add_u32 s38, s38, 0x100
	s_addc_u32 s39, s39, 0
	s_add_u32 s70, s70, 0x100
	s_addc_u32 s71, s71, 0
	s_cmp_gt_u32 s72, 5
	s_cbranch_scc0 .LBB0_967
	s_and_b64 vcc, exec, s[18:19]
	s_cbranch_vccz .LBB0_970
	s_barrier

; #define PG8_LDA(dst, b, h) do { _Pragma("unroll") for (int m = 0; m < 4; ++m) _Pragma("unroll") for (int k = 0; k < 2; ++k) dst[m][k] = *(const PG8_LAS bf16x8*)(lds + PG8_SA(b, h) + aoff + m * 2048 + k * 1024); } while (0)
; #define PG8_LDB(dst, b, h) do { _Pragma("unroll") for (int n = 0; n < 2; ++n) _Pragma("unroll") for (int k = 0; k < 2; ++k) dst[n][k] = *(const PG8_LAS bf16x8*)(lds + PG8_SB(b, h) + boff + n * 2048 + k * 1024); } while (0)
; #define PG8_WAIT_V(n) asm volatile("s_waitcnt vmcnt(" #n ")" ::: "memory")
; #define PG8_WAIT_L(n) asm volatile("s_waitcnt lgkmcnt(" #n ")" ::: "memory")
; #define PG8_BAR __builtin_amdgcn_s_barrier()
; #define PG8_SCHED __builtin_amdgcn_sched_barrier(0)
; template <class Epi, class Sched, bool ALIGN_EPI = false, bool SP2 = false, bool F8 = false, bool I8 = false, bool PF = false>
; __device__ __forceinline__ void gemm_phase(PG8_LAS unsigned char* lds, const Gemm g, const Sched& S, const Epi& E, const int wave_) {
;     ...
;             PG8_LDB(B0, 0, 0); PG8_LDB(B1, 0, 1); PG8_SCHED; PG8_LDA(At, 0, 0); PG8_STAGE(PG8_SA(1, 1), a1 + hstep, voffA);
;             PG8_WAIT_V(8); PG8_WAIT_L(0); PG8_BAR; PG8_MMA(0, 0, At, B0); PG8_MMA(0, 1, At, B1); PG8_BAR; PG8_SCHED;
;             PG8_LDA(At, 0, 1); PG8_STAGE(PG8_SB(0, 0), b2, voffB); PG8_STAGE(PG8_SB(0, 1), b2 + hstep, voffB); PG8_STAGE(PG8_SA(0, 0), a2, voffA);
;             PG8_WAIT_V(8); PG8_WAIT_L(0); PG8_BAR; PG8_MMA(1, 0, At, B0); PG8_MMA(1, 1, At, B1); PG8_BAR; PG8_SCHED;
.LBB0_1304:
	ds_read_b128 v[128:131], v209
	ds_read_b128 v[132:135], v209 offset:1024
	ds_read_b128 v[136:139], v209 offset:2048
	ds_read_b128 v[140:143], v209 offset:3072
	ds_read_b128 v[144:147], v210
	ds_read_b128 v[148:151], v210 offset:1024
	ds_read_b128 v[152:155], v210 offset:2048
	ds_read_b128 v[156:159], v210 offset:3072
	s_add_u32 s34, s30, 0xfffc0080
	s_addc_u32 s35, s31, -1
	s_cmp_eq_u32 s66, 12
	s_cselect_b32 s37, s21, s35
	s_cselect_b32 s36, s62, s34
	s_cselect_b32 s35, s19, s65
	s_cselect_b32 s34, s63, s64
	v_lshl_add_u64 v[206:207], s[30:31], 0, v[188:189]
	s_add_i32 m0, s29, 0xc000
	ds_read_b128 v[160:163], v211
	ds_read_b128 v[164:167], v211 offset:1024
	ds_read_b128 v[168:171], v211 offset:2048
	ds_read_b128 v[172:175], v211 offset:3072
	ds_read_b128 v[176:179], v211 offset:4096
	ds_read_b128 v[194:197], v211 offset:5120
	ds_read_b128 v[198:201], v211 offset:6144
	ds_read_b128 v[202:205], v211 offset:7168
	global_load_lds_dwordx4 v[206:207], off
	v_lshl_add_u64 v[206:207], s[30:31], 0, v[190:191]
	s_add_i32 m0, s29, 0xe000
	s_nop 0
	global_load_lds_dwordx4 v[206:207], off
	s_waitcnt vmcnt(8)
	s_waitcnt lgkmcnt(0)
	s_barrier
	s_waitcnt lgkmcnt(0)
	v_mfma_f32_16x16x32_bf16 v[124:127], v[128:131], v[160:163], v[124:127]
	v_mfma_f32_16x16x32_bf16 v[120:123], v[136:139], v[160:163], v[120:123]
	v_mfma_f32_16x16x32_bf16 v[108:111], v[128:131], v[168:171], v[108:111]
	v_mfma_f32_16x16x32_bf16 v[104:107], v[136:139], v[168:171], v[104:107]
	v_mfma_f32_16x16x32_bf16 v[92:95], v[128:131], v[176:179], v[92:95]
	v_mfma_f32_16x16x32_bf16 v[88:91], v[136:139], v[176:179], v[88:91]
	v_mfma_f32_16x16x32_bf16 v[76:79], v[128:131], v[198:201], v[76:79]
	v_mfma_f32_16x16x32_bf16 v[72:75], v[136:139], v[198:201], v[72:75]
	v_mfma_f32_16x16x32_bf16 v[124:127], v[132:135], v[164:167], v[124:127]
	v_mfma_f32_16x16x32_bf16 v[120:123], v[140:143], v[164:167], v[120:123]
	v_mfma_f32_16x16x32_bf16 v[108:111], v[132:135], v[172:175], v[108:111]
	v_mfma_f32_16x16x32_bf16 v[104:107], v[140:143], v[172:175], v[104:107]
	v_mfma_f32_16x16x32_bf16 v[92:95], v[132:135], v[194:197], v[92:95]
	v_mfma_f32_16x16x32_bf16 v[88:91], v[140:143], v[194:197], v[88:91]
	v_mfma_f32_16x16x32_bf16 v[76:79], v[132:135], v[202:205], v[76:79]
	v_mfma_f32_16x16x32_bf16 v[72:75], v[140:143], v[202:205], v[72:75]
	v_mfma_f32_16x16x32_bf16 v[116:119], v[144:147], v[160:163], v[116:119]
	v_mfma_f32_16x16x32_bf16 v[112:115], v[152:155], v[160:163], v[112:115]
	v_mfma_f32_16x16x32_bf16 v[100:103], v[144:147], v[168:171], v[100:103]
	v_mfma_f32_16x16x32_bf16 v[96:99], v[152:155], v[168:171], v[96:99]
	v_mfma_f32_16x16x32_bf16 v[84:87], v[144:147], v[176:179], v[84:87]
	v_mfma_f32_16x16x32_bf16 v[80:83], v[152:155], v[176:179], v[80:83]
	v_mfma_f32_16x16x32_bf16 v[68:71], v[144:147], v[198:201], v[68:71]
	v_mfma_f32_16x16x32_bf16 v[64:67], v[152:155], v[198:201], v[64:67]
	v_mfma_f32_16x16x32_bf16 v[116:119], v[148:151], v[164:167], v[116:119]
	v_mfma_f32_16x16x32_bf16 v[112:115], v[156:159], v[164:167], v[112:115]
	v_mfma_f32_16x16x32_bf16 v[100:103], v[148:151], v[172:175], v[100:103]
	v_mfma_f32_16x16x32_bf16 v[96:99], v[156:159], v[172:175], v[96:99]
	v_mfma_f32_16x16x32_bf16 v[84:87], v[148:151], v[194:197], v[84:87]
	v_mfma_f32_16x16x32_bf16 v[80:83], v[156:159], v[194:197], v[80:83]
	v_mfma_f32_16x16x32_bf16 v[68:71], v[148:151], v[202:205], v[68:71]
	v_mfma_f32_16x16x32_bf16 v[64:67], v[156:159], v[202:205], v[64:67]
	s_barrier
	s_add_i32 s67, s55, s40
	v_lshl_add_u64 v[206:207], s[34:35], 0, v[184:185]
	s_mov_b32 m0, s67
	ds_read_b128 v[160:163], v211 offset:16384
	global_load_lds_dwordx4 v[206:207], off
	ds_read_b128 v[164:167], v211 offset:17408
	s_add_i32 m0, s67, 0x2000
	s_add_u32 s68, s34, 0x40000
	v_lshl_add_u64 v[212:213], s[34:35], 0, v[180:181]
	s_addc_u32 s69, s35, 0
	s_add_i32 s67, s56, s40
	global_load_lds_dwordx4 v[212:213], off
	ds_read_b128 v[168:171], v211 offset:18432
	v_lshl_add_u64 v[214:215], s[68:69], 0, v[184:185]
	s_mov_b32 m0, s67
	v_lshl_add_u64 v[216:217], s[36:37], 0, v[182:183]
	global_load_lds_dwordx4 v[214:215], off
	ds_read_b128 v[172:175], v211 offset:19456
	v_lshl_add_u64 v[214:215], s[68:69], 0, v[180:181]
	s_add_i32 m0, s67, 0x2000
	ds_read_b128 v[176:179], v211 offset:20480
	global_load_lds_dwordx4 v[214:215], off
	ds_read_b128 v[194:197], v211 offset:21504
	v_lshl_add_u64 v[214:215], s[36:37], 0, v[186:187]
	s_mov_b32 m0, s29
	ds_read_b128 v[198:201], v211 offset:22528
	global_load_lds_dwordx4 v[214:215], off
	ds_read_b128 v[202:205], v211 offset:23552
	s_mov_b32 m0, s41
	s_nop 0
	global_load_lds_dwordx4 v[216:217], off
	s_waitcnt vmcnt(8)
	s_waitcnt lgkmcnt(0)
	s_barrier
; #define PG8_LDA(dst, b, h) do { _Pragma("unroll") for (int m = 0; m < 4; ++m) _Pragma("unroll") for (int k = 0; k < 2; ++k) dst[m][k] = *(const PG8_LAS bf16x8*)(lds + PG8_SA(b, h) + aoff + m * 2048 + k * 1024); } while (0)
; #define PG8_LDB(dst, b, h) do { _Pragma("unroll") for (int n = 0; n < 2; ++n) _Pragma("unroll") for (int k = 0; k < 2; ++k) dst[n][k] = *(const PG8_LAS bf16x8*)(lds + PG8_SB(b, h) + boff + n * 2048 + k * 1024); } while (0)
; #define PG8_WAIT_V(n) asm volatile("s_waitcnt vmcnt(" #n ")" ::: "memory")
; #define PG8_WAIT_L(n) asm volatile("s_waitcnt lgkmcnt(" #n ")" ::: "memory")
; #define PG8_BAR __builtin_amdgcn_s_barrier()
; #define PG8_SCHED __builtin_amdgcn_sched_barrier(0)
; template <class Epi, class Sched, bool ALIGN_EPI = false, bool SP2 = false, bool F8 = false, bool I8 = false, bool PF = false>
; __device__ __forceinline__ void gemm_phase(PG8_LAS unsigned char* lds, const Gemm g, const Sched& S, const Epi& E, const int wave_) {
;     ...
;             PG8_WAIT_V(8); PG8_WAIT_L(0); PG8_BAR; PG8_MMA(1, 0, At, B0); PG8_MMA(1, 1, At, B1); PG8_BAR; PG8_SCHED;
;             PG8_LDB(B0, 1, 0); PG8_LDB(B1, 1, 1); PG8_SCHED; PG8_LDA(At, 1, 0); PG8_STAGE(PG8_SA(0, 1), a2 + hstep, voffA);
;             PG8_WAIT_V(8); PG8_WAIT_L(0); PG8_BAR; PG8_MMA(0, 0, At, B0); PG8_MMA(0, 1, At, B1); PG8_BAR; PG8_SCHED;
	s_waitcnt lgkmcnt(0)
	v_mfma_f32_16x16x32_bf16 v[60:63], v[128:131], v[160:163], v[60:63]
	v_mfma_f32_16x16x32_bf16 v[56:59], v[136:139], v[160:163], v[56:59]
	v_mfma_f32_16x16x32_bf16 v[44:47], v[128:131], v[168:171], v[44:47]
	v_mfma_f32_16x16x32_bf16 v[40:43], v[136:139], v[168:171], v[40:43]
	v_mfma_f32_16x16x32_bf16 v[28:31], v[128:131], v[176:179], v[28:31]
	v_mfma_f32_16x16x32_bf16 v[24:27], v[136:139], v[176:179], v[24:27]
	v_mfma_f32_16x16x32_bf16 v[12:15], v[128:131], v[198:201], v[12:15]
	v_mfma_f32_16x16x32_bf16 v[8:11], v[136:139], v[198:201], v[8:11]
	v_mfma_f32_16x16x32_bf16 v[60:63], v[132:135], v[164:167], v[60:63]
	v_mfma_f32_16x16x32_bf16 v[56:59], v[140:143], v[164:167], v[56:59]
	v_mfma_f32_16x16x32_bf16 v[44:47], v[132:135], v[172:175], v[44:47]
	v_mfma_f32_16x16x32_bf16 v[40:43], v[140:143], v[172:175], v[40:43]
	v_mfma_f32_16x16x32_bf16 v[28:31], v[132:135], v[194:197], v[28:31]
	v_mfma_f32_16x16x32_bf16 v[24:27], v[140:143], v[194:197], v[24:27]
	v_mfma_f32_16x16x32_bf16 v[12:15], v[132:135], v[202:205], v[12:15]
	v_mfma_f32_16x16x32_bf16 v[8:11], v[140:143], v[202:205], v[8:11]
	v_mfma_f32_16x16x32_bf16 v[52:55], v[144:147], v[160:163], v[52:55]
	v_mfma_f32_16x16x32_bf16 v[48:51], v[152:155], v[160:163], v[48:51]
	v_mfma_f32_16x16x32_bf16 v[36:39], v[144:147], v[168:171], v[36:39]
	v_mfma_f32_16x16x32_bf16 v[32:35], v[152:155], v[168:171], v[32:35]
	v_mfma_f32_16x16x32_bf16 v[20:23], v[144:147], v[176:179], v[20:23]
	v_mfma_f32_16x16x32_bf16 v[16:19], v[152:155], v[176:179], v[16:19]
	v_mfma_f32_16x16x32_bf16 v[4:7], v[144:147], v[198:201], v[4:7]
	v_mfma_f32_16x16x32_bf16 v[0:3], v[152:155], v[198:201], v[0:3]
	v_mfma_f32_16x16x32_bf16 v[52:55], v[148:151], v[164:167], v[52:55]
	v_mfma_f32_16x16x32_bf16 v[48:51], v[156:159], v[164:167], v[48:51]
	v_mfma_f32_16x16x32_bf16 v[36:39], v[148:151], v[172:175], v[36:39]
	v_mfma_f32_16x16x32_bf16 v[32:35], v[156:159], v[172:175], v[32:35]
	v_mfma_f32_16x16x32_bf16 v[20:23], v[148:151], v[194:197], v[20:23]
	v_mfma_f32_16x16x32_bf16 v[16:19], v[156:159], v[194:197], v[16:19]
	v_mfma_f32_16x16x32_bf16 v[4:7], v[148:151], v[202:205], v[4:7]
	v_mfma_f32_16x16x32_bf16 v[0:3], v[156:159], v[202:205], v[0:3]
	s_barrier
	s_add_i32 s67, 0, 0x18000
	s_add_i32 s68, 0, 0x1c000
	v_add_u32_e32 v140, s67, v208
	v_add_u32_e32 v156, s68, v208
	ds_read_b128 v[128:131], v140
	ds_read_b128 v[132:135], v140 offset:1024
	ds_read_b128 v[136:139], v140 offset:2048
	ds_read_b128 v[140:143], v140 offset:3072
	ds_read_b128 v[144:147], v156
	ds_read_b128 v[148:151], v156 offset:1024
	ds_read_b128 v[152:155], v156 offset:2048
	ds_read_b128 v[156:159], v156 offset:3072
	s_add_u32 s36, s36, 0x40000
	s_addc_u32 s37, s37, 0
	s_mov_b32 m0, s42
	v_lshl_add_u64 v[218:219], s[36:37], 0, v[186:187]
	ds_read_b128 v[160:163], v211 offset:32768
	ds_read_b128 v[164:167], v211 offset:33792
	ds_read_b128 v[168:171], v211 offset:34816
	ds_read_b128 v[172:175], v211 offset:35840
	ds_read_b128 v[176:179], v211 offset:36864
	ds_read_b128 v[194:197], v211 offset:37888
	ds_read_b128 v[198:201], v211 offset:38912
	ds_read_b128 v[202:205], v211 offset:39936
	global_load_lds_dwordx4 v[218:219], off
	v_lshl_add_u64 v[218:219], s[36:37], 0, v[182:183]
	s_mov_b32 m0, s43
	s_nop 0
	global_load_lds_dwordx4 v[218:219], off
	s_waitcnt vmcnt(8)
	s_waitcnt lgkmcnt(0)
	s_barrier
	s_waitcnt lgkmcnt(0)
	v_mfma_f32_16x16x32_bf16 v[124:127], v[128:131], v[160:163], v[124:127]
	v_mfma_f32_16x16x32_bf16 v[120:123], v[136:139], v[160:163], v[120:123]
	v_mfma_f32_16x16x32_bf16 v[108:111], v[128:131], v[168:171], v[108:111]
	v_mfma_f32_16x16x32_bf16 v[104:107], v[136:139], v[168:171], v[104:107]
	v_mfma_f32_16x16x32_bf16 v[92:95], v[128:131], v[176:179], v[92:95]
	v_mfma_f32_16x16x32_bf16 v[88:91], v[136:139], v[176:179], v[88:91]
	v_mfma_f32_16x16x32_bf16 v[76:79], v[128:131], v[198:201], v[76:79]
	v_mfma_f32_16x16x32_bf16 v[72:75], v[136:139], v[198:201], v[72:75]
	v_mfma_f32_16x16x32_bf16 v[124:127], v[132:135], v[164:167], v[124:127]
	v_mfma_f32_16x16x32_bf16 v[120:123], v[140:143], v[164:167], v[120:123]
	v_mfma_f32_16x16x32_bf16 v[108:111], v[132:135], v[172:175], v[108:111]
	v_mfma_f32_16x16x32_bf16 v[104:107], v[140:143], v[172:175], v[104:107]
	v_mfma_f32_16x16x32_bf16 v[92:95], v[132:135], v[194:197], v[92:95]
	v_mfma_f32_16x16x32_bf16 v[88:91], v[140:143], v[194:197], v[88:91]
	v_mfma_f32_16x16x32_bf16 v[76:79], v[132:135], v[202:205], v[76:79]
	v_mfma_f32_16x16x32_bf16 v[72:75], v[140:143], v[202:205], v[72:75]
	v_mfma_f32_16x16x32_bf16 v[116:119], v[144:147], v[160:163], v[116:119]
	v_mfma_f32_16x16x32_bf16 v[112:115], v[152:155], v[160:163], v[112:115]
	v_mfma_f32_16x16x32_bf16 v[100:103], v[144:147], v[168:171], v[100:103]
	v_mfma_f32_16x16x32_bf16 v[96:99], v[152:155], v[168:171], v[96:99]
	v_mfma_f32_16x16x32_bf16 v[84:87], v[144:147], v[176:179], v[84:87]
	v_mfma_f32_16x16x32_bf16 v[80:83], v[152:155], v[176:179], v[80:83]
	v_mfma_f32_16x16x32_bf16 v[68:71], v[144:147], v[198:201], v[68:71]
	v_mfma_f32_16x16x32_bf16 v[64:67], v[152:155], v[198:201], v[64:67]
	v_mfma_f32_16x16x32_bf16 v[116:119], v[148:151], v[164:167], v[116:119]
	v_mfma_f32_16x16x32_bf16 v[112:115], v[156:159], v[164:167], v[112:115]
	v_mfma_f32_16x16x32_bf16 v[100:103], v[148:151], v[172:175], v[100:103]
	v_mfma_f32_16x16x32_bf16 v[96:99], v[156:159], v[172:175], v[96:99]
	v_mfma_f32_16x16x32_bf16 v[84:87], v[148:151], v[194:197], v[84:87]
	v_mfma_f32_16x16x32_bf16 v[80:83], v[156:159], v[194:197], v[80:83]
	v_mfma_f32_16x16x32_bf16 v[68:71], v[148:151], v[202:205], v[68:71]
	v_mfma_f32_16x16x32_bf16 v[64:67], v[156:159], v[202:205], v[64:67]
	s_barrier
; #define PG8_LDA(dst, b, h) do { _Pragma("unroll") for (int m = 0; m < 4; ++m) _Pragma("unroll") for (int k = 0; k < 2; ++k) dst[m][k] = *(const PG8_LAS bf16x8*)(lds + PG8_SA(b, h) + aoff + m * 2048 + k * 1024); } while (0)
; #define PG8_WAIT_V(n) asm volatile("s_waitcnt vmcnt(" #n ")" ::: "memory")
; #define PG8_WAIT_L(n) asm volatile("s_waitcnt lgkmcnt(" #n ")" ::: "memory")
; #define PG8_BAR __builtin_amdgcn_s_barrier()
; #define PG8_SCHED __builtin_amdgcn_sched_barrier(0)
; template <class Epi, class Sched, bool ALIGN_EPI = false, bool SP2 = false, bool F8 = false, bool I8 = false, bool PF = false>
; __device__ __forceinline__ void gemm_phase(PG8_LAS unsigned char* lds, const Gemm g, const Sched& S, const Epi& E, const int wave_) {
;     ...
;             PG8_LDA(At, 1, 1); PG8_STAGE(PG8_SB(1, 0), b3, voffB); PG8_STAGE(PG8_SB(1, 1), b3 + hstep, voffB); PG8_STAGE(PG8_SA(1, 0), a3, voffA);
;             PG8_WAIT_V(8); PG8_WAIT_L(0); PG8_BAR; PG8_MMA(1, 0, At, B0); PG8_MMA(1, 1, At, B1); PG8_BAR; PG8_SCHED;
	s_add_i32 s36, s67, s40
	v_lshl_add_u64 v[206:207], v[206:207], 0, s[8:9]
	s_mov_b32 m0, s36
	ds_read_b128 v[160:163], v211 offset:49152
	global_load_lds_dwordx4 v[206:207], off
	ds_read_b128 v[164:167], v211 offset:50176
	s_add_i32 m0, s36, 0x2000
	s_add_u32 s34, s34, 0x40080
	v_lshl_add_u64 v[206:207], v[212:213], 0, s[8:9]
	s_addc_u32 s35, s35, 0
	s_add_i32 s36, s68, s40
	global_load_lds_dwordx4 v[206:207], off
	ds_read_b128 v[168:171], v211 offset:51200
	v_lshl_add_u64 v[206:207], s[34:35], 0, v[184:185]
	s_mov_b32 m0, s36
	ds_read_b128 v[172:175], v211 offset:52224
	global_load_lds_dwordx4 v[206:207], off
	ds_read_b128 v[176:179], v211 offset:53248
	v_lshl_add_u64 v[206:207], s[34:35], 0, v[180:181]
	s_add_i32 m0, s36, 0x2000
	ds_read_b128 v[194:197], v211 offset:54272
	global_load_lds_dwordx4 v[206:207], off
	ds_read_b128 v[198:201], v211 offset:55296
	v_lshl_add_u64 v[206:207], v[214:215], 0, s[8:9]
	s_mov_b32 m0, s52
	ds_read_b128 v[202:205], v211 offset:56320
	global_load_lds_dwordx4 v[206:207], off
	v_lshl_add_u64 v[206:207], v[216:217], 0, s[8:9]
	s_mov_b32 m0, s53
	s_nop 0
	global_load_lds_dwordx4 v[206:207], off
	s_waitcnt vmcnt(8)
	s_waitcnt lgkmcnt(0)
	s_barrier
	s_waitcnt lgkmcnt(0)
	v_mfma_f32_16x16x32_bf16 v[60:63], v[128:131], v[160:163], v[60:63]
	v_mfma_f32_16x16x32_bf16 v[56:59], v[136:139], v[160:163], v[56:59]
	v_mfma_f32_16x16x32_bf16 v[44:47], v[128:131], v[168:171], v[44:47]
	v_mfma_f32_16x16x32_bf16 v[40:43], v[136:139], v[168:171], v[40:43]
	v_mfma_f32_16x16x32_bf16 v[28:31], v[128:131], v[176:179], v[28:31]
	v_mfma_f32_16x16x32_bf16 v[24:27], v[136:139], v[176:179], v[24:27]
	v_mfma_f32_16x16x32_bf16 v[12:15], v[128:131], v[198:201], v[12:15]
	v_mfma_f32_16x16x32_bf16 v[8:11], v[136:139], v[198:201], v[8:11]
	v_mfma_f32_16x16x32_bf16 v[60:63], v[132:135], v[164:167], v[60:63]
	v_mfma_f32_16x16x32_bf16 v[56:59], v[140:143], v[164:167], v[56:59]
	v_mfma_f32_16x16x32_bf16 v[44:47], v[132:135], v[172:175], v[44:47]
	v_mfma_f32_16x16x32_bf16 v[40:43], v[140:143], v[172:175], v[40:43]
	v_mfma_f32_16x16x32_bf16 v[28:31], v[132:135], v[194:197], v[28:31]
	v_mfma_f32_16x16x32_bf16 v[24:27], v[140:143], v[194:197], v[24:27]
	v_mfma_f32_16x16x32_bf16 v[12:15], v[132:135], v[202:205], v[12:15]
	v_mfma_f32_16x16x32_bf16 v[8:11], v[140:143], v[202:205], v[8:11]
	v_mfma_f32_16x16x32_bf16 v[52:55], v[144:147], v[160:163], v[52:55]
	v_mfma_f32_16x16x32_bf16 v[48:51], v[152:155], v[160:163], v[48:51]
	v_mfma_f32_16x16x32_bf16 v[36:39], v[144:147], v[168:171], v[36:39]
	v_mfma_f32_16x16x32_bf16 v[32:35], v[152:155], v[168:171], v[32:35]
	v_mfma_f32_16x16x32_bf16 v[20:23], v[144:147], v[176:179], v[20:23]
	v_mfma_f32_16x16x32_bf16 v[16:19], v[152:155], v[176:179], v[16:19]
	v_mfma_f32_16x16x32_bf16 v[4:7], v[144:147], v[198:201], v[4:7]
	v_mfma_f32_16x16x32_bf16 v[0:3], v[152:155], v[198:201], v[0:3]
	v_mfma_f32_16x16x32_bf16 v[52:55], v[148:151], v[164:167], v[52:55]
	v_mfma_f32_16x16x32_bf16 v[48:51], v[156:159], v[164:167], v[48:51]
	v_mfma_f32_16x16x32_bf16 v[36:39], v[148:151], v[172:175], v[36:39]
	v_mfma_f32_16x16x32_bf16 v[32:35], v[156:159], v[172:175], v[32:35]
	v_mfma_f32_16x16x32_bf16 v[20:23], v[148:151], v[194:197], v[20:23]
	v_mfma_f32_16x16x32_bf16 v[16:19], v[156:159], v[194:197], v[16:19]
	v_mfma_f32_16x16x32_bf16 v[4:7], v[148:151], v[202:205], v[4:7]
	v_mfma_f32_16x16x32_bf16 v[0:3], v[156:159], v[202:205], v[0:3]
	s_barrier
	s_add_i32 s66, s66, 2
	s_add_u32 s30, s30, 0x100
	s_addc_u32 s31, s31, 0
	s_add_u32 s64, s64, 0x100
	s_addc_u32 s65, s65, 0
	s_cmp_gt_u32 s66, 13
	s_cbranch_scc0 .LBB0_1304
	s_and_b64 vcc, exec, s[10:11]
	s_cbranch_vccz .LBB0_1307
	s_barrier

; #define PG8_LDA(dst, b, h) do { _Pragma("unroll") for (int m = 0; m < 4; ++m) _Pragma("unroll") for (int k = 0; k < 2; ++k) dst[m][k] = *(const PG8_LAS bf16x8*)(lds + PG8_SA(b, h) + aoff + m * 2048 + k * 1024); } while (0)
; #define PG8_LDB(dst, b, h) do { _Pragma("unroll") for (int n = 0; n < 2; ++n) _Pragma("unroll") for (int k = 0; k < 2; ++k) dst[n][k] = *(const PG8_LAS bf16x8*)(lds + PG8_SB(b, h) + boff + n * 2048 + k * 1024); } while (0)
; #define PG8_WAIT_V(n) asm volatile("s_waitcnt vmcnt(" #n ")" ::: "memory")
; #define PG8_WAIT_L(n) asm volatile("s_waitcnt lgkmcnt(" #n ")" ::: "memory")
; #define PG8_BAR __builtin_amdgcn_s_barrier()
; #define PG8_SCHED __builtin_amdgcn_sched_barrier(0)
; template <class Epi, class Sched, bool ALIGN_EPI = false, bool SP2 = false, bool F8 = false, bool I8 = false, bool PF = false>
; __device__ __forceinline__ void gemm_phase(PG8_LAS unsigned char* lds, const Gemm g, const Sched& S, const Epi& E, const int wave_) {
;     ...
;             PG8_LDB(B0, 0, 0); PG8_LDB(B1, 0, 1); PG8_SCHED; PG8_LDA(At, 0, 0); PG8_STAGE(PG8_SA(1, 1), a1 + hstep, voffA);
;             PG8_WAIT_V(8); PG8_WAIT_L(0); PG8_BAR; PG8_MMA(0, 0, At, B0); PG8_MMA(0, 1, At, B1); PG8_BAR; PG8_SCHED;
;             PG8_LDA(At, 0, 1); PG8_STAGE(PG8_SB(0, 0), b2, voffB); PG8_STAGE(PG8_SB(0, 1), b2 + hstep, voffB); PG8_STAGE(PG8_SA(0, 0), a2, voffA);
;             PG8_WAIT_V(8); PG8_WAIT_L(0); PG8_BAR; PG8_MMA(1, 0, At, B0); PG8_MMA(1, 1, At, B1); PG8_BAR; PG8_SCHED;
.LBB0_1540:
	ds_read_b128 v[24:27], v181
	ds_read_b128 v[28:31], v181 offset:1024
	ds_read_b128 v[16:19], v181 offset:2048
	ds_read_b128 v[20:23], v181 offset:3072
	ds_read_b128 v[8:11], v182
	ds_read_b128 v[12:15], v182 offset:1024
	ds_read_b128 v[0:3], v182 offset:2048
	ds_read_b128 v[4:7], v182 offset:3072
	s_add_u32 s34, s30, 0xfffe0080
	s_addc_u32 s35, s31, -1
	s_cmp_eq_u32 s74, 4
	s_cselect_b32 s37, s19, s35
	s_cselect_b32 s36, s21, s34
	s_cselect_b32 s35, s17, s73
	s_cselect_b32 s34, s71, s72
	v_lshl_add_u64 v[210:211], s[30:31], 0, v[168:169]
	s_add_i32 m0, s29, 0xc000
	ds_read_b128 v[172:175], v183
	ds_read_b128 v[176:179], v183 offset:1024
	ds_read_b128 v[186:189], v183 offset:2048
	ds_read_b128 v[190:193], v183 offset:3072
	ds_read_b128 v[194:197], v183 offset:4096
	ds_read_b128 v[198:201], v183 offset:5120
	ds_read_b128 v[202:205], v183 offset:6144
	ds_read_b128 v[206:209], v183 offset:7168
	global_load_lds_dwordx4 v[210:211], off
	v_lshl_add_u64 v[210:211], s[30:31], 0, v[170:171]
	s_add_i32 m0, s29, 0xe000
	s_nop 0
	global_load_lds_dwordx4 v[210:211], off
	s_waitcnt vmcnt(8)
	s_waitcnt lgkmcnt(0)
	s_barrier
	s_waitcnt lgkmcnt(0)
	v_mfma_f32_16x16x128_f8f6f4 v[156:159], v[24:31], v[172:179], v[156:159]
	v_lshl_add_u64 v[222:223], s[34:35], 0, v[160:161]
	v_mfma_f32_16x16x128_f8f6f4 v[148:151], v[16:23], v[172:179], v[148:151]
	v_lshl_add_u64 v[224:225], s[34:35], 0, v[166:167]
	v_mfma_f32_16x16x128_f8f6f4 v[140:143], v[24:31], v[186:193], v[140:143]
	s_add_u32 s76, s34, 0x20000
	s_addc_u32 s77, s35, 0
	v_mfma_f32_16x16x128_f8f6f4 v[132:135], v[16:23], v[186:193], v[132:135]
	v_lshl_add_u64 v[226:227], s[76:77], 0, v[160:161]
	v_mfma_f32_16x16x128_f8f6f4 v[124:127], v[24:31], v[194:201], v[124:127]
	v_lshl_add_u64 v[228:229], s[76:77], 0, v[166:167]
	v_mfma_f32_16x16x128_f8f6f4 v[116:119], v[16:23], v[194:201], v[116:119]
	v_lshl_add_u64 v[230:231], s[36:37], 0, v[162:163]
	v_mfma_f32_16x16x128_f8f6f4 v[108:111], v[24:31], v[202:209], v[108:111]
	v_lshl_add_u64 v[232:233], s[36:37], 0, v[164:165]
	v_mfma_f32_16x16x128_f8f6f4 v[100:103], v[16:23], v[202:209], v[100:103]
	v_mfma_f32_16x16x128_f8f6f4 v[152:155], v[8:15], v[172:179], v[152:155]
	v_mfma_f32_16x16x128_f8f6f4 v[144:147], v[0:7], v[172:179], v[144:147]
	v_mfma_f32_16x16x128_f8f6f4 v[136:139], v[8:15], v[186:193], v[136:139]
	v_mfma_f32_16x16x128_f8f6f4 v[128:131], v[0:7], v[186:193], v[128:131]
	v_mfma_f32_16x16x128_f8f6f4 v[120:123], v[8:15], v[194:201], v[120:123]
	v_mfma_f32_16x16x128_f8f6f4 v[112:115], v[0:7], v[194:201], v[112:115]
	v_mfma_f32_16x16x128_f8f6f4 v[104:107], v[8:15], v[202:209], v[104:107]
	v_mfma_f32_16x16x128_f8f6f4 v[96:99], v[0:7], v[202:209], v[96:99]
	s_barrier
	s_add_i32 s75, s55, s39
	s_mov_b32 m0, s75
	ds_read_b128 v[186:189], v183 offset:16384
	global_load_lds_dwordx4 v[222:223], off
	ds_read_b128 v[190:193], v183 offset:17408
	s_add_i32 m0, s75, 0x2000
	s_add_i32 s75, s64, s39
	global_load_lds_dwordx4 v[224:225], off
	ds_read_b128 v[194:197], v183 offset:18432
	s_mov_b32 m0, s75
	ds_read_b128 v[198:201], v183 offset:19456
	global_load_lds_dwordx4 v[226:227], off
	ds_read_b128 v[202:205], v183 offset:20480
	s_add_i32 m0, s75, 0x2000
	ds_read_b128 v[206:209], v183 offset:21504
	global_load_lds_dwordx4 v[228:229], off
	ds_read_b128 v[210:213], v183 offset:22528
	s_mov_b32 m0, s29
	ds_read_b128 v[214:217], v183 offset:23552
	global_load_lds_dwordx4 v[230:231], off
	s_mov_b32 m0, s42
	s_nop 0
	global_load_lds_dwordx4 v[232:233], off
	s_waitcnt vmcnt(8)
	s_waitcnt lgkmcnt(0)
	s_barrier
	s_waitcnt lgkmcnt(0)
	v_mfma_f32_16x16x128_f8f6f4 v[92:95], v[24:31], v[186:193], v[92:95]
	v_mfma_f32_16x16x128_f8f6f4 v[84:87], v[16:23], v[186:193], v[84:87]
	v_mfma_f32_16x16x128_f8f6f4 v[76:79], v[24:31], v[194:201], v[76:79]
	v_mfma_f32_16x16x128_f8f6f4 v[68:71], v[16:23], v[194:201], v[68:71]
	v_mfma_f32_16x16x128_f8f6f4 v[60:63], v[24:31], v[202:209], v[60:63]
	v_mfma_f32_16x16x128_f8f6f4 v[52:55], v[16:23], v[202:209], v[52:55]
	v_mfma_f32_16x16x128_f8f6f4 v[44:47], v[24:31], v[210:217], v[44:47]
	v_mfma_f32_16x16x128_f8f6f4 v[36:39], v[16:23], v[210:217], v[36:39]
	v_mfma_f32_16x16x128_f8f6f4 v[88:91], v[8:15], v[186:193], v[88:91]
	v_mfma_f32_16x16x128_f8f6f4 v[80:83], v[0:7], v[186:193], v[80:83]
	v_mfma_f32_16x16x128_f8f6f4 v[72:75], v[8:15], v[194:201], v[72:75]
	v_mfma_f32_16x16x128_f8f6f4 v[64:67], v[0:7], v[194:201], v[64:67]
	v_mfma_f32_16x16x128_f8f6f4 v[56:59], v[8:15], v[202:209], v[56:59]
	v_mfma_f32_16x16x128_f8f6f4 v[48:51], v[0:7], v[202:209], v[48:51]
	v_mfma_f32_16x16x128_f8f6f4 v[40:43], v[8:15], v[210:217], v[40:43]
	v_mfma_f32_16x16x128_f8f6f4 v[32:35], v[0:7], v[210:217], v[32:35]
	s_barrier
; #define PG8_LDA(dst, b, h) do { _Pragma("unroll") for (int m = 0; m < 4; ++m) _Pragma("unroll") for (int k = 0; k < 2; ++k) dst[m][k] = *(const PG8_LAS bf16x8*)(lds + PG8_SA(b, h) + aoff + m * 2048 + k * 1024); } while (0)
; #define PG8_LDB(dst, b, h) do { _Pragma("unroll") for (int n = 0; n < 2; ++n) _Pragma("unroll") for (int k = 0; k < 2; ++k) dst[n][k] = *(const PG8_LAS bf16x8*)(lds + PG8_SB(b, h) + boff + n * 2048 + k * 1024); } while (0)
; #define PG8_WAIT_V(n) asm volatile("s_waitcnt vmcnt(" #n ")" ::: "memory")
; #define PG8_WAIT_L(n) asm volatile("s_waitcnt lgkmcnt(" #n ")" ::: "memory")
; #define PG8_BAR __builtin_amdgcn_s_barrier()
; #define PG8_SCHED __builtin_amdgcn_sched_barrier(0)
; template <class Epi, class Sched, bool ALIGN_EPI = false, bool SP2 = false, bool F8 = false, bool I8 = false, bool PF = false>
; __device__ __forceinline__ void gemm_phase(PG8_LAS unsigned char* lds, const Gemm g, const Sched& S, const Epi& E, const int wave_) {
;     ...
;             PG8_WAIT_V(8); PG8_WAIT_L(0); PG8_BAR; PG8_MMA(1, 0, At, B0); PG8_MMA(1, 1, At, B1); PG8_BAR; PG8_SCHED;
;             PG8_LDB(B0, 1, 0); PG8_LDB(B1, 1, 1); PG8_SCHED; PG8_LDA(At, 1, 0); PG8_STAGE(PG8_SA(0, 1), a2 + hstep, voffA);
;             PG8_WAIT_V(8); PG8_WAIT_L(0); PG8_BAR; PG8_MMA(0, 0, At, B0); PG8_MMA(0, 1, At, B1); PG8_BAR; PG8_SCHED;
;             PG8_LDA(At, 1, 1); PG8_STAGE(PG8_SB(1, 0), b3, voffB); PG8_STAGE(PG8_SB(1, 1), b3 + hstep, voffB); PG8_STAGE(PG8_SA(1, 0), a3, voffA);
;             PG8_WAIT_V(8); PG8_WAIT_L(0); PG8_BAR; PG8_MMA(1, 0, At, B0); PG8_MMA(1, 1, At, B1); PG8_BAR; PG8_SCHED;
	s_add_i32 s75, 0, 0x18000
	s_add_i32 s76, 0, 0x1c000
	v_add_u32_e32 v12, s75, v180
	v_add_u32_e32 v28, s76, v180
	ds_read_b128 v[0:3], v12
	ds_read_b128 v[4:7], v12 offset:1024
	ds_read_b128 v[8:11], v12 offset:2048
	ds_read_b128 v[12:15], v12 offset:3072
	ds_read_b128 v[16:19], v28
	ds_read_b128 v[20:23], v28 offset:1024
	ds_read_b128 v[24:27], v28 offset:2048
	ds_read_b128 v[28:31], v28 offset:3072
	s_add_u32 s36, s36, 0x20000
	s_addc_u32 s37, s37, 0
	s_mov_b32 m0, s43
	v_lshl_add_u64 v[218:219], s[36:37], 0, v[162:163]
	ds_read_b128 v[186:189], v183 offset:32768
	ds_read_b128 v[190:193], v183 offset:33792
	ds_read_b128 v[194:197], v183 offset:34816
	ds_read_b128 v[198:201], v183 offset:35840
	ds_read_b128 v[202:205], v183 offset:36864
	ds_read_b128 v[206:209], v183 offset:37888
	ds_read_b128 v[210:213], v183 offset:38912
	ds_read_b128 v[214:217], v183 offset:39936
	global_load_lds_dwordx4 v[218:219], off
	v_lshl_add_u64 v[218:219], s[36:37], 0, v[164:165]
	s_mov_b32 m0, s44
	s_nop 0
	global_load_lds_dwordx4 v[218:219], off
	s_waitcnt vmcnt(8)
	s_waitcnt lgkmcnt(0)
	s_barrier
	s_waitcnt lgkmcnt(0)
	v_mfma_f32_16x16x128_f8f6f4 v[156:159], v[0:7], v[186:193], v[156:159]
	v_lshl_add_u64 v[222:223], v[222:223], 0, s[8:9]
	v_mfma_f32_16x16x128_f8f6f4 v[148:151], v[8:15], v[186:193], v[148:151]
	v_lshl_add_u64 v[224:225], v[224:225], 0, s[8:9]
	v_mfma_f32_16x16x128_f8f6f4 v[140:143], v[0:7], v[194:201], v[140:143]
	v_lshl_add_u64 v[226:227], v[226:227], 0, s[8:9]
	v_mfma_f32_16x16x128_f8f6f4 v[132:135], v[8:15], v[194:201], v[132:135]
	v_lshl_add_u64 v[228:229], v[228:229], 0, s[8:9]
	v_mfma_f32_16x16x128_f8f6f4 v[124:127], v[0:7], v[202:209], v[124:127]
	v_lshl_add_u64 v[230:231], v[230:231], 0, s[8:9]
	v_mfma_f32_16x16x128_f8f6f4 v[116:119], v[8:15], v[202:209], v[116:119]
	v_lshl_add_u64 v[232:233], v[232:233], 0, s[8:9]
	v_mfma_f32_16x16x128_f8f6f4 v[108:111], v[0:7], v[210:217], v[108:111]
	v_mfma_f32_16x16x128_f8f6f4 v[100:103], v[8:15], v[210:217], v[100:103]
	v_mfma_f32_16x16x128_f8f6f4 v[152:155], v[16:23], v[186:193], v[152:155]
	v_mfma_f32_16x16x128_f8f6f4 v[144:147], v[24:31], v[186:193], v[144:147]
	v_mfma_f32_16x16x128_f8f6f4 v[136:139], v[16:23], v[194:201], v[136:139]
	v_mfma_f32_16x16x128_f8f6f4 v[128:131], v[24:31], v[194:201], v[128:131]
	v_mfma_f32_16x16x128_f8f6f4 v[120:123], v[16:23], v[202:209], v[120:123]
	v_mfma_f32_16x16x128_f8f6f4 v[112:115], v[24:31], v[202:209], v[112:115]
	v_mfma_f32_16x16x128_f8f6f4 v[104:107], v[16:23], v[210:217], v[104:107]
	v_mfma_f32_16x16x128_f8f6f4 v[96:99], v[24:31], v[210:217], v[96:99]
	s_barrier
	s_add_i32 s36, s75, s39
	s_mov_b32 m0, s36
	ds_read_b128 v[186:189], v183 offset:49152
	global_load_lds_dwordx4 v[222:223], off
	ds_read_b128 v[190:193], v183 offset:50176
	s_add_i32 m0, s36, 0x2000
	s_add_u32 s34, s34, 0x20080
	s_addc_u32 s35, s35, 0
	s_add_i32 s36, s76, s39
	global_load_lds_dwordx4 v[224:225], off
	ds_read_b128 v[194:197], v183 offset:51200
	s_mov_b32 m0, s36
	ds_read_b128 v[198:201], v183 offset:52224
	global_load_lds_dwordx4 v[226:227], off
	ds_read_b128 v[202:205], v183 offset:53248
	s_add_i32 m0, s36, 0x2000
	ds_read_b128 v[206:209], v183 offset:54272
	global_load_lds_dwordx4 v[228:229], off
	ds_read_b128 v[210:213], v183 offset:55296
	s_mov_b32 m0, s48
	ds_read_b128 v[214:217], v183 offset:56320
	global_load_lds_dwordx4 v[230:231], off
	s_mov_b32 m0, s49
	s_nop 0
	global_load_lds_dwordx4 v[232:233], off
	s_waitcnt vmcnt(8)
	s_waitcnt lgkmcnt(0)
	s_barrier
	s_waitcnt lgkmcnt(0)
	v_mfma_f32_16x16x128_f8f6f4 v[92:95], v[0:7], v[186:193], v[92:95]
	v_mfma_f32_16x16x128_f8f6f4 v[84:87], v[8:15], v[186:193], v[84:87]
	v_mfma_f32_16x16x128_f8f6f4 v[76:79], v[0:7], v[194:201], v[76:79]
	v_mfma_f32_16x16x128_f8f6f4 v[68:71], v[8:15], v[194:201], v[68:71]
	v_mfma_f32_16x16x128_f8f6f4 v[60:63], v[0:7], v[202:209], v[60:63]
	v_mfma_f32_16x16x128_f8f6f4 v[52:55], v[8:15], v[202:209], v[52:55]
	v_mfma_f32_16x16x128_f8f6f4 v[44:47], v[0:7], v[210:217], v[44:47]
	v_mfma_f32_16x16x128_f8f6f4 v[36:39], v[8:15], v[210:217], v[36:39]
	v_mfma_f32_16x16x128_f8f6f4 v[88:91], v[16:23], v[186:193], v[88:91]
	v_mfma_f32_16x16x128_f8f6f4 v[80:83], v[24:31], v[186:193], v[80:83]
	v_mfma_f32_16x16x128_f8f6f4 v[72:75], v[16:23], v[194:201], v[72:75]
	v_mfma_f32_16x16x128_f8f6f4 v[64:67], v[24:31], v[194:201], v[64:67]
	v_mfma_f32_16x16x128_f8f6f4 v[56:59], v[16:23], v[202:209], v[56:59]
	v_mfma_f32_16x16x128_f8f6f4 v[48:51], v[24:31], v[202:209], v[48:51]
	v_mfma_f32_16x16x128_f8f6f4 v[40:43], v[16:23], v[210:217], v[40:43]
	v_mfma_f32_16x16x128_f8f6f4 v[32:35], v[24:31], v[210:217], v[32:35]
	s_barrier
	s_add_i32 s74, s74, 2
	s_add_u32 s30, s30, 0x100
	s_addc_u32 s31, s31, 0
	s_add_u32 s72, s72, 0x100
	s_addc_u32 s73, s73, 0
	s_cmp_gt_u32 s74, 5
	s_cbranch_scc0 .LBB0_1540
	s_and_b64 vcc, exec, s[10:11]
	s_cbranch_vccz .LBB0_1543
	s_barrier

; #define PG8_LDA(dst, b, h) do { _Pragma("unroll") for (int m = 0; m < 4; ++m) _Pragma("unroll") for (int k = 0; k < 2; ++k) dst[m][k] = *(const PG8_LAS bf16x8*)(lds + PG8_SA(b, h) + aoff + m * 2048 + k * 1024); } while (0)
; #define PG8_LDB(dst, b, h) do { _Pragma("unroll") for (int n = 0; n < 2; ++n) _Pragma("unroll") for (int k = 0; k < 2; ++k) dst[n][k] = *(const PG8_LAS bf16x8*)(lds + PG8_SB(b, h) + boff + n * 2048 + k * 1024); } while (0)
; #define PG8_WAIT_V(n) asm volatile("s_waitcnt vmcnt(" #n ")" ::: "memory")
; #define PG8_WAIT_L(n) asm volatile("s_waitcnt lgkmcnt(" #n ")" ::: "memory")
; #define PG8_BAR __builtin_amdgcn_s_barrier()
; #define PG8_SCHED __builtin_amdgcn_sched_barrier(0)
; template <class Epi, class Sched, bool ALIGN_EPI = false, bool SP2 = false, bool F8 = false, bool I8 = false, bool PF = false>
; __device__ __forceinline__ void gemm_phase(PG8_LAS unsigned char* lds, const Gemm g, const Sched& S, const Epi& E, const int wave_) {
;     ...
;             PG8_LDB(B0, 0, 0); PG8_LDB(B1, 0, 1); PG8_SCHED; PG8_LDA(At, 0, 0); PG8_STAGE(PG8_SA(1, 1), a1 + hstep, voffA);
;             PG8_WAIT_V(8); PG8_WAIT_L(0); PG8_BAR; PG8_MMA(0, 0, At, B0); PG8_MMA(0, 1, At, B1); PG8_BAR; PG8_SCHED;
;             PG8_LDA(At, 0, 1); PG8_STAGE(PG8_SB(0, 0), b2, voffB); PG8_STAGE(PG8_SB(0, 1), b2 + hstep, voffB); PG8_STAGE(PG8_SA(0, 0), a2, voffA);
;             PG8_WAIT_V(8); PG8_WAIT_L(0); PG8_BAR; PG8_MMA(1, 0, At, B0); PG8_MMA(1, 1, At, B1); PG8_BAR; PG8_SCHED;
.LBB0_1621:
	ds_read_b128 v[24:27], v181
	ds_read_b128 v[28:31], v181 offset:1024
	ds_read_b128 v[16:19], v181 offset:2048
	ds_read_b128 v[20:23], v181 offset:3072
	ds_read_b128 v[8:11], v182
	ds_read_b128 v[12:15], v182 offset:1024
	ds_read_b128 v[0:3], v182 offset:2048
	ds_read_b128 v[4:7], v182 offset:3072
	s_add_u32 s30, s34, 0x100
	s_addc_u32 s31, s35, 0
	s_cmp_eq_u32 s73, 24
	s_cselect_b32 s39, s25, s31
	s_cselect_b32 s38, s24, s30
	s_cselect_b32 s37, s27, s72
	s_cselect_b32 s36, s26, s71
	v_lshl_add_u64 v[208:209], s[34:35], 0, v[168:169]
	s_add_i32 m0, s29, 0xc000
	ds_read_b128 v[172:175], v183
	ds_read_b128 v[176:179], v183 offset:1024
	ds_read_b128 v[184:187], v183 offset:2048
	ds_read_b128 v[188:191], v183 offset:3072
	ds_read_b128 v[192:195], v183 offset:4096
	ds_read_b128 v[196:199], v183 offset:5120
	ds_read_b128 v[200:203], v183 offset:6144
	ds_read_b128 v[204:207], v183 offset:7168
	global_load_lds_dwordx4 v[208:209], off
	v_lshl_add_u64 v[208:209], s[34:35], 0, v[170:171]
	s_add_i32 m0, s29, 0xe000
	s_nop 0
	global_load_lds_dwordx4 v[208:209], off
	s_waitcnt vmcnt(8)
	s_waitcnt lgkmcnt(0)
	s_barrier
	s_waitcnt lgkmcnt(0)
	v_mfma_f32_16x16x128_f8f6f4 v[156:159], v[24:31], v[172:179], v[156:159]
	v_mfma_f32_16x16x128_f8f6f4 v[152:155], v[16:23], v[172:179], v[152:155]
	v_mfma_f32_16x16x128_f8f6f4 v[144:147], v[24:31], v[184:191], v[144:147]
	v_mfma_f32_16x16x128_f8f6f4 v[136:139], v[16:23], v[184:191], v[136:139]
	v_mfma_f32_16x16x128_f8f6f4 v[128:131], v[24:31], v[192:199], v[128:131]
	v_mfma_f32_16x16x128_f8f6f4 v[120:123], v[16:23], v[192:199], v[120:123]
	v_mfma_f32_16x16x128_f8f6f4 v[112:115], v[24:31], v[200:207], v[112:115]
	v_mfma_f32_16x16x128_f8f6f4 v[104:107], v[16:23], v[200:207], v[104:107]
	v_mfma_f32_16x16x128_f8f6f4 v[148:151], v[8:15], v[172:179], v[148:151]
	v_mfma_f32_16x16x128_f8f6f4 v[140:143], v[0:7], v[172:179], v[140:143]
	v_mfma_f32_16x16x128_f8f6f4 v[132:135], v[8:15], v[184:191], v[132:135]
	v_mfma_f32_16x16x128_f8f6f4 v[124:127], v[0:7], v[184:191], v[124:127]
	v_mfma_f32_16x16x128_f8f6f4 v[116:119], v[8:15], v[192:199], v[116:119]
	v_mfma_f32_16x16x128_f8f6f4 v[108:111], v[0:7], v[192:199], v[108:111]
	v_mfma_f32_16x16x128_f8f6f4 v[100:103], v[8:15], v[200:207], v[100:103]
	v_mfma_f32_16x16x128_f8f6f4 v[96:99], v[0:7], v[200:207], v[96:99]
	s_barrier
	s_add_i32 s34, s53, s42
	v_lshl_add_u64 v[172:173], s[36:37], 0, v[160:161]
	s_mov_b32 m0, s34
	ds_read_b128 v[184:187], v183 offset:16384
	global_load_lds_dwordx4 v[172:173], off
	ds_read_b128 v[188:191], v183 offset:17408
	s_add_i32 m0, s34, 0x2000
	s_add_u32 s34, s36, 0x70000
	v_lshl_add_u64 v[174:175], s[36:37], 0, v[166:167]
	s_addc_u32 s35, s37, 0
	s_add_i32 s74, s54, s42
	global_load_lds_dwordx4 v[174:175], off
	ds_read_b128 v[192:195], v183 offset:18432
	v_lshl_add_u64 v[176:177], s[34:35], 0, v[160:161]
	s_mov_b32 m0, s74
	v_lshl_add_u64 v[178:179], s[38:39], 0, v[164:165]
	global_load_lds_dwordx4 v[176:177], off
	ds_read_b128 v[196:199], v183 offset:19456
	v_lshl_add_u64 v[176:177], s[34:35], 0, v[166:167]
	s_add_i32 m0, s74, 0x2000
	ds_read_b128 v[200:203], v183 offset:20480
	global_load_lds_dwordx4 v[176:177], off
	ds_read_b128 v[204:207], v183 offset:21504
	v_lshl_add_u64 v[176:177], s[38:39], 0, v[162:163]
	s_mov_b32 m0, s29
	ds_read_b128 v[208:211], v183 offset:22528
	global_load_lds_dwordx4 v[176:177], off
	ds_read_b128 v[212:215], v183 offset:23552
	s_mov_b32 m0, s45
	s_nop 0
	global_load_lds_dwordx4 v[178:179], off
	s_waitcnt vmcnt(8)
	s_waitcnt lgkmcnt(0)
	s_barrier
	s_waitcnt lgkmcnt(0)
	v_mfma_f32_16x16x128_f8f6f4 v[92:95], v[24:31], v[184:191], v[92:95]
	v_mfma_f32_16x16x128_f8f6f4 v[88:91], v[16:23], v[184:191], v[88:91]
	v_mfma_f32_16x16x128_f8f6f4 v[80:83], v[24:31], v[192:199], v[80:83]
	v_mfma_f32_16x16x128_f8f6f4 v[72:75], v[16:23], v[192:199], v[72:75]
	v_mfma_f32_16x16x128_f8f6f4 v[64:67], v[24:31], v[200:207], v[64:67]
	v_mfma_f32_16x16x128_f8f6f4 v[56:59], v[16:23], v[200:207], v[56:59]
	v_mfma_f32_16x16x128_f8f6f4 v[48:51], v[24:31], v[208:215], v[48:51]
	v_mfma_f32_16x16x128_f8f6f4 v[40:43], v[16:23], v[208:215], v[40:43]
	v_mfma_f32_16x16x128_f8f6f4 v[84:87], v[8:15], v[184:191], v[84:87]
	v_mfma_f32_16x16x128_f8f6f4 v[76:79], v[0:7], v[184:191], v[76:79]
	v_mfma_f32_16x16x128_f8f6f4 v[68:71], v[8:15], v[192:199], v[68:71]
	v_mfma_f32_16x16x128_f8f6f4 v[60:63], v[0:7], v[192:199], v[60:63]
	v_mfma_f32_16x16x128_f8f6f4 v[52:55], v[8:15], v[200:207], v[52:55]
	v_mfma_f32_16x16x128_f8f6f4 v[44:47], v[0:7], v[200:207], v[44:47]
	v_mfma_f32_16x16x128_f8f6f4 v[36:39], v[8:15], v[208:215], v[36:39]
	v_mfma_f32_16x16x128_f8f6f4 v[32:35], v[0:7], v[208:215], v[32:35]
	s_barrier
; #define PG8_LDA(dst, b, h) do { _Pragma("unroll") for (int m = 0; m < 4; ++m) _Pragma("unroll") for (int k = 0; k < 2; ++k) dst[m][k] = *(const PG8_LAS bf16x8*)(lds + PG8_SA(b, h) + aoff + m * 2048 + k * 1024); } while (0)
; #define PG8_LDB(dst, b, h) do { _Pragma("unroll") for (int n = 0; n < 2; ++n) _Pragma("unroll") for (int k = 0; k < 2; ++k) dst[n][k] = *(const PG8_LAS bf16x8*)(lds + PG8_SB(b, h) + boff + n * 2048 + k * 1024); } while (0)
; #define PG8_WAIT_V(n) asm volatile("s_waitcnt vmcnt(" #n ")" ::: "memory")
; #define PG8_WAIT_L(n) asm volatile("s_waitcnt lgkmcnt(" #n ")" ::: "memory")
; #define PG8_BAR __builtin_amdgcn_s_barrier()
; #define PG8_SCHED __builtin_amdgcn_sched_barrier(0)
; template <class Epi, class Sched, bool ALIGN_EPI = false, bool SP2 = false, bool F8 = false, bool I8 = false, bool PF = false>
; __device__ __forceinline__ void gemm_phase(PG8_LAS unsigned char* lds, const Gemm g, const Sched& S, const Epi& E, const int wave_) {
;     ...
;             PG8_WAIT_V(8); PG8_WAIT_L(0); PG8_BAR; PG8_MMA(1, 0, At, B0); PG8_MMA(1, 1, At, B1); PG8_BAR; PG8_SCHED;
;             PG8_LDB(B0, 1, 0); PG8_LDB(B1, 1, 1); PG8_SCHED; PG8_LDA(At, 1, 0); PG8_STAGE(PG8_SA(0, 1), a2 + hstep, voffA);
;             PG8_WAIT_V(8); PG8_WAIT_L(0); PG8_BAR; PG8_MMA(0, 0, At, B0); PG8_MMA(0, 1, At, B1); PG8_BAR; PG8_SCHED;
;             PG8_LDA(At, 1, 1); PG8_STAGE(PG8_SB(1, 0), b3, voffB); PG8_STAGE(PG8_SB(1, 1), b3 + hstep, voffB); PG8_STAGE(PG8_SA(1, 0), a3, voffA);
;             PG8_WAIT_V(8); PG8_WAIT_L(0); PG8_BAR; PG8_MMA(1, 0, At, B0); PG8_MMA(1, 1, At, B1); PG8_BAR; PG8_SCHED;
	s_add_i32 s74, 0, 0x18000
	s_add_i32 s75, 0, 0x1c000
	v_add_u32_e32 v12, s74, v180
	v_add_u32_e32 v28, s75, v180
	ds_read_b128 v[0:3], v12
	ds_read_b128 v[4:7], v12 offset:1024
	ds_read_b128 v[8:11], v12 offset:2048
	ds_read_b128 v[12:15], v12 offset:3072
	ds_read_b128 v[16:19], v28
	ds_read_b128 v[20:23], v28 offset:1024
	ds_read_b128 v[24:27], v28 offset:2048
	ds_read_b128 v[28:31], v28 offset:3072
	s_add_u32 s34, s38, 0x70000
	s_addc_u32 s35, s39, 0
	s_mov_b32 m0, s46
	v_lshl_add_u64 v[216:217], s[34:35], 0, v[162:163]
	ds_read_b128 v[184:187], v183 offset:32768
	ds_read_b128 v[188:191], v183 offset:33792
	ds_read_b128 v[192:195], v183 offset:34816
	ds_read_b128 v[196:199], v183 offset:35840
	ds_read_b128 v[200:203], v183 offset:36864
	ds_read_b128 v[204:207], v183 offset:37888
	ds_read_b128 v[208:211], v183 offset:38912
	ds_read_b128 v[212:215], v183 offset:39936
	global_load_lds_dwordx4 v[216:217], off
	v_lshl_add_u64 v[216:217], s[34:35], 0, v[164:165]
	s_mov_b32 m0, s47
	s_nop 0
	global_load_lds_dwordx4 v[216:217], off
	s_waitcnt vmcnt(8)
	s_waitcnt lgkmcnt(0)
	s_barrier
	s_waitcnt lgkmcnt(0)
	v_mfma_f32_16x16x128_f8f6f4 v[156:159], v[0:7], v[184:191], v[156:159]
	v_mfma_f32_16x16x128_f8f6f4 v[152:155], v[8:15], v[184:191], v[152:155]
	v_mfma_f32_16x16x128_f8f6f4 v[144:147], v[0:7], v[192:199], v[144:147]
	v_mfma_f32_16x16x128_f8f6f4 v[136:139], v[8:15], v[192:199], v[136:139]
	v_mfma_f32_16x16x128_f8f6f4 v[128:131], v[0:7], v[200:207], v[128:131]
	v_mfma_f32_16x16x128_f8f6f4 v[120:123], v[8:15], v[200:207], v[120:123]
	v_mfma_f32_16x16x128_f8f6f4 v[112:115], v[0:7], v[208:215], v[112:115]
	v_mfma_f32_16x16x128_f8f6f4 v[104:107], v[8:15], v[208:215], v[104:107]
	v_mfma_f32_16x16x128_f8f6f4 v[148:151], v[16:23], v[184:191], v[148:151]
	v_mfma_f32_16x16x128_f8f6f4 v[140:143], v[24:31], v[184:191], v[140:143]
	v_mfma_f32_16x16x128_f8f6f4 v[132:135], v[16:23], v[192:199], v[132:135]
	v_mfma_f32_16x16x128_f8f6f4 v[124:127], v[24:31], v[192:199], v[124:127]
	v_mfma_f32_16x16x128_f8f6f4 v[116:119], v[16:23], v[200:207], v[116:119]
	v_mfma_f32_16x16x128_f8f6f4 v[108:111], v[24:31], v[200:207], v[108:111]
	v_mfma_f32_16x16x128_f8f6f4 v[100:103], v[16:23], v[208:215], v[100:103]
	v_mfma_f32_16x16x128_f8f6f4 v[96:99], v[24:31], v[208:215], v[96:99]
	s_barrier
	s_add_i32 s34, s74, s42
	v_lshl_add_u64 v[172:173], v[172:173], 0, s[8:9]
	s_mov_b32 m0, s34
	ds_read_b128 v[184:187], v183 offset:49152
	global_load_lds_dwordx4 v[172:173], off
	ds_read_b128 v[188:191], v183 offset:50176
	s_add_i32 m0, s34, 0x2000
	s_add_u32 s34, s36, 0x70080
	v_lshl_add_u64 v[172:173], v[174:175], 0, s[8:9]
	s_addc_u32 s35, s37, 0
	s_add_i32 s36, s75, s42
	global_load_lds_dwordx4 v[172:173], off
	ds_read_b128 v[192:195], v183 offset:51200
	v_lshl_add_u64 v[172:173], s[34:35], 0, v[160:161]
	s_mov_b32 m0, s36
	ds_read_b128 v[196:199], v183 offset:52224
	global_load_lds_dwordx4 v[172:173], off
	ds_read_b128 v[200:203], v183 offset:53248
	v_lshl_add_u64 v[172:173], s[34:35], 0, v[166:167]
	s_add_i32 m0, s36, 0x2000
	ds_read_b128 v[204:207], v183 offset:54272
	global_load_lds_dwordx4 v[172:173], off
	ds_read_b128 v[208:211], v183 offset:55296
	v_lshl_add_u64 v[172:173], v[176:177], 0, s[8:9]
	s_mov_b32 m0, s51
	ds_read_b128 v[212:215], v183 offset:56320
	global_load_lds_dwordx4 v[172:173], off
	v_lshl_add_u64 v[172:173], v[178:179], 0, s[8:9]
	s_mov_b32 m0, s52
	s_nop 0
	global_load_lds_dwordx4 v[172:173], off
	s_waitcnt vmcnt(8)
	s_waitcnt lgkmcnt(0)
	s_barrier
	s_waitcnt lgkmcnt(0)
	v_mfma_f32_16x16x128_f8f6f4 v[92:95], v[0:7], v[184:191], v[92:95]
	v_mfma_f32_16x16x128_f8f6f4 v[88:91], v[8:15], v[184:191], v[88:91]
	v_mfma_f32_16x16x128_f8f6f4 v[80:83], v[0:7], v[192:199], v[80:83]
	v_mfma_f32_16x16x128_f8f6f4 v[72:75], v[8:15], v[192:199], v[72:75]
	v_mfma_f32_16x16x128_f8f6f4 v[64:67], v[0:7], v[200:207], v[64:67]
	v_mfma_f32_16x16x128_f8f6f4 v[56:59], v[8:15], v[200:207], v[56:59]
	v_mfma_f32_16x16x128_f8f6f4 v[48:51], v[0:7], v[208:215], v[48:51]
	v_mfma_f32_16x16x128_f8f6f4 v[40:43], v[8:15], v[208:215], v[40:43]
	v_mfma_f32_16x16x128_f8f6f4 v[84:87], v[16:23], v[184:191], v[84:87]
	v_mfma_f32_16x16x128_f8f6f4 v[76:79], v[24:31], v[184:191], v[76:79]
	v_mfma_f32_16x16x128_f8f6f4 v[68:71], v[16:23], v[192:199], v[68:71]
	v_mfma_f32_16x16x128_f8f6f4 v[60:63], v[24:31], v[192:199], v[60:63]
	v_mfma_f32_16x16x128_f8f6f4 v[52:55], v[16:23], v[200:207], v[52:55]
	v_mfma_f32_16x16x128_f8f6f4 v[44:47], v[24:31], v[200:207], v[44:47]
	v_mfma_f32_16x16x128_f8f6f4 v[36:39], v[16:23], v[208:215], v[36:39]
	v_mfma_f32_16x16x128_f8f6f4 v[32:35], v[24:31], v[208:215], v[32:35]
	s_barrier
	s_add_i32 s73, s73, 2
	s_add_u32 s71, s71, 0x100
	s_addc_u32 s72, s72, 0
	s_cmp_gt_u32 s73, 25
	s_mov_b64 s[34:35], s[30:31]
	s_cbranch_scc0 .LBB0_1621
	s_and_b64 vcc, exec, s[10:11]
	s_cbranch_vccz .LBB0_1624
	s_barrier

; #define PG8_LDA(dst, b, h) do { _Pragma("unroll") for (int m = 0; m < 4; ++m) _Pragma("unroll") for (int k = 0; k < 2; ++k) dst[m][k] = *(const PG8_LAS bf16x8*)(lds + PG8_SA(b, h) + aoff + m * 2048 + k * 1024); } while (0)
; #define PG8_LDB(dst, b, h) do { _Pragma("unroll") for (int n = 0; n < 2; ++n) _Pragma("unroll") for (int k = 0; k < 2; ++k) dst[n][k] = *(const PG8_LAS bf16x8*)(lds + PG8_SB(b, h) + boff + n * 2048 + k * 1024); } while (0)
; #define PG8_WAIT_V(n) asm volatile("s_waitcnt vmcnt(" #n ")" ::: "memory")
; #define PG8_WAIT_L(n) asm volatile("s_waitcnt lgkmcnt(" #n ")" ::: "memory")
; #define PG8_BAR __builtin_amdgcn_s_barrier()
; #define PG8_SCHED __builtin_amdgcn_sched_barrier(0)
; template <class Epi, class Sched, bool ALIGN_EPI = false, bool SP2 = false, bool F8 = false, bool I8 = false, bool PF = false>
; __device__ __forceinline__ void gemm_phase(PG8_LAS unsigned char* lds, const Gemm g, const Sched& S, const Epi& E, const int wave_) {
;     ...
;             PG8_LDB(B0, 0, 0); PG8_LDB(B1, 0, 1); PG8_SCHED; PG8_LDA(At, 0, 0); PG8_STAGE(PG8_SA(1, 1), a1 + hstep, voffA);
;             PG8_WAIT_V(8); PG8_WAIT_L(0); PG8_BAR; PG8_MMA(0, 0, At, B0); PG8_MMA(0, 1, At, B1); PG8_BAR; PG8_SCHED;
;             PG8_LDA(At, 0, 1); PG8_STAGE(PG8_SB(0, 0), b2, voffB); PG8_STAGE(PG8_SB(0, 1), b2 + hstep, voffB); PG8_STAGE(PG8_SA(0, 0), a2, voffA);
;             PG8_WAIT_V(8); PG8_WAIT_L(0); PG8_BAR; PG8_MMA(1, 0, At, B0); PG8_MMA(1, 1, At, B1); PG8_BAR; PG8_SCHED;
.LBB0_1718:
	ds_read_b128 v[24:27], v181
	ds_read_b128 v[28:31], v181 offset:1024
	ds_read_b128 v[16:19], v181 offset:2048
	ds_read_b128 v[20:23], v181 offset:3072
	ds_read_b128 v[8:11], v182
	ds_read_b128 v[12:15], v182 offset:1024
	ds_read_b128 v[0:3], v182 offset:2048
	ds_read_b128 v[4:7], v182 offset:3072
	s_add_u32 s30, s34, 0x100
	s_addc_u32 s31, s35, 0
	s_cmp_eq_u32 s73, 24
	s_cselect_b32 s39, s25, s31
	s_cselect_b32 s38, s24, s30
	s_cselect_b32 s37, s27, s72
	s_cselect_b32 s36, s26, s71
	v_lshl_add_u64 v[208:209], s[34:35], 0, v[168:169]
	s_add_i32 m0, s29, 0xc000
	ds_read_b128 v[172:175], v183
	ds_read_b128 v[176:179], v183 offset:1024
	ds_read_b128 v[184:187], v183 offset:2048
	ds_read_b128 v[188:191], v183 offset:3072
	ds_read_b128 v[192:195], v183 offset:4096
	ds_read_b128 v[196:199], v183 offset:5120
	ds_read_b128 v[200:203], v183 offset:6144
	ds_read_b128 v[204:207], v183 offset:7168
	global_load_lds_dwordx4 v[208:209], off
	v_lshl_add_u64 v[208:209], s[34:35], 0, v[170:171]
	s_add_i32 m0, s29, 0xe000
	s_nop 0
	global_load_lds_dwordx4 v[208:209], off
	s_waitcnt vmcnt(8)
	s_waitcnt lgkmcnt(0)
	s_barrier
	s_waitcnt lgkmcnt(0)
	v_mfma_f32_16x16x128_f8f6f4 v[156:159], v[24:31], v[172:179], v[156:159]
	v_mfma_f32_16x16x128_f8f6f4 v[152:155], v[16:23], v[172:179], v[152:155]
	v_mfma_f32_16x16x128_f8f6f4 v[144:147], v[24:31], v[184:191], v[144:147]
	v_mfma_f32_16x16x128_f8f6f4 v[136:139], v[16:23], v[184:191], v[136:139]
	v_mfma_f32_16x16x128_f8f6f4 v[128:131], v[24:31], v[192:199], v[128:131]
	v_mfma_f32_16x16x128_f8f6f4 v[120:123], v[16:23], v[192:199], v[120:123]
	v_mfma_f32_16x16x128_f8f6f4 v[112:115], v[24:31], v[200:207], v[112:115]
	v_mfma_f32_16x16x128_f8f6f4 v[104:107], v[16:23], v[200:207], v[104:107]
	v_mfma_f32_16x16x128_f8f6f4 v[148:151], v[8:15], v[172:179], v[148:151]
	v_mfma_f32_16x16x128_f8f6f4 v[140:143], v[0:7], v[172:179], v[140:143]
	v_mfma_f32_16x16x128_f8f6f4 v[132:135], v[8:15], v[184:191], v[132:135]
	v_mfma_f32_16x16x128_f8f6f4 v[124:127], v[0:7], v[184:191], v[124:127]
	v_mfma_f32_16x16x128_f8f6f4 v[116:119], v[8:15], v[192:199], v[116:119]
	v_mfma_f32_16x16x128_f8f6f4 v[108:111], v[0:7], v[192:199], v[108:111]
	v_mfma_f32_16x16x128_f8f6f4 v[100:103], v[8:15], v[200:207], v[100:103]
	v_mfma_f32_16x16x128_f8f6f4 v[96:99], v[0:7], v[200:207], v[96:99]
	s_barrier
	s_add_i32 s34, s53, s43
	v_lshl_add_u64 v[172:173], s[36:37], 0, v[160:161]
	s_mov_b32 m0, s34
	ds_read_b128 v[184:187], v183 offset:16384
	global_load_lds_dwordx4 v[172:173], off
	ds_read_b128 v[188:191], v183 offset:17408
	s_add_i32 m0, s34, 0x2000
	s_add_u32 s34, s36, 0x70000
	v_lshl_add_u64 v[174:175], s[36:37], 0, v[162:163]
	s_addc_u32 s35, s37, 0
	s_add_i32 s74, s54, s43
	global_load_lds_dwordx4 v[174:175], off
	ds_read_b128 v[192:195], v183 offset:18432
	v_lshl_add_u64 v[176:177], s[34:35], 0, v[160:161]
	s_mov_b32 m0, s74
	v_lshl_add_u64 v[178:179], s[38:39], 0, v[164:165]
	global_load_lds_dwordx4 v[176:177], off
	ds_read_b128 v[196:199], v183 offset:19456
	v_lshl_add_u64 v[176:177], s[34:35], 0, v[162:163]
	s_add_i32 m0, s74, 0x2000
	ds_read_b128 v[200:203], v183 offset:20480
	global_load_lds_dwordx4 v[176:177], off
	ds_read_b128 v[204:207], v183 offset:21504
	v_lshl_add_u64 v[176:177], s[38:39], 0, v[166:167]
	s_mov_b32 m0, s29
	ds_read_b128 v[208:211], v183 offset:22528
	global_load_lds_dwordx4 v[176:177], off
	ds_read_b128 v[212:215], v183 offset:23552
	s_mov_b32 m0, s45
	s_nop 0
	global_load_lds_dwordx4 v[178:179], off
	s_waitcnt vmcnt(8)
	s_waitcnt lgkmcnt(0)
	s_barrier
	s_waitcnt lgkmcnt(0)
	v_mfma_f32_16x16x128_f8f6f4 v[92:95], v[24:31], v[184:191], v[92:95]
	v_mfma_f32_16x16x128_f8f6f4 v[88:91], v[16:23], v[184:191], v[88:91]
	v_mfma_f32_16x16x128_f8f6f4 v[80:83], v[24:31], v[192:199], v[80:83]
	v_mfma_f32_16x16x128_f8f6f4 v[72:75], v[16:23], v[192:199], v[72:75]
	v_mfma_f32_16x16x128_f8f6f4 v[64:67], v[24:31], v[200:207], v[64:67]
	v_mfma_f32_16x16x128_f8f6f4 v[56:59], v[16:23], v[200:207], v[56:59]
	v_mfma_f32_16x16x128_f8f6f4 v[48:51], v[24:31], v[208:215], v[48:51]
	v_mfma_f32_16x16x128_f8f6f4 v[40:43], v[16:23], v[208:215], v[40:43]
	v_mfma_f32_16x16x128_f8f6f4 v[84:87], v[8:15], v[184:191], v[84:87]
	v_mfma_f32_16x16x128_f8f6f4 v[76:79], v[0:7], v[184:191], v[76:79]
	v_mfma_f32_16x16x128_f8f6f4 v[68:71], v[8:15], v[192:199], v[68:71]
	v_mfma_f32_16x16x128_f8f6f4 v[60:63], v[0:7], v[192:199], v[60:63]
	v_mfma_f32_16x16x128_f8f6f4 v[52:55], v[8:15], v[200:207], v[52:55]
	v_mfma_f32_16x16x128_f8f6f4 v[44:47], v[0:7], v[200:207], v[44:47]
	v_mfma_f32_16x16x128_f8f6f4 v[36:39], v[8:15], v[208:215], v[36:39]
	v_mfma_f32_16x16x128_f8f6f4 v[32:35], v[0:7], v[208:215], v[32:35]
	s_barrier
; #define PG8_LDA(dst, b, h) do { _Pragma("unroll") for (int m = 0; m < 4; ++m) _Pragma("unroll") for (int k = 0; k < 2; ++k) dst[m][k] = *(const PG8_LAS bf16x8*)(lds + PG8_SA(b, h) + aoff + m * 2048 + k * 1024); } while (0)
; #define PG8_LDB(dst, b, h) do { _Pragma("unroll") for (int n = 0; n < 2; ++n) _Pragma("unroll") for (int k = 0; k < 2; ++k) dst[n][k] = *(const PG8_LAS bf16x8*)(lds + PG8_SB(b, h) + boff + n * 2048 + k * 1024); } while (0)
; #define PG8_WAIT_V(n) asm volatile("s_waitcnt vmcnt(" #n ")" ::: "memory")
; #define PG8_WAIT_L(n) asm volatile("s_waitcnt lgkmcnt(" #n ")" ::: "memory")
; #define PG8_BAR __builtin_amdgcn_s_barrier()
; #define PG8_SCHED __builtin_amdgcn_sched_barrier(0)
; template <class Epi, class Sched, bool ALIGN_EPI = false, bool SP2 = false, bool F8 = false, bool I8 = false, bool PF = false>
; __device__ __forceinline__ void gemm_phase(PG8_LAS unsigned char* lds, const Gemm g, const Sched& S, const Epi& E, const int wave_) {
;     ...
;             PG8_WAIT_V(8); PG8_WAIT_L(0); PG8_BAR; PG8_MMA(1, 0, At, B0); PG8_MMA(1, 1, At, B1); PG8_BAR; PG8_SCHED;
;             PG8_LDB(B0, 1, 0); PG8_LDB(B1, 1, 1); PG8_SCHED; PG8_LDA(At, 1, 0); PG8_STAGE(PG8_SA(0, 1), a2 + hstep, voffA);
;             PG8_WAIT_V(8); PG8_WAIT_L(0); PG8_BAR; PG8_MMA(0, 0, At, B0); PG8_MMA(0, 1, At, B1); PG8_BAR; PG8_SCHED;
;             PG8_LDA(At, 1, 1); PG8_STAGE(PG8_SB(1, 0), b3, voffB); PG8_STAGE(PG8_SB(1, 1), b3 + hstep, voffB); PG8_STAGE(PG8_SA(1, 0), a3, voffA);
;             PG8_WAIT_V(8); PG8_WAIT_L(0); PG8_BAR; PG8_MMA(1, 0, At, B0); PG8_MMA(1, 1, At, B1); PG8_BAR; PG8_SCHED;
	s_add_i32 s74, 0, 0x18000
	s_add_i32 s75, 0, 0x1c000
	v_add_u32_e32 v12, s74, v180
	v_add_u32_e32 v28, s75, v180
	ds_read_b128 v[0:3], v12
	ds_read_b128 v[4:7], v12 offset:1024
	ds_read_b128 v[8:11], v12 offset:2048
	ds_read_b128 v[12:15], v12 offset:3072
	ds_read_b128 v[16:19], v28
	ds_read_b128 v[20:23], v28 offset:1024
	ds_read_b128 v[24:27], v28 offset:2048
	ds_read_b128 v[28:31], v28 offset:3072
	s_add_u32 s34, s38, 0x70000
	s_addc_u32 s35, s39, 0
	s_mov_b32 m0, s46
	v_lshl_add_u64 v[216:217], s[34:35], 0, v[166:167]
	ds_read_b128 v[184:187], v183 offset:32768
	ds_read_b128 v[188:191], v183 offset:33792
	ds_read_b128 v[192:195], v183 offset:34816
	ds_read_b128 v[196:199], v183 offset:35840
	ds_read_b128 v[200:203], v183 offset:36864
	ds_read_b128 v[204:207], v183 offset:37888
	ds_read_b128 v[208:211], v183 offset:38912
	ds_read_b128 v[212:215], v183 offset:39936
	global_load_lds_dwordx4 v[216:217], off
	v_lshl_add_u64 v[216:217], s[34:35], 0, v[164:165]
	s_mov_b32 m0, s47
	s_nop 0
	global_load_lds_dwordx4 v[216:217], off
	s_waitcnt vmcnt(8)
	s_waitcnt lgkmcnt(0)
	s_barrier
	s_waitcnt lgkmcnt(0)
	v_mfma_f32_16x16x128_f8f6f4 v[156:159], v[0:7], v[184:191], v[156:159]
	v_mfma_f32_16x16x128_f8f6f4 v[152:155], v[8:15], v[184:191], v[152:155]
	v_mfma_f32_16x16x128_f8f6f4 v[144:147], v[0:7], v[192:199], v[144:147]
	v_mfma_f32_16x16x128_f8f6f4 v[136:139], v[8:15], v[192:199], v[136:139]
	v_mfma_f32_16x16x128_f8f6f4 v[128:131], v[0:7], v[200:207], v[128:131]
	v_mfma_f32_16x16x128_f8f6f4 v[120:123], v[8:15], v[200:207], v[120:123]
	v_mfma_f32_16x16x128_f8f6f4 v[112:115], v[0:7], v[208:215], v[112:115]
	v_mfma_f32_16x16x128_f8f6f4 v[104:107], v[8:15], v[208:215], v[104:107]
	v_mfma_f32_16x16x128_f8f6f4 v[148:151], v[16:23], v[184:191], v[148:151]
	v_mfma_f32_16x16x128_f8f6f4 v[140:143], v[24:31], v[184:191], v[140:143]
	v_mfma_f32_16x16x128_f8f6f4 v[132:135], v[16:23], v[192:199], v[132:135]
	v_mfma_f32_16x16x128_f8f6f4 v[124:127], v[24:31], v[192:199], v[124:127]
	v_mfma_f32_16x16x128_f8f6f4 v[116:119], v[16:23], v[200:207], v[116:119]
	v_mfma_f32_16x16x128_f8f6f4 v[108:111], v[24:31], v[200:207], v[108:111]
	v_mfma_f32_16x16x128_f8f6f4 v[100:103], v[16:23], v[208:215], v[100:103]
	v_mfma_f32_16x16x128_f8f6f4 v[96:99], v[24:31], v[208:215], v[96:99]
	s_barrier
	s_add_i32 s34, s74, s43
	v_lshl_add_u64 v[172:173], v[172:173], 0, s[8:9]
	s_mov_b32 m0, s34
	ds_read_b128 v[184:187], v183 offset:49152
	global_load_lds_dwordx4 v[172:173], off
	ds_read_b128 v[188:191], v183 offset:50176
	s_add_i32 m0, s34, 0x2000
	s_add_u32 s34, s36, 0x70080
	v_lshl_add_u64 v[172:173], v[174:175], 0, s[8:9]
	s_addc_u32 s35, s37, 0
	s_add_i32 s36, s75, s43
	global_load_lds_dwordx4 v[172:173], off
	ds_read_b128 v[192:195], v183 offset:51200
	v_lshl_add_u64 v[172:173], s[34:35], 0, v[160:161]
	s_mov_b32 m0, s36
	ds_read_b128 v[196:199], v183 offset:52224
	global_load_lds_dwordx4 v[172:173], off
	ds_read_b128 v[200:203], v183 offset:53248
	v_lshl_add_u64 v[172:173], s[34:35], 0, v[162:163]
	s_add_i32 m0, s36, 0x2000
	ds_read_b128 v[204:207], v183 offset:54272
	global_load_lds_dwordx4 v[172:173], off
	ds_read_b128 v[208:211], v183 offset:55296
	v_lshl_add_u64 v[172:173], v[176:177], 0, s[8:9]
	s_mov_b32 m0, s51
	ds_read_b128 v[212:215], v183 offset:56320
	global_load_lds_dwordx4 v[172:173], off
	v_lshl_add_u64 v[172:173], v[178:179], 0, s[8:9]
	s_mov_b32 m0, s52
	s_nop 0
	global_load_lds_dwordx4 v[172:173], off
	s_waitcnt vmcnt(8)
	s_waitcnt lgkmcnt(0)
	s_barrier
	s_waitcnt lgkmcnt(0)
	v_mfma_f32_16x16x128_f8f6f4 v[92:95], v[0:7], v[184:191], v[92:95]
	v_mfma_f32_16x16x128_f8f6f4 v[88:91], v[8:15], v[184:191], v[88:91]
	v_mfma_f32_16x16x128_f8f6f4 v[80:83], v[0:7], v[192:199], v[80:83]
	v_mfma_f32_16x16x128_f8f6f4 v[72:75], v[8:15], v[192:199], v[72:75]
	v_mfma_f32_16x16x128_f8f6f4 v[64:67], v[0:7], v[200:207], v[64:67]
	v_mfma_f32_16x16x128_f8f6f4 v[56:59], v[8:15], v[200:207], v[56:59]
	v_mfma_f32_16x16x128_f8f6f4 v[48:51], v[0:7], v[208:215], v[48:51]
	v_mfma_f32_16x16x128_f8f6f4 v[40:43], v[8:15], v[208:215], v[40:43]
	v_mfma_f32_16x16x128_f8f6f4 v[84:87], v[16:23], v[184:191], v[84:87]
	v_mfma_f32_16x16x128_f8f6f4 v[76:79], v[24:31], v[184:191], v[76:79]
	v_mfma_f32_16x16x128_f8f6f4 v[68:71], v[16:23], v[192:199], v[68:71]
	v_mfma_f32_16x16x128_f8f6f4 v[60:63], v[24:31], v[192:199], v[60:63]
	v_mfma_f32_16x16x128_f8f6f4 v[52:55], v[16:23], v[200:207], v[52:55]
	v_mfma_f32_16x16x128_f8f6f4 v[44:47], v[24:31], v[200:207], v[44:47]
	v_mfma_f32_16x16x128_f8f6f4 v[36:39], v[16:23], v[208:215], v[36:39]
	v_mfma_f32_16x16x128_f8f6f4 v[32:35], v[24:31], v[208:215], v[32:35]
	s_barrier
	s_add_i32 s73, s73, 2
	s_add_u32 s71, s71, 0x100
	s_addc_u32 s72, s72, 0
	s_cmp_gt_u32 s73, 25
	s_mov_b64 s[34:35], s[30:31]
	s_cbranch_scc0 .LBB0_1718
	s_and_b64 vcc, exec, s[10:11]
	s_cbranch_vccz .LBB0_1721
	s_barrier
